# lever 9 (loop-edge edit): loop-carried scalar updates + exit compare of the 13 GEMM K loops moved in front of the loop-back barrier; only the branch stays behind it
# baseline (speedup 1.0000x reference)
; #define PG8_STAGE(bufoff, gbase, voff) do { _Pragma("unroll") for (int _i = 0; _i < 2; ++_i) \
;         __builtin_amdgcn_global_load_lds((const unsigned*)((const char*)(gbase) + (voff)[_i]), (PG8_LAS unsigned*)(lds + (bufoff) + ldsw + _i * 8192), 16, 0, 0); } while (0)
; #define PG8_STAGE_A(bufoff, gbase, h, nx) do { _Pragma("unroll") for (int _i = 0; _i < 2; ++_i) { \
;         const unsigned vo_ = GA ? ((nx) ? vgn[h][_i] : vgc[h][_i]) : voffA[_i]; \
;         __builtin_amdgcn_global_load_lds((const unsigned*)((const char*)(gbase) + vo_), (PG8_LAS unsigned*)(lds + (bufoff) + ldsw + _i * 8192), 16, 0, 0); } } while (0)
; #define PG8_LDA(dst, b, h) do { _Pragma("unroll") for (int m = 0; m < 4; ++m) _Pragma("unroll") for (int k = 0; k < 2; ++k) dst[m][k] = *(const PG8_LAS bf16x8*)(lds + PG8_SA(b, h) + aoff + m * 2048 + k * 1024); } while (0)
; #define PG8_LDB(dst, b, h) do { _Pragma("unroll") for (int n = 0; n < 2; ++n) _Pragma("unroll") for (int k = 0; k < 2; ++k) dst[n][k] = *(const PG8_LAS bf16x8*)(lds + PG8_SB(b, h) + boff + n * 2048 + k * 1024); } while (0)
; #define PG8_WAIT_V(n) asm volatile("s_waitcnt vmcnt(" #n ")" ::: "memory")
; #define PG8_WAIT_L(n) asm volatile("s_waitcnt lgkmcnt(" #n ")" ::: "memory")
; #define PG8_BAR __builtin_amdgcn_s_barrier()
; #define PG8_SCHED __builtin_amdgcn_sched_barrier(0)
; template <class Epi, class Sched>
; __device__ __forceinline__ void gemm_phase(const int WID_, PG8_LAS unsigned char* lds, const Sched& S, const Epi& E) {
;     ...
;         for (int t = 0; t < nt; t += 2) {
;             const bool last = (t == nt - 2);
;             const char* a1 = cA + (size_t)(t + 1) * kstep;
;             const char* a2 = last ? nA : cA + (size_t)(t + 2) * kstep; const char* b2 = last ? nB : cB + (size_t)(t + 2) * kstep;
;             const char* a3 = a2 + kstep; const char* b3 = b2 + kstep;
;             PG8_LDB(B0, 0, 0); PG8_LDB(B1, 0, 1); PG8_SCHED; PG8_LDA(At, 0, 0); PG8_STAGE_A(PG8_SA(1, 1), a1 + hstepA, 1, false);
;             PG8_WAIT_V(8); PG8_WAIT_L(0); PG8_BAR; PG8_MMA(0, 0, At, B0); PG8_MMA(0, 1, At, B1); PG8_BAR; PG8_SCHED;
;             PG8_LDA(At, 0, 1); PG8_STAGE(PG8_SB(0, 0), b2, voffB); PG8_STAGE(PG8_SB(0, 1), b2 + hstepB, voffB); PG8_STAGE_A(PG8_SA(0, 0), a2, 0, last);
;             PG8_WAIT_V(8); PG8_WAIT_L(0); PG8_BAR; PG8_MMA(1, 0, At, B0); PG8_MMA(1, 1, At, B1); PG8_BAR; PG8_SCHED;
.LBB0_114:
	ds_read_b128 v[148:151], v156
	ds_read_b128 v[160:163], v156 offset:1024
	ds_read_b128 v[164:167], v156 offset:2048
	ds_read_b128 v[168:171], v156 offset:3072
	ds_read_b128 v[172:175], v157
	ds_read_b128 v[176:179], v157 offset:1024
	ds_read_b128 v[180:183], v157 offset:2048
	ds_read_b128 v[184:187], v157 offset:3072
	s_add_u32 s22, s20, 0xfffc0080
	s_addc_u32 s23, s21, -1
	s_cmp_eq_u32 s48, 12
	s_cselect_b32 s29, s3, s23
	s_cselect_b32 s28, s13, s22
	s_cselect_b32 s23, s11, s47
	s_cselect_b32 s22, s19, s46
	v_lshl_add_u64 v[152:153], s[20:21], 0, v[140:141]
	s_add_i32 m0, s31, 0xc000
	ds_read_b128 v[188:191], v158
	ds_read_b128 v[192:195], v158 offset:1024
	ds_read_b128 v[196:199], v158 offset:2048
	ds_read_b128 v[200:203], v158 offset:3072
	ds_read_b128 v[204:207], v158 offset:4096
	ds_read_b128 v[208:211], v158 offset:5120
	ds_read_b128 v[212:215], v158 offset:6144
	ds_read_b128 v[216:219], v158 offset:7168
	global_load_lds_dwordx4 v[152:153], off
	v_lshl_add_u64 v[152:153], s[20:21], 0, v[142:143]
	s_add_i32 m0, s31, 0xe000
	s_nop 0
	global_load_lds_dwordx4 v[152:153], off
	s_waitcnt vmcnt(8)
	s_waitcnt lgkmcnt(0)
	s_barrier
	s_setprio 1
	s_waitcnt lgkmcnt(0)
	v_mfma_f32_16x16x32_bf16 v[124:127], v[148:151], v[188:191], v[124:127]
	v_mfma_f32_16x16x32_bf16 v[120:123], v[164:167], v[188:191], v[120:123]
	v_mfma_f32_16x16x32_bf16 v[108:111], v[148:151], v[196:199], v[108:111]
	v_mfma_f32_16x16x32_bf16 v[104:107], v[164:167], v[196:199], v[104:107]
	v_mfma_f32_16x16x32_bf16 v[92:95], v[148:151], v[204:207], v[92:95]
	v_mfma_f32_16x16x32_bf16 v[88:91], v[164:167], v[204:207], v[88:91]
	v_mfma_f32_16x16x32_bf16 v[76:79], v[148:151], v[212:215], v[76:79]
	v_mfma_f32_16x16x32_bf16 v[72:75], v[164:167], v[212:215], v[72:75]
	v_mfma_f32_16x16x32_bf16 v[124:127], v[160:163], v[192:195], v[124:127]
	v_mfma_f32_16x16x32_bf16 v[120:123], v[168:171], v[192:195], v[120:123]
	v_mfma_f32_16x16x32_bf16 v[108:111], v[160:163], v[200:203], v[108:111]
	v_mfma_f32_16x16x32_bf16 v[104:107], v[168:171], v[200:203], v[104:107]
	v_mfma_f32_16x16x32_bf16 v[92:95], v[160:163], v[208:211], v[92:95]
	v_mfma_f32_16x16x32_bf16 v[88:91], v[168:171], v[208:211], v[88:91]
	v_mfma_f32_16x16x32_bf16 v[76:79], v[160:163], v[216:219], v[76:79]
	v_mfma_f32_16x16x32_bf16 v[72:75], v[168:171], v[216:219], v[72:75]
	s_setprio 0
	s_setprio 1
	v_mfma_f32_16x16x32_bf16 v[116:119], v[172:175], v[188:191], v[116:119]
	v_mfma_f32_16x16x32_bf16 v[112:115], v[180:183], v[188:191], v[112:115]
	v_mfma_f32_16x16x32_bf16 v[100:103], v[172:175], v[196:199], v[100:103]
	v_mfma_f32_16x16x32_bf16 v[96:99], v[180:183], v[196:199], v[96:99]
	v_mfma_f32_16x16x32_bf16 v[84:87], v[172:175], v[204:207], v[84:87]
	v_mfma_f32_16x16x32_bf16 v[80:83], v[180:183], v[204:207], v[80:83]
	v_mfma_f32_16x16x32_bf16 v[68:71], v[172:175], v[212:215], v[68:71]
	v_mfma_f32_16x16x32_bf16 v[64:67], v[180:183], v[212:215], v[64:67]
	v_mfma_f32_16x16x32_bf16 v[116:119], v[176:179], v[192:195], v[116:119]
	v_mfma_f32_16x16x32_bf16 v[112:115], v[184:187], v[192:195], v[112:115]
	v_mfma_f32_16x16x32_bf16 v[100:103], v[176:179], v[200:203], v[100:103]
	v_mfma_f32_16x16x32_bf16 v[96:99], v[184:187], v[200:203], v[96:99]
	v_mfma_f32_16x16x32_bf16 v[84:87], v[176:179], v[208:211], v[84:87]
	v_mfma_f32_16x16x32_bf16 v[80:83], v[184:187], v[208:211], v[80:83]
	v_mfma_f32_16x16x32_bf16 v[68:71], v[176:179], v[216:219], v[68:71]
	v_mfma_f32_16x16x32_bf16 v[64:67], v[184:187], v[216:219], v[64:67]
	s_setprio 0
	s_barrier
	s_add_i32 s49, s42, s30
	v_lshl_add_u64 v[152:153], s[22:23], 0, v[130:131]
	s_mov_b32 m0, s49
	ds_read_b128 v[188:191], v158 offset:16384
	ds_read_b128 v[192:195], v158 offset:17408
	ds_read_b128 v[196:199], v158 offset:18432
	ds_read_b128 v[200:203], v158 offset:19456
	ds_read_b128 v[204:207], v158 offset:20480
	ds_read_b128 v[208:211], v158 offset:21504
	ds_read_b128 v[212:215], v158 offset:22528
	ds_read_b128 v[216:219], v158 offset:23552
	global_load_lds_dwordx4 v[152:153], off
	s_add_i32 m0, s49, 0x2000
	s_add_u32 s50, s22, 0x40000
	v_lshl_add_u64 v[220:221], s[22:23], 0, v[134:135]
	s_addc_u32 s51, s23, 0
	s_add_i32 s49, s43, s30
	global_load_lds_dwordx4 v[220:221], off
	v_lshl_add_u64 v[222:223], s[50:51], 0, v[130:131]
	s_mov_b32 m0, s49
	v_lshl_add_u64 v[224:225], s[28:29], 0, v[132:133]
	global_load_lds_dwordx4 v[222:223], off
	v_lshl_add_u64 v[222:223], s[50:51], 0, v[134:135]
	s_add_i32 m0, s49, 0x2000
	s_nop 0
	global_load_lds_dwordx4 v[222:223], off
	v_lshl_add_u64 v[222:223], s[28:29], 0, v[128:129]
	s_mov_b32 m0, s31
	s_nop 0
	global_load_lds_dwordx4 v[222:223], off
	s_mov_b32 m0, s33
	s_nop 0
	global_load_lds_dwordx4 v[224:225], off
	s_waitcnt vmcnt(8)
	s_waitcnt lgkmcnt(0)
	s_barrier
; #define PG8_STAGE(bufoff, gbase, voff) do { _Pragma("unroll") for (int _i = 0; _i < 2; ++_i) \
;         __builtin_amdgcn_global_load_lds((const unsigned*)((const char*)(gbase) + (voff)[_i]), (PG8_LAS unsigned*)(lds + (bufoff) + ldsw + _i * 8192), 16, 0, 0); } while (0)
; #define PG8_STAGE_A(bufoff, gbase, h, nx) do { _Pragma("unroll") for (int _i = 0; _i < 2; ++_i) { \
;         const unsigned vo_ = GA ? ((nx) ? vgn[h][_i] : vgc[h][_i]) : voffA[_i]; \
;         __builtin_amdgcn_global_load_lds((const unsigned*)((const char*)(gbase) + vo_), (PG8_LAS unsigned*)(lds + (bufoff) + ldsw + _i * 8192), 16, 0, 0); } } while (0)
; #define PG8_LDA(dst, b, h) do { _Pragma("unroll") for (int m = 0; m < 4; ++m) _Pragma("unroll") for (int k = 0; k < 2; ++k) dst[m][k] = *(const PG8_LAS bf16x8*)(lds + PG8_SA(b, h) + aoff + m * 2048 + k * 1024); } while (0)
; #define PG8_LDB(dst, b, h) do { _Pragma("unroll") for (int n = 0; n < 2; ++n) _Pragma("unroll") for (int k = 0; k < 2; ++k) dst[n][k] = *(const PG8_LAS bf16x8*)(lds + PG8_SB(b, h) + boff + n * 2048 + k * 1024); } while (0)
; #define PG8_MMA(ai, bj, At, Bt) do { __builtin_amdgcn_s_setprio(1); _Pragma("unroll") for (int m = 0; m < 4; ++m) _Pragma("unroll") for (int n = 0; n < 2; ++n) _Pragma("unroll") for (int k = 0; k < 2; ++k) \
;         acc[ai][bj][m][n] = __builtin_amdgcn_mfma_f32_16x16x32_bf16(Bt[n][k], At[m][k], acc[ai][bj][m][n], 0, 0, 0); __builtin_amdgcn_s_setprio(0); } while (0)
; #define PG8_WAIT_V(n) asm volatile("s_waitcnt vmcnt(" #n ")" ::: "memory")
; #define PG8_BAR __builtin_amdgcn_s_barrier()
; template <class Epi, class Sched>
; __device__ __forceinline__ void gemm_phase(const int WID_, PG8_LAS unsigned char* lds, const Sched& S, const Epi& E) {
;     ...
;             PG8_WAIT_V(8); PG8_WAIT_L(0); PG8_BAR; PG8_MMA(1, 0, At, B0); PG8_MMA(1, 1, At, B1); PG8_BAR; PG8_SCHED;
;             PG8_LDB(B0, 1, 0); PG8_LDB(B1, 1, 1); PG8_SCHED; PG8_LDA(At, 1, 0); PG8_STAGE_A(PG8_SA(0, 1), a2 + hstepA, 1, last);
;             PG8_WAIT_V(8); PG8_WAIT_L(0); PG8_BAR; PG8_MMA(0, 0, At, B0); PG8_MMA(0, 1, At, B1); PG8_BAR; PG8_SCHED;
;             PG8_LDA(At, 1, 1); PG8_STAGE(PG8_SB(1, 0), b3, voffB); PG8_STAGE(PG8_SB(1, 1), b3 + hstepB, voffB); PG8_STAGE_A(PG8_SA(1, 0), a3, 0, last);
;             PG8_WAIT_V(8); PG8_WAIT_L(0); PG8_BAR; PG8_MMA(1, 0, At, B0); PG8_MMA(1, 1, At, B1); PG8_BAR; PG8_SCHED;
	s_setprio 1
	s_waitcnt lgkmcnt(0)
	v_mfma_f32_16x16x32_bf16 v[60:63], v[148:151], v[188:191], v[60:63]
	v_mfma_f32_16x16x32_bf16 v[56:59], v[164:167], v[188:191], v[56:59]
	v_mfma_f32_16x16x32_bf16 v[44:47], v[148:151], v[196:199], v[44:47]
	v_mfma_f32_16x16x32_bf16 v[40:43], v[164:167], v[196:199], v[40:43]
	v_mfma_f32_16x16x32_bf16 v[28:31], v[148:151], v[204:207], v[28:31]
	v_mfma_f32_16x16x32_bf16 v[24:27], v[164:167], v[204:207], v[24:27]
	v_mfma_f32_16x16x32_bf16 v[12:15], v[148:151], v[212:215], v[12:15]
	v_mfma_f32_16x16x32_bf16 v[8:11], v[164:167], v[212:215], v[8:11]
	v_mfma_f32_16x16x32_bf16 v[60:63], v[160:163], v[192:195], v[60:63]
	v_mfma_f32_16x16x32_bf16 v[56:59], v[168:171], v[192:195], v[56:59]
	v_mfma_f32_16x16x32_bf16 v[44:47], v[160:163], v[200:203], v[44:47]
	v_mfma_f32_16x16x32_bf16 v[40:43], v[168:171], v[200:203], v[40:43]
	v_mfma_f32_16x16x32_bf16 v[28:31], v[160:163], v[208:211], v[28:31]
	v_mfma_f32_16x16x32_bf16 v[24:27], v[168:171], v[208:211], v[24:27]
	v_mfma_f32_16x16x32_bf16 v[12:15], v[160:163], v[216:219], v[12:15]
	v_mfma_f32_16x16x32_bf16 v[8:11], v[168:171], v[216:219], v[8:11]
	s_setprio 0
	s_setprio 1
	v_mfma_f32_16x16x32_bf16 v[52:55], v[172:175], v[188:191], v[52:55]
	v_mfma_f32_16x16x32_bf16 v[48:51], v[180:183], v[188:191], v[48:51]
	v_mfma_f32_16x16x32_bf16 v[36:39], v[172:175], v[196:199], v[36:39]
	v_mfma_f32_16x16x32_bf16 v[32:35], v[180:183], v[196:199], v[32:35]
	v_mfma_f32_16x16x32_bf16 v[20:23], v[172:175], v[204:207], v[20:23]
	v_mfma_f32_16x16x32_bf16 v[16:19], v[180:183], v[204:207], v[16:19]
	v_mfma_f32_16x16x32_bf16 v[4:7], v[172:175], v[212:215], v[4:7]
	v_mfma_f32_16x16x32_bf16 v[0:3], v[180:183], v[212:215], v[0:3]
	v_mfma_f32_16x16x32_bf16 v[52:55], v[176:179], v[192:195], v[52:55]
	v_mfma_f32_16x16x32_bf16 v[48:51], v[184:187], v[192:195], v[48:51]
	v_mfma_f32_16x16x32_bf16 v[36:39], v[176:179], v[200:203], v[36:39]
	v_mfma_f32_16x16x32_bf16 v[32:35], v[184:187], v[200:203], v[32:35]
	v_mfma_f32_16x16x32_bf16 v[20:23], v[176:179], v[208:211], v[20:23]
	v_mfma_f32_16x16x32_bf16 v[16:19], v[184:187], v[208:211], v[16:19]
	v_mfma_f32_16x16x32_bf16 v[4:7], v[176:179], v[216:219], v[4:7]
	v_mfma_f32_16x16x32_bf16 v[0:3], v[184:187], v[216:219], v[0:3]
	s_setprio 0
	s_barrier
	s_add_i32 s49, 0, 0x18000
	v_add_u32_e32 v136, s49, v154
	s_add_i32 s50, 0, 0x1c000
	ds_read_b128 v[148:151], v136
	ds_read_b128 v[160:163], v136 offset:1024
	ds_read_b128 v[164:167], v136 offset:2048
	ds_read_b128 v[168:171], v136 offset:3072
	v_add_u32_e32 v136, s50, v154
	ds_read_b128 v[172:175], v136
	ds_read_b128 v[176:179], v136 offset:1024
	ds_read_b128 v[180:183], v136 offset:2048
	ds_read_b128 v[184:187], v136 offset:3072
	s_add_u32 s28, s28, 0x40000
	s_addc_u32 s29, s29, 0
	s_mov_b32 m0, s34
	v_lshl_add_u64 v[226:227], s[28:29], 0, v[128:129]
	ds_read_b128 v[188:191], v158 offset:32768
	ds_read_b128 v[192:195], v158 offset:33792
	ds_read_b128 v[196:199], v158 offset:34816
	ds_read_b128 v[200:203], v158 offset:35840
	ds_read_b128 v[204:207], v158 offset:36864
	ds_read_b128 v[208:211], v158 offset:37888
	ds_read_b128 v[212:215], v158 offset:38912
	ds_read_b128 v[216:219], v158 offset:39936
	global_load_lds_dwordx4 v[226:227], off
	v_lshl_add_u64 v[226:227], s[28:29], 0, v[132:133]
	s_mov_b32 m0, s35
	s_nop 0
	global_load_lds_dwordx4 v[226:227], off
	s_waitcnt vmcnt(8)
	s_waitcnt lgkmcnt(0)
	s_barrier
	s_setprio 1
	s_waitcnt lgkmcnt(0)
	v_mfma_f32_16x16x32_bf16 v[124:127], v[148:151], v[188:191], v[124:127]
	v_mfma_f32_16x16x32_bf16 v[120:123], v[164:167], v[188:191], v[120:123]
	v_mfma_f32_16x16x32_bf16 v[108:111], v[148:151], v[196:199], v[108:111]
	v_mfma_f32_16x16x32_bf16 v[104:107], v[164:167], v[196:199], v[104:107]
	v_mfma_f32_16x16x32_bf16 v[92:95], v[148:151], v[204:207], v[92:95]
	v_mfma_f32_16x16x32_bf16 v[88:91], v[164:167], v[204:207], v[88:91]
	v_mfma_f32_16x16x32_bf16 v[76:79], v[148:151], v[212:215], v[76:79]
	v_mfma_f32_16x16x32_bf16 v[72:75], v[164:167], v[212:215], v[72:75]
	v_mfma_f32_16x16x32_bf16 v[124:127], v[160:163], v[192:195], v[124:127]
	v_mfma_f32_16x16x32_bf16 v[120:123], v[168:171], v[192:195], v[120:123]
	v_mfma_f32_16x16x32_bf16 v[108:111], v[160:163], v[200:203], v[108:111]
	v_mfma_f32_16x16x32_bf16 v[104:107], v[168:171], v[200:203], v[104:107]
	v_mfma_f32_16x16x32_bf16 v[92:95], v[160:163], v[208:211], v[92:95]
	v_mfma_f32_16x16x32_bf16 v[88:91], v[168:171], v[208:211], v[88:91]
	v_mfma_f32_16x16x32_bf16 v[76:79], v[160:163], v[216:219], v[76:79]
	v_mfma_f32_16x16x32_bf16 v[72:75], v[168:171], v[216:219], v[72:75]
	s_setprio 0
	s_setprio 1
	v_mfma_f32_16x16x32_bf16 v[116:119], v[172:175], v[188:191], v[116:119]
	v_mfma_f32_16x16x32_bf16 v[112:115], v[180:183], v[188:191], v[112:115]
	v_mfma_f32_16x16x32_bf16 v[100:103], v[172:175], v[196:199], v[100:103]
	v_mfma_f32_16x16x32_bf16 v[96:99], v[180:183], v[196:199], v[96:99]
	v_mfma_f32_16x16x32_bf16 v[84:87], v[172:175], v[204:207], v[84:87]
	v_mfma_f32_16x16x32_bf16 v[80:83], v[180:183], v[204:207], v[80:83]
	v_mfma_f32_16x16x32_bf16 v[68:71], v[172:175], v[212:215], v[68:71]
	v_mfma_f32_16x16x32_bf16 v[64:67], v[180:183], v[212:215], v[64:67]
	v_mfma_f32_16x16x32_bf16 v[116:119], v[176:179], v[192:195], v[116:119]
	v_mfma_f32_16x16x32_bf16 v[112:115], v[184:187], v[192:195], v[112:115]
	v_mfma_f32_16x16x32_bf16 v[100:103], v[176:179], v[200:203], v[100:103]
	v_mfma_f32_16x16x32_bf16 v[96:99], v[184:187], v[200:203], v[96:99]
	v_mfma_f32_16x16x32_bf16 v[84:87], v[176:179], v[208:211], v[84:87]
	v_mfma_f32_16x16x32_bf16 v[80:83], v[184:187], v[208:211], v[80:83]
	v_mfma_f32_16x16x32_bf16 v[68:71], v[176:179], v[216:219], v[68:71]
	v_mfma_f32_16x16x32_bf16 v[64:67], v[184:187], v[216:219], v[64:67]
	s_setprio 0
	s_barrier
; #define PG8_STAGE(bufoff, gbase, voff) do { _Pragma("unroll") for (int _i = 0; _i < 2; ++_i) \
;         __builtin_amdgcn_global_load_lds((const unsigned*)((const char*)(gbase) + (voff)[_i]), (PG8_LAS unsigned*)(lds + (bufoff) + ldsw + _i * 8192), 16, 0, 0); } while (0)
; #define PG8_STAGE_A(bufoff, gbase, h, nx) do { _Pragma("unroll") for (int _i = 0; _i < 2; ++_i) { \
;         const unsigned vo_ = GA ? ((nx) ? vgn[h][_i] : vgc[h][_i]) : voffA[_i]; \
;         __builtin_amdgcn_global_load_lds((const unsigned*)((const char*)(gbase) + vo_), (PG8_LAS unsigned*)(lds + (bufoff) + ldsw + _i * 8192), 16, 0, 0); } } while (0)
; #define PG8_LDA(dst, b, h) do { _Pragma("unroll") for (int m = 0; m < 4; ++m) _Pragma("unroll") for (int k = 0; k < 2; ++k) dst[m][k] = *(const PG8_LAS bf16x8*)(lds + PG8_SA(b, h) + aoff + m * 2048 + k * 1024); } while (0)
; #define PG8_MMA(ai, bj, At, Bt) do { __builtin_amdgcn_s_setprio(1); _Pragma("unroll") for (int m = 0; m < 4; ++m) _Pragma("unroll") for (int n = 0; n < 2; ++n) _Pragma("unroll") for (int k = 0; k < 2; ++k) \
;         acc[ai][bj][m][n] = __builtin_amdgcn_mfma_f32_16x16x32_bf16(Bt[n][k], At[m][k], acc[ai][bj][m][n], 0, 0, 0); __builtin_amdgcn_s_setprio(0); } while (0)
; #define PG8_WAIT_V(n) asm volatile("s_waitcnt vmcnt(" #n ")" ::: "memory")
; #define PG8_WAIT_L(n) asm volatile("s_waitcnt lgkmcnt(" #n ")" ::: "memory")
; #define PG8_BAR __builtin_amdgcn_s_barrier()
; #define PG8_SCHED __builtin_amdgcn_sched_barrier(0)
; template <class Epi, class Sched>
; __device__ __forceinline__ void gemm_phase(const int WID_, PG8_LAS unsigned char* lds, const Sched& S, const Epi& E) {
;     ...
;             PG8_LDA(At, 1, 1); PG8_STAGE(PG8_SB(1, 0), b3, voffB); PG8_STAGE(PG8_SB(1, 1), b3 + hstepB, voffB); PG8_STAGE_A(PG8_SA(1, 0), a3, 0, last);
;             PG8_WAIT_V(8); PG8_WAIT_L(0); PG8_BAR; PG8_MMA(1, 0, At, B0); PG8_MMA(1, 1, At, B1); PG8_BAR; PG8_SCHED;
;         }
	s_add_i32 s28, s49, s30
	v_lshl_add_u64 v[152:153], v[152:153], 0, s[6:7]
	s_mov_b32 m0, s28
	ds_read_b128 v[188:191], v158 offset:49152
	ds_read_b128 v[192:195], v158 offset:50176
	ds_read_b128 v[196:199], v158 offset:51200
	ds_read_b128 v[200:203], v158 offset:52224
	ds_read_b128 v[204:207], v158 offset:53248
	ds_read_b128 v[208:211], v158 offset:54272
	ds_read_b128 v[212:215], v158 offset:55296
	ds_read_b128 v[216:219], v158 offset:56320
	global_load_lds_dwordx4 v[152:153], off
	s_add_i32 m0, s28, 0x2000
	s_add_u32 s22, s22, 0x40080
	v_lshl_add_u64 v[152:153], v[220:221], 0, s[6:7]
	s_addc_u32 s23, s23, 0
	s_add_i32 s28, s50, s30
	global_load_lds_dwordx4 v[152:153], off
	v_lshl_add_u64 v[152:153], s[22:23], 0, v[130:131]
	s_mov_b32 m0, s28
	s_nop 0
	global_load_lds_dwordx4 v[152:153], off
	v_lshl_add_u64 v[152:153], s[22:23], 0, v[134:135]
	s_add_i32 m0, s28, 0x2000
	s_nop 0
	global_load_lds_dwordx4 v[152:153], off
	v_lshl_add_u64 v[152:153], v[222:223], 0, s[6:7]
	s_mov_b32 m0, s37
	s_nop 0
	global_load_lds_dwordx4 v[152:153], off
	v_lshl_add_u64 v[152:153], v[224:225], 0, s[6:7]
	s_mov_b32 m0, s38
	s_nop 0
	global_load_lds_dwordx4 v[152:153], off
	s_waitcnt vmcnt(8)
	s_waitcnt lgkmcnt(0)
	s_barrier
	s_setprio 1
	s_waitcnt lgkmcnt(0)
	v_mfma_f32_16x16x32_bf16 v[60:63], v[148:151], v[188:191], v[60:63]
	v_mfma_f32_16x16x32_bf16 v[56:59], v[164:167], v[188:191], v[56:59]
	v_mfma_f32_16x16x32_bf16 v[44:47], v[148:151], v[196:199], v[44:47]
	v_mfma_f32_16x16x32_bf16 v[40:43], v[164:167], v[196:199], v[40:43]
	v_mfma_f32_16x16x32_bf16 v[28:31], v[148:151], v[204:207], v[28:31]
	v_mfma_f32_16x16x32_bf16 v[24:27], v[164:167], v[204:207], v[24:27]
	v_mfma_f32_16x16x32_bf16 v[12:15], v[148:151], v[212:215], v[12:15]
	v_mfma_f32_16x16x32_bf16 v[8:11], v[164:167], v[212:215], v[8:11]
	v_mfma_f32_16x16x32_bf16 v[60:63], v[160:163], v[192:195], v[60:63]
	v_mfma_f32_16x16x32_bf16 v[56:59], v[168:171], v[192:195], v[56:59]
	v_mfma_f32_16x16x32_bf16 v[44:47], v[160:163], v[200:203], v[44:47]
	v_mfma_f32_16x16x32_bf16 v[40:43], v[168:171], v[200:203], v[40:43]
	v_mfma_f32_16x16x32_bf16 v[28:31], v[160:163], v[208:211], v[28:31]
	v_mfma_f32_16x16x32_bf16 v[24:27], v[168:171], v[208:211], v[24:27]
	v_mfma_f32_16x16x32_bf16 v[12:15], v[160:163], v[216:219], v[12:15]
	v_mfma_f32_16x16x32_bf16 v[8:11], v[168:171], v[216:219], v[8:11]
	s_setprio 0
	s_setprio 1
	v_mfma_f32_16x16x32_bf16 v[52:55], v[172:175], v[188:191], v[52:55]
	v_mfma_f32_16x16x32_bf16 v[48:51], v[180:183], v[188:191], v[48:51]
	v_mfma_f32_16x16x32_bf16 v[36:39], v[172:175], v[196:199], v[36:39]
	v_mfma_f32_16x16x32_bf16 v[32:35], v[180:183], v[196:199], v[32:35]
	v_mfma_f32_16x16x32_bf16 v[20:23], v[172:175], v[204:207], v[20:23]
	v_mfma_f32_16x16x32_bf16 v[16:19], v[180:183], v[204:207], v[16:19]
	v_mfma_f32_16x16x32_bf16 v[4:7], v[172:175], v[212:215], v[4:7]
	v_mfma_f32_16x16x32_bf16 v[0:3], v[180:183], v[212:215], v[0:3]
	v_mfma_f32_16x16x32_bf16 v[52:55], v[176:179], v[192:195], v[52:55]
	v_mfma_f32_16x16x32_bf16 v[48:51], v[184:187], v[192:195], v[48:51]
	v_mfma_f32_16x16x32_bf16 v[36:39], v[176:179], v[200:203], v[36:39]
	v_mfma_f32_16x16x32_bf16 v[32:35], v[184:187], v[200:203], v[32:35]
	v_mfma_f32_16x16x32_bf16 v[20:23], v[176:179], v[208:211], v[20:23]
	v_mfma_f32_16x16x32_bf16 v[16:19], v[184:187], v[208:211], v[16:19]
	v_mfma_f32_16x16x32_bf16 v[4:7], v[176:179], v[216:219], v[4:7]
	v_mfma_f32_16x16x32_bf16 v[0:3], v[184:187], v[216:219], v[0:3]
	s_setprio 0
	s_add_i32 s48, s48, 2
	s_add_u32 s20, s20, 0x100
	s_addc_u32 s21, s21, 0
	s_add_u32 s46, s46, 0x100
	s_addc_u32 s47, s47, 0
	s_cmp_gt_u32 s48, 13
	s_barrier
	s_cbranch_scc0 .LBB0_114
	s_and_b64 vcc, exec, s[8:9]
	s_cbranch_vccz .LBB0_117
	s_barrier

; #define PG8_STAGE(bufoff, gbase, voff) do { _Pragma("unroll") for (int _i = 0; _i < 2; ++_i) \
;         __builtin_amdgcn_global_load_lds((const unsigned*)((const char*)(gbase) + (voff)[_i]), (PG8_LAS unsigned*)(lds + (bufoff) + ldsw + _i * 8192), 16, 0, 0); } while (0)
; #define PG8_STAGE_A(bufoff, gbase, h, nx) do { _Pragma("unroll") for (int _i = 0; _i < 2; ++_i) { \
;         const unsigned vo_ = GA ? ((nx) ? vgn[h][_i] : vgc[h][_i]) : voffA[_i]; \
;         __builtin_amdgcn_global_load_lds((const unsigned*)((const char*)(gbase) + vo_), (PG8_LAS unsigned*)(lds + (bufoff) + ldsw + _i * 8192), 16, 0, 0); } } while (0)
; #define PG8_LDA(dst, b, h) do { _Pragma("unroll") for (int m = 0; m < 4; ++m) _Pragma("unroll") for (int k = 0; k < 2; ++k) dst[m][k] = *(const PG8_LAS bf16x8*)(lds + PG8_SA(b, h) + aoff + m * 2048 + k * 1024); } while (0)
; #define PG8_LDB(dst, b, h) do { _Pragma("unroll") for (int n = 0; n < 2; ++n) _Pragma("unroll") for (int k = 0; k < 2; ++k) dst[n][k] = *(const PG8_LAS bf16x8*)(lds + PG8_SB(b, h) + boff + n * 2048 + k * 1024); } while (0)
; #define PG8_WAIT_V(n) asm volatile("s_waitcnt vmcnt(" #n ")" ::: "memory")
; #define PG8_WAIT_L(n) asm volatile("s_waitcnt lgkmcnt(" #n ")" ::: "memory")
; #define PG8_BAR __builtin_amdgcn_s_barrier()
; #define PG8_SCHED __builtin_amdgcn_sched_barrier(0)
; template <class Epi, class Sched>
; __device__ __forceinline__ void gemm_phase(const int WID_, PG8_LAS unsigned char* lds, const Sched& S, const Epi& E) {
;     ...
;         for (int t = 0; t < nt; t += 2) {
;             const bool last = (t == nt - 2);
;             const char* a1 = cA + (size_t)(t + 1) * kstep;
;             const char* a2 = last ? nA : cA + (size_t)(t + 2) * kstep; const char* b2 = last ? nB : cB + (size_t)(t + 2) * kstep;
;             const char* a3 = a2 + kstep; const char* b3 = b2 + kstep;
;             PG8_LDB(B0, 0, 0); PG8_LDB(B1, 0, 1); PG8_SCHED; PG8_LDA(At, 0, 0); PG8_STAGE_A(PG8_SA(1, 1), a1 + hstepA, 1, false);
;             PG8_WAIT_V(8); PG8_WAIT_L(0); PG8_BAR; PG8_MMA(0, 0, At, B0); PG8_MMA(0, 1, At, B1); PG8_BAR; PG8_SCHED;
;             PG8_LDA(At, 0, 1); PG8_STAGE(PG8_SB(0, 0), b2, voffB); PG8_STAGE(PG8_SB(0, 1), b2 + hstepB, voffB); PG8_STAGE_A(PG8_SA(0, 0), a2, 0, last);
;             PG8_WAIT_V(8); PG8_WAIT_L(0); PG8_BAR; PG8_MMA(1, 0, At, B0); PG8_MMA(1, 1, At, B1); PG8_BAR; PG8_SCHED;
.LBB0_263:
	ds_read_b128 v[138:141], v149
	ds_read_b128 v[142:145], v149 offset:1024
	ds_read_b128 v[152:155], v149 offset:2048
	ds_read_b128 v[156:159], v149 offset:3072
	ds_read_b128 v[160:163], v150
	ds_read_b128 v[164:167], v150 offset:1024
	ds_read_b128 v[168:171], v150 offset:2048
	ds_read_b128 v[172:175], v150 offset:3072
	s_add_u32 s8, s6, 0xfffe0080
	s_addc_u32 s9, s7, -1
	s_cmp_eq_u32 s35, 4
	s_cselect_b32 s11, s23, s9
	s_cselect_b32 s10, s22, s8
	s_cselect_b32 s9, s29, s21
	s_cselect_b32 s8, s28, s5
	v_lshl_add_u64 v[208:209], s[6:7], 0, v[134:135]
	s_add_i32 m0, s38, 0xc000
	ds_read_b128 v[176:179], v151
	ds_read_b128 v[180:183], v151 offset:1024
	ds_read_b128 v[184:187], v151 offset:2048
	ds_read_b128 v[188:191], v151 offset:3072
	ds_read_b128 v[192:195], v151 offset:4096
	ds_read_b128 v[196:199], v151 offset:5120
	ds_read_b128 v[200:203], v151 offset:6144
	ds_read_b128 v[204:207], v151 offset:7168
	global_load_lds_dwordx4 v[208:209], off
	v_lshl_add_u64 v[208:209], s[6:7], 0, v[136:137]
	s_add_i32 m0, s38, 0xe000
	s_nop 0
	global_load_lds_dwordx4 v[208:209], off
	s_waitcnt vmcnt(8)
	s_waitcnt lgkmcnt(0)
	s_barrier
	s_setprio 1
	s_waitcnt lgkmcnt(0)
	v_mfma_f32_16x16x32_bf16 v[124:127], v[138:141], v[176:179], v[124:127]
	v_mfma_f32_16x16x32_bf16 v[120:123], v[152:155], v[176:179], v[120:123]
	v_mfma_f32_16x16x32_bf16 v[108:111], v[138:141], v[184:187], v[108:111]
	v_mfma_f32_16x16x32_bf16 v[104:107], v[152:155], v[184:187], v[104:107]
	v_mfma_f32_16x16x32_bf16 v[92:95], v[138:141], v[192:195], v[92:95]
	v_mfma_f32_16x16x32_bf16 v[88:91], v[152:155], v[192:195], v[88:91]
	v_mfma_f32_16x16x32_bf16 v[76:79], v[138:141], v[200:203], v[76:79]
	v_mfma_f32_16x16x32_bf16 v[72:75], v[152:155], v[200:203], v[72:75]
	v_mfma_f32_16x16x32_bf16 v[124:127], v[142:145], v[180:183], v[124:127]
	v_mfma_f32_16x16x32_bf16 v[120:123], v[156:159], v[180:183], v[120:123]
	v_mfma_f32_16x16x32_bf16 v[108:111], v[142:145], v[188:191], v[108:111]
	v_mfma_f32_16x16x32_bf16 v[104:107], v[156:159], v[188:191], v[104:107]
	v_mfma_f32_16x16x32_bf16 v[92:95], v[142:145], v[196:199], v[92:95]
	v_mfma_f32_16x16x32_bf16 v[88:91], v[156:159], v[196:199], v[88:91]
	v_mfma_f32_16x16x32_bf16 v[76:79], v[142:145], v[204:207], v[76:79]
	v_mfma_f32_16x16x32_bf16 v[72:75], v[156:159], v[204:207], v[72:75]
	s_setprio 0
	s_setprio 1
	v_mfma_f32_16x16x32_bf16 v[116:119], v[160:163], v[176:179], v[116:119]
	v_mfma_f32_16x16x32_bf16 v[112:115], v[168:171], v[176:179], v[112:115]
	v_mfma_f32_16x16x32_bf16 v[100:103], v[160:163], v[184:187], v[100:103]
	v_mfma_f32_16x16x32_bf16 v[96:99], v[168:171], v[184:187], v[96:99]
	v_mfma_f32_16x16x32_bf16 v[84:87], v[160:163], v[192:195], v[84:87]
	v_mfma_f32_16x16x32_bf16 v[80:83], v[168:171], v[192:195], v[80:83]
	v_mfma_f32_16x16x32_bf16 v[68:71], v[160:163], v[200:203], v[68:71]
	v_mfma_f32_16x16x32_bf16 v[64:67], v[168:171], v[200:203], v[64:67]
	v_mfma_f32_16x16x32_bf16 v[116:119], v[164:167], v[180:183], v[116:119]
	v_mfma_f32_16x16x32_bf16 v[112:115], v[172:175], v[180:183], v[112:115]
	v_mfma_f32_16x16x32_bf16 v[100:103], v[164:167], v[188:191], v[100:103]
	v_mfma_f32_16x16x32_bf16 v[96:99], v[172:175], v[188:191], v[96:99]
	v_mfma_f32_16x16x32_bf16 v[84:87], v[164:167], v[196:199], v[84:87]
	v_mfma_f32_16x16x32_bf16 v[80:83], v[172:175], v[196:199], v[80:83]
	v_mfma_f32_16x16x32_bf16 v[68:71], v[164:167], v[204:207], v[68:71]
	v_mfma_f32_16x16x32_bf16 v[64:67], v[172:175], v[204:207], v[64:67]
	s_setprio 0
	s_barrier
	s_add_i32 s36, s47, s33
	v_lshl_add_u64 v[208:209], s[8:9], 0, v[128:129]
	s_mov_b32 m0, s36
	ds_read_b128 v[176:179], v151 offset:16384
	ds_read_b128 v[180:183], v151 offset:17408
	ds_read_b128 v[184:187], v151 offset:18432
	ds_read_b128 v[188:191], v151 offset:19456
	ds_read_b128 v[192:195], v151 offset:20480
	ds_read_b128 v[196:199], v151 offset:21504
	ds_read_b128 v[200:203], v151 offset:22528
	ds_read_b128 v[204:207], v151 offset:23552
	global_load_lds_dwordx4 v[208:209], off
	s_add_i32 m0, s36, 0x2000
	s_add_u32 s36, s8, 0x20000
	v_lshl_add_u64 v[210:211], s[8:9], 0, v[130:131]
	s_addc_u32 s37, s9, 0
	s_add_i32 s52, s48, s33
	global_load_lds_dwordx4 v[210:211], off
	v_lshl_add_u64 v[212:213], s[36:37], 0, v[128:129]
	s_mov_b32 m0, s52
	v_lshl_add_u64 v[214:215], s[10:11], 0, v[130:131]
	global_load_lds_dwordx4 v[212:213], off
	v_lshl_add_u64 v[212:213], s[36:37], 0, v[130:131]
	s_add_i32 m0, s52, 0x2000
	s_nop 0
	global_load_lds_dwordx4 v[212:213], off
	v_lshl_add_u64 v[212:213], s[10:11], 0, v[128:129]
	s_mov_b32 m0, s38
	s_nop 0
	global_load_lds_dwordx4 v[212:213], off
	s_mov_b32 m0, s39
	s_nop 0
	global_load_lds_dwordx4 v[214:215], off
	s_waitcnt vmcnt(8)
	s_waitcnt lgkmcnt(0)
	s_barrier
; #define PG8_STAGE(bufoff, gbase, voff) do { _Pragma("unroll") for (int _i = 0; _i < 2; ++_i) \
;         __builtin_amdgcn_global_load_lds((const unsigned*)((const char*)(gbase) + (voff)[_i]), (PG8_LAS unsigned*)(lds + (bufoff) + ldsw + _i * 8192), 16, 0, 0); } while (0)
; #define PG8_STAGE_A(bufoff, gbase, h, nx) do { _Pragma("unroll") for (int _i = 0; _i < 2; ++_i) { \
;         const unsigned vo_ = GA ? ((nx) ? vgn[h][_i] : vgc[h][_i]) : voffA[_i]; \
;         __builtin_amdgcn_global_load_lds((const unsigned*)((const char*)(gbase) + vo_), (PG8_LAS unsigned*)(lds + (bufoff) + ldsw + _i * 8192), 16, 0, 0); } } while (0)
; #define PG8_LDA(dst, b, h) do { _Pragma("unroll") for (int m = 0; m < 4; ++m) _Pragma("unroll") for (int k = 0; k < 2; ++k) dst[m][k] = *(const PG8_LAS bf16x8*)(lds + PG8_SA(b, h) + aoff + m * 2048 + k * 1024); } while (0)
; #define PG8_LDB(dst, b, h) do { _Pragma("unroll") for (int n = 0; n < 2; ++n) _Pragma("unroll") for (int k = 0; k < 2; ++k) dst[n][k] = *(const PG8_LAS bf16x8*)(lds + PG8_SB(b, h) + boff + n * 2048 + k * 1024); } while (0)
; #define PG8_MMA(ai, bj, At, Bt) do { __builtin_amdgcn_s_setprio(1); _Pragma("unroll") for (int m = 0; m < 4; ++m) _Pragma("unroll") for (int n = 0; n < 2; ++n) _Pragma("unroll") for (int k = 0; k < 2; ++k) \
;         acc[ai][bj][m][n] = __builtin_amdgcn_mfma_f32_16x16x32_bf16(Bt[n][k], At[m][k], acc[ai][bj][m][n], 0, 0, 0); __builtin_amdgcn_s_setprio(0); } while (0)
; #define PG8_WAIT_V(n) asm volatile("s_waitcnt vmcnt(" #n ")" ::: "memory")
; #define PG8_BAR __builtin_amdgcn_s_barrier()
; template <class Epi, class Sched>
; __device__ __forceinline__ void gemm_phase(const int WID_, PG8_LAS unsigned char* lds, const Sched& S, const Epi& E) {
;     ...
;             PG8_WAIT_V(8); PG8_WAIT_L(0); PG8_BAR; PG8_MMA(1, 0, At, B0); PG8_MMA(1, 1, At, B1); PG8_BAR; PG8_SCHED;
;             PG8_LDB(B0, 1, 0); PG8_LDB(B1, 1, 1); PG8_SCHED; PG8_LDA(At, 1, 0); PG8_STAGE_A(PG8_SA(0, 1), a2 + hstepA, 1, last);
;             PG8_WAIT_V(8); PG8_WAIT_L(0); PG8_BAR; PG8_MMA(0, 0, At, B0); PG8_MMA(0, 1, At, B1); PG8_BAR; PG8_SCHED;
;             PG8_LDA(At, 1, 1); PG8_STAGE(PG8_SB(1, 0), b3, voffB); PG8_STAGE(PG8_SB(1, 1), b3 + hstepB, voffB); PG8_STAGE_A(PG8_SA(1, 0), a3, 0, last);
;             PG8_WAIT_V(8); PG8_WAIT_L(0); PG8_BAR; PG8_MMA(1, 0, At, B0); PG8_MMA(1, 1, At, B1); PG8_BAR; PG8_SCHED;
	s_setprio 1
	s_waitcnt lgkmcnt(0)
	v_mfma_f32_16x16x32_bf16 v[60:63], v[138:141], v[176:179], v[60:63]
	v_mfma_f32_16x16x32_bf16 v[56:59], v[152:155], v[176:179], v[56:59]
	v_mfma_f32_16x16x32_bf16 v[44:47], v[138:141], v[184:187], v[44:47]
	v_mfma_f32_16x16x32_bf16 v[40:43], v[152:155], v[184:187], v[40:43]
	v_mfma_f32_16x16x32_bf16 v[28:31], v[138:141], v[192:195], v[28:31]
	v_mfma_f32_16x16x32_bf16 v[24:27], v[152:155], v[192:195], v[24:27]
	v_mfma_f32_16x16x32_bf16 v[12:15], v[138:141], v[200:203], v[12:15]
	v_mfma_f32_16x16x32_bf16 v[8:11], v[152:155], v[200:203], v[8:11]
	v_mfma_f32_16x16x32_bf16 v[60:63], v[142:145], v[180:183], v[60:63]
	v_mfma_f32_16x16x32_bf16 v[56:59], v[156:159], v[180:183], v[56:59]
	v_mfma_f32_16x16x32_bf16 v[44:47], v[142:145], v[188:191], v[44:47]
	v_mfma_f32_16x16x32_bf16 v[40:43], v[156:159], v[188:191], v[40:43]
	v_mfma_f32_16x16x32_bf16 v[28:31], v[142:145], v[196:199], v[28:31]
	v_mfma_f32_16x16x32_bf16 v[24:27], v[156:159], v[196:199], v[24:27]
	v_mfma_f32_16x16x32_bf16 v[12:15], v[142:145], v[204:207], v[12:15]
	v_mfma_f32_16x16x32_bf16 v[8:11], v[156:159], v[204:207], v[8:11]
	s_setprio 0
	s_setprio 1
	v_mfma_f32_16x16x32_bf16 v[52:55], v[160:163], v[176:179], v[52:55]
	v_mfma_f32_16x16x32_bf16 v[48:51], v[168:171], v[176:179], v[48:51]
	v_mfma_f32_16x16x32_bf16 v[36:39], v[160:163], v[184:187], v[36:39]
	v_mfma_f32_16x16x32_bf16 v[32:35], v[168:171], v[184:187], v[32:35]
	v_mfma_f32_16x16x32_bf16 v[20:23], v[160:163], v[192:195], v[20:23]
	v_mfma_f32_16x16x32_bf16 v[16:19], v[168:171], v[192:195], v[16:19]
	v_mfma_f32_16x16x32_bf16 v[4:7], v[160:163], v[200:203], v[4:7]
	v_mfma_f32_16x16x32_bf16 v[0:3], v[168:171], v[200:203], v[0:3]
	v_mfma_f32_16x16x32_bf16 v[52:55], v[164:167], v[180:183], v[52:55]
	v_mfma_f32_16x16x32_bf16 v[48:51], v[172:175], v[180:183], v[48:51]
	v_mfma_f32_16x16x32_bf16 v[36:39], v[164:167], v[188:191], v[36:39]
	v_mfma_f32_16x16x32_bf16 v[32:35], v[172:175], v[188:191], v[32:35]
	v_mfma_f32_16x16x32_bf16 v[20:23], v[164:167], v[196:199], v[20:23]
	v_mfma_f32_16x16x32_bf16 v[16:19], v[172:175], v[196:199], v[16:19]
	v_mfma_f32_16x16x32_bf16 v[4:7], v[164:167], v[204:207], v[4:7]
	v_mfma_f32_16x16x32_bf16 v[0:3], v[172:175], v[204:207], v[0:3]
	s_setprio 0
	s_barrier
	s_add_i32 s36, 0, 0x18000
	v_add_u32_e32 v132, s36, v147
	s_add_i32 s37, 0, 0x1c000
	ds_read_b128 v[138:141], v132
	ds_read_b128 v[142:145], v132 offset:1024
	ds_read_b128 v[152:155], v132 offset:2048
	ds_read_b128 v[156:159], v132 offset:3072
	v_add_u32_e32 v132, s37, v147
	ds_read_b128 v[160:163], v132
	ds_read_b128 v[164:167], v132 offset:1024
	ds_read_b128 v[168:171], v132 offset:2048
	ds_read_b128 v[172:175], v132 offset:3072
	s_add_u32 s10, s10, 0x20000
	s_addc_u32 s11, s11, 0
	s_mov_b32 m0, s40
	v_lshl_add_u64 v[216:217], s[10:11], 0, v[128:129]
	ds_read_b128 v[176:179], v151 offset:32768
	ds_read_b128 v[180:183], v151 offset:33792
	ds_read_b128 v[184:187], v151 offset:34816
	ds_read_b128 v[188:191], v151 offset:35840
	ds_read_b128 v[192:195], v151 offset:36864
	ds_read_b128 v[196:199], v151 offset:37888
	ds_read_b128 v[200:203], v151 offset:38912
	ds_read_b128 v[204:207], v151 offset:39936
	global_load_lds_dwordx4 v[216:217], off
	v_lshl_add_u64 v[216:217], s[10:11], 0, v[130:131]
	s_mov_b32 m0, s41
	s_nop 0
	global_load_lds_dwordx4 v[216:217], off
	s_waitcnt vmcnt(8)
	s_waitcnt lgkmcnt(0)
	s_barrier
	s_setprio 1
	s_waitcnt lgkmcnt(0)
	v_mfma_f32_16x16x32_bf16 v[124:127], v[138:141], v[176:179], v[124:127]
	v_mfma_f32_16x16x32_bf16 v[120:123], v[152:155], v[176:179], v[120:123]
	v_mfma_f32_16x16x32_bf16 v[108:111], v[138:141], v[184:187], v[108:111]
	v_mfma_f32_16x16x32_bf16 v[104:107], v[152:155], v[184:187], v[104:107]
	v_mfma_f32_16x16x32_bf16 v[92:95], v[138:141], v[192:195], v[92:95]
	v_mfma_f32_16x16x32_bf16 v[88:91], v[152:155], v[192:195], v[88:91]
	v_mfma_f32_16x16x32_bf16 v[76:79], v[138:141], v[200:203], v[76:79]
	v_mfma_f32_16x16x32_bf16 v[72:75], v[152:155], v[200:203], v[72:75]
	v_mfma_f32_16x16x32_bf16 v[124:127], v[142:145], v[180:183], v[124:127]
	v_mfma_f32_16x16x32_bf16 v[120:123], v[156:159], v[180:183], v[120:123]
	v_mfma_f32_16x16x32_bf16 v[108:111], v[142:145], v[188:191], v[108:111]
	v_mfma_f32_16x16x32_bf16 v[104:107], v[156:159], v[188:191], v[104:107]
	v_mfma_f32_16x16x32_bf16 v[92:95], v[142:145], v[196:199], v[92:95]
	v_mfma_f32_16x16x32_bf16 v[88:91], v[156:159], v[196:199], v[88:91]
	v_mfma_f32_16x16x32_bf16 v[76:79], v[142:145], v[204:207], v[76:79]
	v_mfma_f32_16x16x32_bf16 v[72:75], v[156:159], v[204:207], v[72:75]
	s_setprio 0
	s_setprio 1
	v_mfma_f32_16x16x32_bf16 v[116:119], v[160:163], v[176:179], v[116:119]
	v_mfma_f32_16x16x32_bf16 v[112:115], v[168:171], v[176:179], v[112:115]
	v_mfma_f32_16x16x32_bf16 v[100:103], v[160:163], v[184:187], v[100:103]
	v_mfma_f32_16x16x32_bf16 v[96:99], v[168:171], v[184:187], v[96:99]
	v_mfma_f32_16x16x32_bf16 v[84:87], v[160:163], v[192:195], v[84:87]
	v_mfma_f32_16x16x32_bf16 v[80:83], v[168:171], v[192:195], v[80:83]
	v_mfma_f32_16x16x32_bf16 v[68:71], v[160:163], v[200:203], v[68:71]
	v_mfma_f32_16x16x32_bf16 v[64:67], v[168:171], v[200:203], v[64:67]
	v_mfma_f32_16x16x32_bf16 v[116:119], v[164:167], v[180:183], v[116:119]
	v_mfma_f32_16x16x32_bf16 v[112:115], v[172:175], v[180:183], v[112:115]
	v_mfma_f32_16x16x32_bf16 v[100:103], v[164:167], v[188:191], v[100:103]
	v_mfma_f32_16x16x32_bf16 v[96:99], v[172:175], v[188:191], v[96:99]
	v_mfma_f32_16x16x32_bf16 v[84:87], v[164:167], v[196:199], v[84:87]
	v_mfma_f32_16x16x32_bf16 v[80:83], v[172:175], v[196:199], v[80:83]
	v_mfma_f32_16x16x32_bf16 v[68:71], v[164:167], v[204:207], v[68:71]
	v_mfma_f32_16x16x32_bf16 v[64:67], v[172:175], v[204:207], v[64:67]
	s_setprio 0
	s_barrier
; #define PG8_STAGE(bufoff, gbase, voff) do { _Pragma("unroll") for (int _i = 0; _i < 2; ++_i) \
;         __builtin_amdgcn_global_load_lds((const unsigned*)((const char*)(gbase) + (voff)[_i]), (PG8_LAS unsigned*)(lds + (bufoff) + ldsw + _i * 8192), 16, 0, 0); } while (0)
; #define PG8_STAGE_A(bufoff, gbase, h, nx) do { _Pragma("unroll") for (int _i = 0; _i < 2; ++_i) { \
;         const unsigned vo_ = GA ? ((nx) ? vgn[h][_i] : vgc[h][_i]) : voffA[_i]; \
;         __builtin_amdgcn_global_load_lds((const unsigned*)((const char*)(gbase) + vo_), (PG8_LAS unsigned*)(lds + (bufoff) + ldsw + _i * 8192), 16, 0, 0); } } while (0)
; #define PG8_LDA(dst, b, h) do { _Pragma("unroll") for (int m = 0; m < 4; ++m) _Pragma("unroll") for (int k = 0; k < 2; ++k) dst[m][k] = *(const PG8_LAS bf16x8*)(lds + PG8_SA(b, h) + aoff + m * 2048 + k * 1024); } while (0)
; #define PG8_MMA(ai, bj, At, Bt) do { __builtin_amdgcn_s_setprio(1); _Pragma("unroll") for (int m = 0; m < 4; ++m) _Pragma("unroll") for (int n = 0; n < 2; ++n) _Pragma("unroll") for (int k = 0; k < 2; ++k) \
;         acc[ai][bj][m][n] = __builtin_amdgcn_mfma_f32_16x16x32_bf16(Bt[n][k], At[m][k], acc[ai][bj][m][n], 0, 0, 0); __builtin_amdgcn_s_setprio(0); } while (0)
; #define PG8_WAIT_V(n) asm volatile("s_waitcnt vmcnt(" #n ")" ::: "memory")
; #define PG8_WAIT_L(n) asm volatile("s_waitcnt lgkmcnt(" #n ")" ::: "memory")
; #define PG8_BAR __builtin_amdgcn_s_barrier()
; #define PG8_SCHED __builtin_amdgcn_sched_barrier(0)
; template <class Epi, class Sched>
; __device__ __forceinline__ void gemm_phase(const int WID_, PG8_LAS unsigned char* lds, const Sched& S, const Epi& E) {
;     ...
;             PG8_LDA(At, 1, 1); PG8_STAGE(PG8_SB(1, 0), b3, voffB); PG8_STAGE(PG8_SB(1, 1), b3 + hstepB, voffB); PG8_STAGE_A(PG8_SA(1, 0), a3, 0, last);
;             PG8_WAIT_V(8); PG8_WAIT_L(0); PG8_BAR; PG8_MMA(1, 0, At, B0); PG8_MMA(1, 1, At, B1); PG8_BAR; PG8_SCHED;
;         }
	s_add_i32 s10, s36, s33
	v_lshl_add_u64 v[208:209], v[208:209], 0, s[16:17]
	s_mov_b32 m0, s10
	ds_read_b128 v[176:179], v151 offset:49152
	ds_read_b128 v[180:183], v151 offset:50176
	ds_read_b128 v[184:187], v151 offset:51200
	ds_read_b128 v[188:191], v151 offset:52224
	ds_read_b128 v[192:195], v151 offset:53248
	ds_read_b128 v[196:199], v151 offset:54272
	ds_read_b128 v[200:203], v151 offset:55296
	ds_read_b128 v[204:207], v151 offset:56320
	global_load_lds_dwordx4 v[208:209], off
	s_add_i32 m0, s10, 0x2000
	s_add_u32 s8, s8, 0x20080
	v_lshl_add_u64 v[208:209], v[210:211], 0, s[16:17]
	s_addc_u32 s9, s9, 0
	s_add_i32 s10, s37, s33
	global_load_lds_dwordx4 v[208:209], off
	v_lshl_add_u64 v[208:209], s[8:9], 0, v[128:129]
	s_mov_b32 m0, s10
	s_nop 0
	global_load_lds_dwordx4 v[208:209], off
	v_lshl_add_u64 v[208:209], s[8:9], 0, v[130:131]
	s_add_i32 m0, s10, 0x2000
	s_nop 0
	global_load_lds_dwordx4 v[208:209], off
	v_lshl_add_u64 v[208:209], v[212:213], 0, s[16:17]
	s_mov_b32 m0, s43
	s_nop 0
	global_load_lds_dwordx4 v[208:209], off
	v_lshl_add_u64 v[208:209], v[214:215], 0, s[16:17]
	s_mov_b32 m0, s44
	s_nop 0
	global_load_lds_dwordx4 v[208:209], off
	s_waitcnt vmcnt(8)
	s_waitcnt lgkmcnt(0)
	s_barrier
	s_setprio 1
	s_waitcnt lgkmcnt(0)
	v_mfma_f32_16x16x32_bf16 v[60:63], v[138:141], v[176:179], v[60:63]
	v_mfma_f32_16x16x32_bf16 v[56:59], v[152:155], v[176:179], v[56:59]
	v_mfma_f32_16x16x32_bf16 v[44:47], v[138:141], v[184:187], v[44:47]
	v_mfma_f32_16x16x32_bf16 v[40:43], v[152:155], v[184:187], v[40:43]
	v_mfma_f32_16x16x32_bf16 v[28:31], v[138:141], v[192:195], v[28:31]
	v_mfma_f32_16x16x32_bf16 v[24:27], v[152:155], v[192:195], v[24:27]
	v_mfma_f32_16x16x32_bf16 v[12:15], v[138:141], v[200:203], v[12:15]
	v_mfma_f32_16x16x32_bf16 v[8:11], v[152:155], v[200:203], v[8:11]
	v_mfma_f32_16x16x32_bf16 v[60:63], v[142:145], v[180:183], v[60:63]
	v_mfma_f32_16x16x32_bf16 v[56:59], v[156:159], v[180:183], v[56:59]
	v_mfma_f32_16x16x32_bf16 v[44:47], v[142:145], v[188:191], v[44:47]
	v_mfma_f32_16x16x32_bf16 v[40:43], v[156:159], v[188:191], v[40:43]
	v_mfma_f32_16x16x32_bf16 v[28:31], v[142:145], v[196:199], v[28:31]
	v_mfma_f32_16x16x32_bf16 v[24:27], v[156:159], v[196:199], v[24:27]
	v_mfma_f32_16x16x32_bf16 v[12:15], v[142:145], v[204:207], v[12:15]
	v_mfma_f32_16x16x32_bf16 v[8:11], v[156:159], v[204:207], v[8:11]
	s_setprio 0
	s_setprio 1
	v_mfma_f32_16x16x32_bf16 v[52:55], v[160:163], v[176:179], v[52:55]
	v_mfma_f32_16x16x32_bf16 v[48:51], v[168:171], v[176:179], v[48:51]
	v_mfma_f32_16x16x32_bf16 v[36:39], v[160:163], v[184:187], v[36:39]
	v_mfma_f32_16x16x32_bf16 v[32:35], v[168:171], v[184:187], v[32:35]
	v_mfma_f32_16x16x32_bf16 v[20:23], v[160:163], v[192:195], v[20:23]
	v_mfma_f32_16x16x32_bf16 v[16:19], v[168:171], v[192:195], v[16:19]
	v_mfma_f32_16x16x32_bf16 v[4:7], v[160:163], v[200:203], v[4:7]
	v_mfma_f32_16x16x32_bf16 v[0:3], v[168:171], v[200:203], v[0:3]
	v_mfma_f32_16x16x32_bf16 v[52:55], v[164:167], v[180:183], v[52:55]
	v_mfma_f32_16x16x32_bf16 v[48:51], v[172:175], v[180:183], v[48:51]
	v_mfma_f32_16x16x32_bf16 v[36:39], v[164:167], v[188:191], v[36:39]
	v_mfma_f32_16x16x32_bf16 v[32:35], v[172:175], v[188:191], v[32:35]
	v_mfma_f32_16x16x32_bf16 v[20:23], v[164:167], v[196:199], v[20:23]
	v_mfma_f32_16x16x32_bf16 v[16:19], v[172:175], v[196:199], v[16:19]
	v_mfma_f32_16x16x32_bf16 v[4:7], v[164:167], v[204:207], v[4:7]
	v_mfma_f32_16x16x32_bf16 v[0:3], v[172:175], v[204:207], v[0:3]
	s_setprio 0
	s_add_i32 s35, s35, 2
	s_add_u32 s6, s6, 0x100
	s_addc_u32 s7, s7, 0
	s_add_u32 s5, s5, 0x100
	s_addc_u32 s21, s21, 0
	s_cmp_gt_u32 s35, 5
	s_barrier
	s_cbranch_scc0 .LBB0_263
	s_and_b64 vcc, exec, s[18:19]
	s_cbranch_vccz .LBB0_266
	s_barrier

; #define PG8_STAGE(bufoff, gbase, voff) do { _Pragma("unroll") for (int _i = 0; _i < 2; ++_i) \
;         __builtin_amdgcn_global_load_lds((const unsigned*)((const char*)(gbase) + (voff)[_i]), (PG8_LAS unsigned*)(lds + (bufoff) + ldsw + _i * 8192), 16, 0, 0); } while (0)
; #define PG8_STAGE_A(bufoff, gbase, h, nx) do { _Pragma("unroll") for (int _i = 0; _i < 2; ++_i) { \
;         const unsigned vo_ = GA ? ((nx) ? vgn[h][_i] : vgc[h][_i]) : voffA[_i]; \
;         __builtin_amdgcn_global_load_lds((const unsigned*)((const char*)(gbase) + vo_), (PG8_LAS unsigned*)(lds + (bufoff) + ldsw + _i * 8192), 16, 0, 0); } } while (0)
; #define PG8_LDA(dst, b, h) do { _Pragma("unroll") for (int m = 0; m < 4; ++m) _Pragma("unroll") for (int k = 0; k < 2; ++k) dst[m][k] = *(const PG8_LAS bf16x8*)(lds + PG8_SA(b, h) + aoff + m * 2048 + k * 1024); } while (0)
; #define PG8_LDB(dst, b, h) do { _Pragma("unroll") for (int n = 0; n < 2; ++n) _Pragma("unroll") for (int k = 0; k < 2; ++k) dst[n][k] = *(const PG8_LAS bf16x8*)(lds + PG8_SB(b, h) + boff + n * 2048 + k * 1024); } while (0)
; #define PG8_WAIT_V(n) asm volatile("s_waitcnt vmcnt(" #n ")" ::: "memory")
; #define PG8_WAIT_L(n) asm volatile("s_waitcnt lgkmcnt(" #n ")" ::: "memory")
; #define PG8_BAR __builtin_amdgcn_s_barrier()
; #define PG8_SCHED __builtin_amdgcn_sched_barrier(0)
; template <class Epi, class Sched>
; __device__ __forceinline__ void gemm_phase(const int WID_, PG8_LAS unsigned char* lds, const Sched& S, const Epi& E) {
;     ...
;         for (int t = 0; t < nt; t += 2) {
;             const bool last = (t == nt - 2);
;             const char* a1 = cA + (size_t)(t + 1) * kstep;
;             const char* a2 = last ? nA : cA + (size_t)(t + 2) * kstep; const char* b2 = last ? nB : cB + (size_t)(t + 2) * kstep;
;             const char* a3 = a2 + kstep; const char* b3 = b2 + kstep;
;             PG8_LDB(B0, 0, 0); PG8_LDB(B1, 0, 1); PG8_SCHED; PG8_LDA(At, 0, 0); PG8_STAGE_A(PG8_SA(1, 1), a1 + hstepA, 1, false);
;             PG8_WAIT_V(8); PG8_WAIT_L(0); PG8_BAR; PG8_MMA(0, 0, At, B0); PG8_MMA(0, 1, At, B1); PG8_BAR; PG8_SCHED;
;             PG8_LDA(At, 0, 1); PG8_STAGE(PG8_SB(0, 0), b2, voffB); PG8_STAGE(PG8_SB(0, 1), b2 + hstepB, voffB); PG8_STAGE_A(PG8_SA(0, 0), a2, 0, last);
;             PG8_WAIT_V(8); PG8_WAIT_L(0); PG8_BAR; PG8_MMA(1, 0, At, B0); PG8_MMA(1, 1, At, B1); PG8_BAR; PG8_SCHED;
.LBB0_568:
	s_add_i32 s62, s2, 2
	s_add_u32 s3, s0, 0xffff0080
	s_addc_u32 s4, s1, -1
	s_add_i32 s63, 0, 0x10000
	s_cmp_eq_u32 s11, s2
	s_cselect_b32 s5, s53, s4
	s_cselect_b32 s4, s52, s3
	v_add_u32_e32 v136, s63, v153
	s_cselect_b32 s3, s61, s51
	s_cselect_b32 s2, s60, s49
	s_add_i32 s69, 0, 0x14000
	ds_read_b128 v[80:83], v136
	ds_read_b128 v[88:91], v136 offset:1024
	ds_read_b128 v[156:159], v136 offset:2048
	ds_read_b128 v[160:163], v136 offset:3072
	v_add_u32_e32 v136, s69, v153
	ds_read_b128 v[164:167], v136
	ds_read_b128 v[168:171], v136 offset:1024
	ds_read_b128 v[172:175], v136 offset:2048
	ds_read_b128 v[176:179], v136 offset:3072
	v_lshl_add_u64 v[212:213], s[0:1], 0, v[146:147]
	s_add_i32 m0, s37, 0xc000
	ds_read_b128 v[180:183], v155
	ds_read_b128 v[184:187], v155 offset:1024
	ds_read_b128 v[188:191], v155 offset:2048
	ds_read_b128 v[192:195], v155 offset:3072
	ds_read_b128 v[196:199], v155 offset:4096
	ds_read_b128 v[200:203], v155 offset:5120
	ds_read_b128 v[204:207], v155 offset:6144
	ds_read_b128 v[208:211], v155 offset:7168
	global_load_lds_dwordx4 v[212:213], off
	v_lshl_add_u64 v[212:213], s[0:1], 0, v[148:149]
	s_add_i32 m0, s37, 0xe000
	s_nop 0
	global_load_lds_dwordx4 v[212:213], off
	s_waitcnt vmcnt(8)
	s_waitcnt lgkmcnt(0)
	s_barrier
	s_setprio 1
	s_waitcnt lgkmcnt(0)
	v_mfma_f32_16x16x32_bf16 v[132:135], v[80:83], v[180:183], v[132:135]
	v_mfma_f32_16x16x32_bf16 v[128:131], v[156:159], v[180:183], v[128:131]
	v_mfma_f32_16x16x32_bf16 v[124:127], v[80:83], v[188:191], v[124:127]
	v_mfma_f32_16x16x32_bf16 v[120:123], v[156:159], v[188:191], v[120:123]
	v_mfma_f32_16x16x32_bf16 v[116:119], v[80:83], v[196:199], v[116:119]
	v_mfma_f32_16x16x32_bf16 v[112:115], v[156:159], v[196:199], v[112:115]
	v_mfma_f32_16x16x32_bf16 v[108:111], v[80:83], v[204:207], v[108:111]
	v_mfma_f32_16x16x32_bf16 v[104:107], v[156:159], v[204:207], v[104:107]
	v_mfma_f32_16x16x32_bf16 v[132:135], v[88:91], v[184:187], v[132:135]
	v_mfma_f32_16x16x32_bf16 v[128:131], v[160:163], v[184:187], v[128:131]
	v_mfma_f32_16x16x32_bf16 v[124:127], v[88:91], v[192:195], v[124:127]
	v_mfma_f32_16x16x32_bf16 v[120:123], v[160:163], v[192:195], v[120:123]
	v_mfma_f32_16x16x32_bf16 v[116:119], v[88:91], v[200:203], v[116:119]
	v_mfma_f32_16x16x32_bf16 v[112:115], v[160:163], v[200:203], v[112:115]
	v_mfma_f32_16x16x32_bf16 v[108:111], v[88:91], v[208:211], v[108:111]
	v_mfma_f32_16x16x32_bf16 v[104:107], v[160:163], v[208:211], v[104:107]
	s_setprio 0
	s_setprio 1
	v_mfma_f32_16x16x32_bf16 v[60:63], v[164:167], v[180:183], v[60:63]
	v_mfma_f32_16x16x32_bf16 v[56:59], v[172:175], v[180:183], v[56:59]
	v_mfma_f32_16x16x32_bf16 v[52:55], v[164:167], v[188:191], v[52:55]
	v_mfma_f32_16x16x32_bf16 v[48:51], v[172:175], v[188:191], v[48:51]
	v_mfma_f32_16x16x32_bf16 v[44:47], v[164:167], v[196:199], v[44:47]
	v_mfma_f32_16x16x32_bf16 v[40:43], v[172:175], v[196:199], v[40:43]
	v_mfma_f32_16x16x32_bf16 v[36:39], v[164:167], v[204:207], v[36:39]
	v_mfma_f32_16x16x32_bf16 v[32:35], v[172:175], v[204:207], v[32:35]
	v_mfma_f32_16x16x32_bf16 v[60:63], v[168:171], v[184:187], v[60:63]
	v_mfma_f32_16x16x32_bf16 v[56:59], v[176:179], v[184:187], v[56:59]
	v_mfma_f32_16x16x32_bf16 v[52:55], v[168:171], v[192:195], v[52:55]
	v_mfma_f32_16x16x32_bf16 v[48:51], v[176:179], v[192:195], v[48:51]
	v_mfma_f32_16x16x32_bf16 v[44:47], v[168:171], v[200:203], v[44:47]
	v_mfma_f32_16x16x32_bf16 v[40:43], v[176:179], v[200:203], v[40:43]
	v_mfma_f32_16x16x32_bf16 v[36:39], v[168:171], v[208:211], v[36:39]
	v_mfma_f32_16x16x32_bf16 v[32:35], v[176:179], v[208:211], v[32:35]
	s_setprio 0
	s_barrier
	s_add_i32 s63, s63, s35
	v_lshl_add_u64 v[212:213], s[2:3], 0, v[140:141]
	s_mov_b32 m0, s63
	ds_read_b128 v[180:183], v155 offset:16384
	ds_read_b128 v[184:187], v155 offset:17408
	ds_read_b128 v[188:191], v155 offset:18432
	ds_read_b128 v[192:195], v155 offset:19456
	ds_read_b128 v[196:199], v155 offset:20480
	ds_read_b128 v[200:203], v155 offset:21504
	ds_read_b128 v[204:207], v155 offset:22528
	ds_read_b128 v[208:211], v155 offset:23552
	global_load_lds_dwordx4 v[212:213], off
	s_add_i32 m0, s63, 0x2000
	s_add_u32 s76, s2, 0x10000
	v_lshl_add_u64 v[214:215], s[2:3], 0, v[144:145]
	s_addc_u32 s77, s3, 0
	s_add_i32 s63, s69, s35
	global_load_lds_dwordx4 v[214:215], off
	v_lshl_add_u64 v[216:217], s[76:77], 0, v[140:141]
	s_mov_b32 m0, s63
	v_lshl_add_u64 v[218:219], s[4:5], 0, v[142:143]
	global_load_lds_dwordx4 v[216:217], off
	v_lshl_add_u64 v[216:217], s[76:77], 0, v[144:145]
	s_add_i32 m0, s63, 0x2000
	s_nop 0
	global_load_lds_dwordx4 v[216:217], off
	v_lshl_add_u64 v[216:217], s[4:5], 0, v[138:139]
	s_mov_b32 m0, s37
	s_nop 0
	global_load_lds_dwordx4 v[216:217], off
	s_mov_b32 m0, s39
	s_nop 0
	global_load_lds_dwordx4 v[218:219], off
	s_waitcnt vmcnt(8)
	s_waitcnt lgkmcnt(0)
	s_barrier
; #define PG8_STAGE(bufoff, gbase, voff) do { _Pragma("unroll") for (int _i = 0; _i < 2; ++_i) \
;         __builtin_amdgcn_global_load_lds((const unsigned*)((const char*)(gbase) + (voff)[_i]), (PG8_LAS unsigned*)(lds + (bufoff) + ldsw + _i * 8192), 16, 0, 0); } while (0)
; #define PG8_STAGE_A(bufoff, gbase, h, nx) do { _Pragma("unroll") for (int _i = 0; _i < 2; ++_i) { \
;         const unsigned vo_ = GA ? ((nx) ? vgn[h][_i] : vgc[h][_i]) : voffA[_i]; \
;         __builtin_amdgcn_global_load_lds((const unsigned*)((const char*)(gbase) + vo_), (PG8_LAS unsigned*)(lds + (bufoff) + ldsw + _i * 8192), 16, 0, 0); } } while (0)
; #define PG8_LDA(dst, b, h) do { _Pragma("unroll") for (int m = 0; m < 4; ++m) _Pragma("unroll") for (int k = 0; k < 2; ++k) dst[m][k] = *(const PG8_LAS bf16x8*)(lds + PG8_SA(b, h) + aoff + m * 2048 + k * 1024); } while (0)
; #define PG8_LDB(dst, b, h) do { _Pragma("unroll") for (int n = 0; n < 2; ++n) _Pragma("unroll") for (int k = 0; k < 2; ++k) dst[n][k] = *(const PG8_LAS bf16x8*)(lds + PG8_SB(b, h) + boff + n * 2048 + k * 1024); } while (0)
; #define PG8_MMA(ai, bj, At, Bt) do { __builtin_amdgcn_s_setprio(1); _Pragma("unroll") for (int m = 0; m < 4; ++m) _Pragma("unroll") for (int n = 0; n < 2; ++n) _Pragma("unroll") for (int k = 0; k < 2; ++k) \
;         acc[ai][bj][m][n] = __builtin_amdgcn_mfma_f32_16x16x32_bf16(Bt[n][k], At[m][k], acc[ai][bj][m][n], 0, 0, 0); __builtin_amdgcn_s_setprio(0); } while (0)
; #define PG8_WAIT_V(n) asm volatile("s_waitcnt vmcnt(" #n ")" ::: "memory")
; #define PG8_BAR __builtin_amdgcn_s_barrier()
; template <class Epi, class Sched>
; __device__ __forceinline__ void gemm_phase(const int WID_, PG8_LAS unsigned char* lds, const Sched& S, const Epi& E) {
;     ...
;             PG8_WAIT_V(8); PG8_WAIT_L(0); PG8_BAR; PG8_MMA(1, 0, At, B0); PG8_MMA(1, 1, At, B1); PG8_BAR; PG8_SCHED;
;             PG8_LDB(B0, 1, 0); PG8_LDB(B1, 1, 1); PG8_SCHED; PG8_LDA(At, 1, 0); PG8_STAGE_A(PG8_SA(0, 1), a2 + hstepA, 1, last);
;             PG8_WAIT_V(8); PG8_WAIT_L(0); PG8_BAR; PG8_MMA(0, 0, At, B0); PG8_MMA(0, 1, At, B1); PG8_BAR; PG8_SCHED;
;             PG8_LDA(At, 1, 1); PG8_STAGE(PG8_SB(1, 0), b3, voffB); PG8_STAGE(PG8_SB(1, 1), b3 + hstepB, voffB); PG8_STAGE_A(PG8_SA(1, 0), a3, 0, last);
;             PG8_WAIT_V(8); PG8_WAIT_L(0); PG8_BAR; PG8_MMA(1, 0, At, B0); PG8_MMA(1, 1, At, B1); PG8_BAR; PG8_SCHED;
	s_setprio 1
	s_waitcnt lgkmcnt(0)
	v_mfma_f32_16x16x32_bf16 v[100:103], v[80:83], v[180:183], v[100:103]
	v_mfma_f32_16x16x32_bf16 v[96:99], v[156:159], v[180:183], v[96:99]
	v_mfma_f32_16x16x32_bf16 v[92:95], v[80:83], v[188:191], v[92:95]
	v_mfma_f32_16x16x32_bf16 v[84:87], v[156:159], v[188:191], v[84:87]
	v_mfma_f32_16x16x32_bf16 v[76:79], v[80:83], v[196:199], v[76:79]
	v_mfma_f32_16x16x32_bf16 v[72:75], v[156:159], v[196:199], v[72:75]
	v_mfma_f32_16x16x32_bf16 v[68:71], v[80:83], v[204:207], v[68:71]
	v_mfma_f32_16x16x32_bf16 v[64:67], v[156:159], v[204:207], v[64:67]
	v_mfma_f32_16x16x32_bf16 v[100:103], v[88:91], v[184:187], v[100:103]
	v_mfma_f32_16x16x32_bf16 v[96:99], v[160:163], v[184:187], v[96:99]
	v_mfma_f32_16x16x32_bf16 v[92:95], v[88:91], v[192:195], v[92:95]
	v_mfma_f32_16x16x32_bf16 v[84:87], v[160:163], v[192:195], v[84:87]
	v_mfma_f32_16x16x32_bf16 v[76:79], v[88:91], v[200:203], v[76:79]
	v_mfma_f32_16x16x32_bf16 v[72:75], v[160:163], v[200:203], v[72:75]
	v_mfma_f32_16x16x32_bf16 v[68:71], v[88:91], v[208:211], v[68:71]
	v_mfma_f32_16x16x32_bf16 v[64:67], v[160:163], v[208:211], v[64:67]
	s_setprio 0
	s_setprio 1
	v_mfma_f32_16x16x32_bf16 v[28:31], v[164:167], v[180:183], v[28:31]
	v_mfma_f32_16x16x32_bf16 v[24:27], v[172:175], v[180:183], v[24:27]
	v_mfma_f32_16x16x32_bf16 v[20:23], v[164:167], v[188:191], v[20:23]
	v_mfma_f32_16x16x32_bf16 v[16:19], v[172:175], v[188:191], v[16:19]
	v_mfma_f32_16x16x32_bf16 v[12:15], v[164:167], v[196:199], v[12:15]
	v_mfma_f32_16x16x32_bf16 v[8:11], v[172:175], v[196:199], v[8:11]
	v_mfma_f32_16x16x32_bf16 v[4:7], v[164:167], v[204:207], v[4:7]
	v_mfma_f32_16x16x32_bf16 v[0:3], v[172:175], v[204:207], v[0:3]
	v_mfma_f32_16x16x32_bf16 v[28:31], v[168:171], v[184:187], v[28:31]
	v_mfma_f32_16x16x32_bf16 v[24:27], v[176:179], v[184:187], v[24:27]
	v_mfma_f32_16x16x32_bf16 v[20:23], v[168:171], v[192:195], v[20:23]
	v_mfma_f32_16x16x32_bf16 v[16:19], v[176:179], v[192:195], v[16:19]
	v_mfma_f32_16x16x32_bf16 v[12:15], v[168:171], v[200:203], v[12:15]
	v_mfma_f32_16x16x32_bf16 v[8:11], v[176:179], v[200:203], v[8:11]
	v_mfma_f32_16x16x32_bf16 v[4:7], v[168:171], v[208:211], v[4:7]
	v_mfma_f32_16x16x32_bf16 v[0:3], v[176:179], v[208:211], v[0:3]
	s_setprio 0
	s_barrier
	s_add_i32 s63, 0, 0x18000
	v_add_u32_e32 v136, s63, v153
	s_add_i32 s69, 0, 0x1c000
	ds_read_b128 v[80:83], v136
	ds_read_b128 v[88:91], v136 offset:1024
	ds_read_b128 v[156:159], v136 offset:2048
	ds_read_b128 v[160:163], v136 offset:3072
	v_add_u32_e32 v136, s69, v153
	ds_read_b128 v[164:167], v136
	ds_read_b128 v[168:171], v136 offset:1024
	ds_read_b128 v[172:175], v136 offset:2048
	ds_read_b128 v[176:179], v136 offset:3072
	s_add_u32 s4, s4, 0x10000
	s_addc_u32 s5, s5, 0
	s_mov_b32 m0, s41
	v_lshl_add_u64 v[220:221], s[4:5], 0, v[138:139]
	ds_read_b128 v[180:183], v155 offset:32768
	ds_read_b128 v[184:187], v155 offset:33792
	ds_read_b128 v[188:191], v155 offset:34816
	ds_read_b128 v[192:195], v155 offset:35840
	ds_read_b128 v[196:199], v155 offset:36864
	ds_read_b128 v[200:203], v155 offset:37888
	ds_read_b128 v[204:207], v155 offset:38912
	ds_read_b128 v[208:211], v155 offset:39936
	global_load_lds_dwordx4 v[220:221], off
	v_lshl_add_u64 v[220:221], s[4:5], 0, v[142:143]
	s_mov_b32 m0, s84
	s_nop 0
	global_load_lds_dwordx4 v[220:221], off
	s_waitcnt vmcnt(8)
	s_waitcnt lgkmcnt(0)
	s_barrier
	s_setprio 1
	s_waitcnt lgkmcnt(0)
	v_mfma_f32_16x16x32_bf16 v[132:135], v[80:83], v[180:183], v[132:135]
	v_mfma_f32_16x16x32_bf16 v[128:131], v[156:159], v[180:183], v[128:131]
	v_mfma_f32_16x16x32_bf16 v[124:127], v[80:83], v[188:191], v[124:127]
	v_mfma_f32_16x16x32_bf16 v[120:123], v[156:159], v[188:191], v[120:123]
	v_mfma_f32_16x16x32_bf16 v[116:119], v[80:83], v[196:199], v[116:119]
	v_mfma_f32_16x16x32_bf16 v[112:115], v[156:159], v[196:199], v[112:115]
	v_mfma_f32_16x16x32_bf16 v[108:111], v[80:83], v[204:207], v[108:111]
	v_mfma_f32_16x16x32_bf16 v[104:107], v[156:159], v[204:207], v[104:107]
	v_mfma_f32_16x16x32_bf16 v[132:135], v[88:91], v[184:187], v[132:135]
	v_mfma_f32_16x16x32_bf16 v[128:131], v[160:163], v[184:187], v[128:131]
	v_mfma_f32_16x16x32_bf16 v[124:127], v[88:91], v[192:195], v[124:127]
	v_mfma_f32_16x16x32_bf16 v[120:123], v[160:163], v[192:195], v[120:123]
	v_mfma_f32_16x16x32_bf16 v[116:119], v[88:91], v[200:203], v[116:119]
	v_mfma_f32_16x16x32_bf16 v[112:115], v[160:163], v[200:203], v[112:115]
	v_mfma_f32_16x16x32_bf16 v[108:111], v[88:91], v[208:211], v[108:111]
	v_mfma_f32_16x16x32_bf16 v[104:107], v[160:163], v[208:211], v[104:107]
	s_setprio 0
	s_setprio 1
	v_mfma_f32_16x16x32_bf16 v[60:63], v[164:167], v[180:183], v[60:63]
	v_mfma_f32_16x16x32_bf16 v[56:59], v[172:175], v[180:183], v[56:59]
	v_mfma_f32_16x16x32_bf16 v[52:55], v[164:167], v[188:191], v[52:55]
	v_mfma_f32_16x16x32_bf16 v[48:51], v[172:175], v[188:191], v[48:51]
	v_mfma_f32_16x16x32_bf16 v[44:47], v[164:167], v[196:199], v[44:47]
	v_mfma_f32_16x16x32_bf16 v[40:43], v[172:175], v[196:199], v[40:43]
	v_mfma_f32_16x16x32_bf16 v[36:39], v[164:167], v[204:207], v[36:39]
	v_mfma_f32_16x16x32_bf16 v[32:35], v[172:175], v[204:207], v[32:35]
	v_mfma_f32_16x16x32_bf16 v[60:63], v[168:171], v[184:187], v[60:63]
	v_mfma_f32_16x16x32_bf16 v[56:59], v[176:179], v[184:187], v[56:59]
	v_mfma_f32_16x16x32_bf16 v[52:55], v[168:171], v[192:195], v[52:55]
	v_mfma_f32_16x16x32_bf16 v[48:51], v[176:179], v[192:195], v[48:51]
	v_mfma_f32_16x16x32_bf16 v[44:47], v[168:171], v[200:203], v[44:47]
	v_mfma_f32_16x16x32_bf16 v[40:43], v[176:179], v[200:203], v[40:43]
	v_mfma_f32_16x16x32_bf16 v[36:39], v[168:171], v[208:211], v[36:39]
	v_mfma_f32_16x16x32_bf16 v[32:35], v[176:179], v[208:211], v[32:35]
	s_setprio 0
	s_barrier
; #define PG8_STAGE(bufoff, gbase, voff) do { _Pragma("unroll") for (int _i = 0; _i < 2; ++_i) \
;         __builtin_amdgcn_global_load_lds((const unsigned*)((const char*)(gbase) + (voff)[_i]), (PG8_LAS unsigned*)(lds + (bufoff) + ldsw + _i * 8192), 16, 0, 0); } while (0)
; #define PG8_STAGE_A(bufoff, gbase, h, nx) do { _Pragma("unroll") for (int _i = 0; _i < 2; ++_i) { \
;         const unsigned vo_ = GA ? ((nx) ? vgn[h][_i] : vgc[h][_i]) : voffA[_i]; \
;         __builtin_amdgcn_global_load_lds((const unsigned*)((const char*)(gbase) + vo_), (PG8_LAS unsigned*)(lds + (bufoff) + ldsw + _i * 8192), 16, 0, 0); } } while (0)
; #define PG8_LDA(dst, b, h) do { _Pragma("unroll") for (int m = 0; m < 4; ++m) _Pragma("unroll") for (int k = 0; k < 2; ++k) dst[m][k] = *(const PG8_LAS bf16x8*)(lds + PG8_SA(b, h) + aoff + m * 2048 + k * 1024); } while (0)
; #define PG8_MMA(ai, bj, At, Bt) do { __builtin_amdgcn_s_setprio(1); _Pragma("unroll") for (int m = 0; m < 4; ++m) _Pragma("unroll") for (int n = 0; n < 2; ++n) _Pragma("unroll") for (int k = 0; k < 2; ++k) \
;         acc[ai][bj][m][n] = __builtin_amdgcn_mfma_f32_16x16x32_bf16(Bt[n][k], At[m][k], acc[ai][bj][m][n], 0, 0, 0); __builtin_amdgcn_s_setprio(0); } while (0)
; #define PG8_WAIT_V(n) asm volatile("s_waitcnt vmcnt(" #n ")" ::: "memory")
; #define PG8_WAIT_L(n) asm volatile("s_waitcnt lgkmcnt(" #n ")" ::: "memory")
; #define PG8_BAR __builtin_amdgcn_s_barrier()
; #define PG8_SCHED __builtin_amdgcn_sched_barrier(0)
; template <class Epi, class Sched>
; __device__ __forceinline__ void gemm_phase(const int WID_, PG8_LAS unsigned char* lds, const Sched& S, const Epi& E) {
;     ...
;             PG8_LDA(At, 1, 1); PG8_STAGE(PG8_SB(1, 0), b3, voffB); PG8_STAGE(PG8_SB(1, 1), b3 + hstepB, voffB); PG8_STAGE_A(PG8_SA(1, 0), a3, 0, last);
;             PG8_WAIT_V(8); PG8_WAIT_L(0); PG8_BAR; PG8_MMA(1, 0, At, B0); PG8_MMA(1, 1, At, B1); PG8_BAR; PG8_SCHED;
;         }
	s_add_i32 s4, s63, s35
	v_lshl_add_u64 v[212:213], v[212:213], 0, s[42:43]
	s_mov_b32 m0, s4
	ds_read_b128 v[180:183], v155 offset:49152
	ds_read_b128 v[184:187], v155 offset:50176
	ds_read_b128 v[188:191], v155 offset:51200
	ds_read_b128 v[192:195], v155 offset:52224
	ds_read_b128 v[196:199], v155 offset:53248
	ds_read_b128 v[200:203], v155 offset:54272
	ds_read_b128 v[204:207], v155 offset:55296
	ds_read_b128 v[208:211], v155 offset:56320
	global_load_lds_dwordx4 v[212:213], off
	s_add_i32 m0, s4, 0x2000
	s_add_u32 s2, s2, 0x10080
	v_lshl_add_u64 v[212:213], v[214:215], 0, s[42:43]
	s_addc_u32 s3, s3, 0
	s_add_i32 s4, s69, s35
	global_load_lds_dwordx4 v[212:213], off
	v_lshl_add_u64 v[212:213], s[2:3], 0, v[140:141]
	s_mov_b32 m0, s4
	s_nop 0
	global_load_lds_dwordx4 v[212:213], off
	v_lshl_add_u64 v[212:213], s[2:3], 0, v[144:145]
	s_add_i32 m0, s4, 0x2000
	s_nop 0
	global_load_lds_dwordx4 v[212:213], off
	v_lshl_add_u64 v[212:213], v[216:217], 0, s[42:43]
	s_mov_b32 m0, s6
	s_nop 0
	global_load_lds_dwordx4 v[212:213], off
	v_lshl_add_u64 v[212:213], v[218:219], 0, s[42:43]
	s_mov_b32 m0, s10
	s_nop 0
	global_load_lds_dwordx4 v[212:213], off
	s_waitcnt vmcnt(8)
	s_waitcnt lgkmcnt(0)
	s_barrier
	s_setprio 1
	s_waitcnt lgkmcnt(0)
	v_mfma_f32_16x16x32_bf16 v[100:103], v[80:83], v[180:183], v[100:103]
	v_mfma_f32_16x16x32_bf16 v[96:99], v[156:159], v[180:183], v[96:99]
	v_mfma_f32_16x16x32_bf16 v[92:95], v[80:83], v[188:191], v[92:95]
	v_mfma_f32_16x16x32_bf16 v[84:87], v[156:159], v[188:191], v[84:87]
	v_mfma_f32_16x16x32_bf16 v[76:79], v[80:83], v[196:199], v[76:79]
	v_mfma_f32_16x16x32_bf16 v[72:75], v[156:159], v[196:199], v[72:75]
	v_mfma_f32_16x16x32_bf16 v[68:71], v[80:83], v[204:207], v[68:71]
	v_mfma_f32_16x16x32_bf16 v[64:67], v[156:159], v[204:207], v[64:67]
	v_mfma_f32_16x16x32_bf16 v[100:103], v[88:91], v[184:187], v[100:103]
	v_mfma_f32_16x16x32_bf16 v[96:99], v[160:163], v[184:187], v[96:99]
	v_mfma_f32_16x16x32_bf16 v[92:95], v[88:91], v[192:195], v[92:95]
	v_mfma_f32_16x16x32_bf16 v[84:87], v[160:163], v[192:195], v[84:87]
	v_mfma_f32_16x16x32_bf16 v[76:79], v[88:91], v[200:203], v[76:79]
	v_mfma_f32_16x16x32_bf16 v[72:75], v[160:163], v[200:203], v[72:75]
	v_mfma_f32_16x16x32_bf16 v[68:71], v[88:91], v[208:211], v[68:71]
	v_mfma_f32_16x16x32_bf16 v[64:67], v[160:163], v[208:211], v[64:67]
	s_setprio 0
	s_setprio 1
	v_mfma_f32_16x16x32_bf16 v[28:31], v[164:167], v[180:183], v[28:31]
	v_mfma_f32_16x16x32_bf16 v[24:27], v[172:175], v[180:183], v[24:27]
	v_mfma_f32_16x16x32_bf16 v[20:23], v[164:167], v[188:191], v[20:23]
	v_mfma_f32_16x16x32_bf16 v[16:19], v[172:175], v[188:191], v[16:19]
	v_mfma_f32_16x16x32_bf16 v[12:15], v[164:167], v[196:199], v[12:15]
	v_mfma_f32_16x16x32_bf16 v[8:11], v[172:175], v[196:199], v[8:11]
	v_mfma_f32_16x16x32_bf16 v[4:7], v[164:167], v[204:207], v[4:7]
	v_mfma_f32_16x16x32_bf16 v[0:3], v[172:175], v[204:207], v[0:3]
	v_mfma_f32_16x16x32_bf16 v[28:31], v[168:171], v[184:187], v[28:31]
	v_mfma_f32_16x16x32_bf16 v[24:27], v[176:179], v[184:187], v[24:27]
	v_mfma_f32_16x16x32_bf16 v[20:23], v[168:171], v[192:195], v[20:23]
	v_mfma_f32_16x16x32_bf16 v[16:19], v[176:179], v[192:195], v[16:19]
	v_mfma_f32_16x16x32_bf16 v[12:15], v[168:171], v[200:203], v[12:15]
	v_mfma_f32_16x16x32_bf16 v[8:11], v[176:179], v[200:203], v[8:11]
	v_mfma_f32_16x16x32_bf16 v[4:7], v[168:171], v[208:211], v[4:7]
	v_mfma_f32_16x16x32_bf16 v[0:3], v[176:179], v[208:211], v[0:3]
	s_setprio 0
	s_add_u32 s0, s0, 0x100
	s_addc_u32 s1, s1, 0
	s_add_u32 s49, s49, 0x100
	s_addc_u32 s51, s51, 0
	s_cmp_ge_i32 s62, s58
	s_mov_b32 s2, s62
	s_barrier
	s_cbranch_scc0 .LBB0_568

; #define PG8_STAGE(bufoff, gbase, voff) do { _Pragma("unroll") for (int _i = 0; _i < 2; ++_i) \
;         __builtin_amdgcn_global_load_lds((const unsigned*)((const char*)(gbase) + (voff)[_i]), (PG8_LAS unsigned*)(lds + (bufoff) + ldsw + _i * 8192), 16, 0, 0); } while (0)
; #define PG8_STAGE_A(bufoff, gbase, h, nx) do { _Pragma("unroll") for (int _i = 0; _i < 2; ++_i) { \
;         const unsigned vo_ = GA ? ((nx) ? vgn[h][_i] : vgc[h][_i]) : voffA[_i]; \
;         __builtin_amdgcn_global_load_lds((const unsigned*)((const char*)(gbase) + vo_), (PG8_LAS unsigned*)(lds + (bufoff) + ldsw + _i * 8192), 16, 0, 0); } } while (0)
; #define PG8_LDA(dst, b, h) do { _Pragma("unroll") for (int m = 0; m < 4; ++m) _Pragma("unroll") for (int k = 0; k < 2; ++k) dst[m][k] = *(const PG8_LAS bf16x8*)(lds + PG8_SA(b, h) + aoff + m * 2048 + k * 1024); } while (0)
; #define PG8_LDB(dst, b, h) do { _Pragma("unroll") for (int n = 0; n < 2; ++n) _Pragma("unroll") for (int k = 0; k < 2; ++k) dst[n][k] = *(const PG8_LAS bf16x8*)(lds + PG8_SB(b, h) + boff + n * 2048 + k * 1024); } while (0)
; #define PG8_WAIT_V(n) asm volatile("s_waitcnt vmcnt(" #n ")" ::: "memory")
; #define PG8_WAIT_L(n) asm volatile("s_waitcnt lgkmcnt(" #n ")" ::: "memory")
; #define PG8_BAR __builtin_amdgcn_s_barrier()
; #define PG8_SCHED __builtin_amdgcn_sched_barrier(0)
; template <class Epi, class Sched>
; __device__ __forceinline__ void gemm_phase(const int WID_, PG8_LAS unsigned char* lds, const Sched& S, const Epi& E) {
;     ...
;         for (int t = 0; t < nt; t += 2) {
;             const bool last = (t == nt - 2);
;             const char* a1 = cA + (size_t)(t + 1) * kstep;
;             const char* a2 = last ? nA : cA + (size_t)(t + 2) * kstep; const char* b2 = last ? nB : cB + (size_t)(t + 2) * kstep;
;             const char* a3 = a2 + kstep; const char* b3 = b2 + kstep;
;             PG8_LDB(B0, 0, 0); PG8_LDB(B1, 0, 1); PG8_SCHED; PG8_LDA(At, 0, 0); PG8_STAGE_A(PG8_SA(1, 1), a1 + hstepA, 1, false);
;             PG8_WAIT_V(8); PG8_WAIT_L(0); PG8_BAR; PG8_MMA(0, 0, At, B0); PG8_MMA(0, 1, At, B1); PG8_BAR; PG8_SCHED;
;             PG8_LDA(At, 0, 1); PG8_STAGE(PG8_SB(0, 0), b2, voffB); PG8_STAGE(PG8_SB(0, 1), b2 + hstepB, voffB); PG8_STAGE_A(PG8_SA(0, 0), a2, 0, last);
;             PG8_WAIT_V(8); PG8_WAIT_L(0); PG8_BAR; PG8_MMA(1, 0, At, B0); PG8_MMA(1, 1, At, B1); PG8_BAR; PG8_SCHED;
.LBB0_1563:
	ds_read_b128 v[146:149], v143
	ds_read_b128 v[150:153], v143 offset:1024
	ds_read_b128 v[154:157], v143 offset:2048
	ds_read_b128 v[158:161], v143 offset:3072
	ds_read_b128 v[162:165], v144
	ds_read_b128 v[166:169], v144 offset:1024
	ds_read_b128 v[170:173], v144 offset:2048
	ds_read_b128 v[174:177], v144 offset:3072
	s_add_u32 s48, s46, 0xfffc0080
	s_addc_u32 s49, s47, -1
	s_cmp_eq_u32 s71, 12
	s_cselect_b32 s51, s37, s49
	s_cselect_b32 s50, s67, s48
	s_cselect_b32 s49, s39, s70
	s_cselect_b32 s48, s68, s69
	v_lshl_add_u64 v[210:211], s[46:47], 0, v[136:137]
	s_add_i32 m0, s52, 0xc000
	ds_read_b128 v[178:181], v145
	ds_read_b128 v[182:185], v145 offset:1024
	ds_read_b128 v[186:189], v145 offset:2048
	ds_read_b128 v[190:193], v145 offset:3072
	ds_read_b128 v[194:197], v145 offset:4096
	ds_read_b128 v[198:201], v145 offset:5120
	ds_read_b128 v[202:205], v145 offset:6144
	ds_read_b128 v[206:209], v145 offset:7168
	global_load_lds_dwordx4 v[210:211], off
	v_lshl_add_u64 v[210:211], s[46:47], 0, v[138:139]
	s_add_i32 m0, s52, 0xe000
	s_nop 0
	global_load_lds_dwordx4 v[210:211], off
	s_waitcnt vmcnt(8)
	s_waitcnt lgkmcnt(0)
	s_barrier
	s_setprio 1
	s_waitcnt lgkmcnt(0)
	v_mfma_f32_16x16x32_bf16 v[124:127], v[146:149], v[178:181], v[124:127]
	v_mfma_f32_16x16x32_bf16 v[120:123], v[154:157], v[178:181], v[120:123]
	v_mfma_f32_16x16x32_bf16 v[116:119], v[146:149], v[186:189], v[116:119]
	v_mfma_f32_16x16x32_bf16 v[112:115], v[154:157], v[186:189], v[112:115]
	v_mfma_f32_16x16x32_bf16 v[100:103], v[146:149], v[194:197], v[100:103]
	v_mfma_f32_16x16x32_bf16 v[96:99], v[154:157], v[194:197], v[96:99]
	v_mfma_f32_16x16x32_bf16 v[84:87], v[146:149], v[202:205], v[84:87]
	v_mfma_f32_16x16x32_bf16 v[80:83], v[154:157], v[202:205], v[80:83]
	v_mfma_f32_16x16x32_bf16 v[124:127], v[150:153], v[182:185], v[124:127]
	v_mfma_f32_16x16x32_bf16 v[120:123], v[158:161], v[182:185], v[120:123]
	v_mfma_f32_16x16x32_bf16 v[116:119], v[150:153], v[190:193], v[116:119]
	v_mfma_f32_16x16x32_bf16 v[112:115], v[158:161], v[190:193], v[112:115]
	v_mfma_f32_16x16x32_bf16 v[100:103], v[150:153], v[198:201], v[100:103]
	v_mfma_f32_16x16x32_bf16 v[96:99], v[158:161], v[198:201], v[96:99]
	v_mfma_f32_16x16x32_bf16 v[84:87], v[150:153], v[206:209], v[84:87]
	v_mfma_f32_16x16x32_bf16 v[80:83], v[158:161], v[206:209], v[80:83]
	s_setprio 0
	s_setprio 1
	v_mfma_f32_16x16x32_bf16 v[108:111], v[162:165], v[178:181], v[108:111]
	v_mfma_f32_16x16x32_bf16 v[104:107], v[170:173], v[178:181], v[104:107]
	v_mfma_f32_16x16x32_bf16 v[92:95], v[162:165], v[186:189], v[92:95]
	v_mfma_f32_16x16x32_bf16 v[88:91], v[170:173], v[186:189], v[88:91]
	v_mfma_f32_16x16x32_bf16 v[76:79], v[162:165], v[194:197], v[76:79]
	v_mfma_f32_16x16x32_bf16 v[72:75], v[170:173], v[194:197], v[72:75]
	v_mfma_f32_16x16x32_bf16 v[68:71], v[162:165], v[202:205], v[68:71]
	v_mfma_f32_16x16x32_bf16 v[64:67], v[170:173], v[202:205], v[64:67]
	v_mfma_f32_16x16x32_bf16 v[108:111], v[166:169], v[182:185], v[108:111]
	v_mfma_f32_16x16x32_bf16 v[104:107], v[174:177], v[182:185], v[104:107]
	v_mfma_f32_16x16x32_bf16 v[92:95], v[166:169], v[190:193], v[92:95]
	v_mfma_f32_16x16x32_bf16 v[88:91], v[174:177], v[190:193], v[88:91]
	v_mfma_f32_16x16x32_bf16 v[76:79], v[166:169], v[198:201], v[76:79]
	v_mfma_f32_16x16x32_bf16 v[72:75], v[174:177], v[198:201], v[72:75]
	v_mfma_f32_16x16x32_bf16 v[68:71], v[166:169], v[206:209], v[68:71]
	v_mfma_f32_16x16x32_bf16 v[64:67], v[174:177], v[206:209], v[64:67]
	s_setprio 0
	s_barrier
	s_add_i32 s76, s63, s33
	v_lshl_add_u64 v[210:211], s[48:49], 0, v[130:131]
	s_mov_b32 m0, s76
	ds_read_b128 v[178:181], v145 offset:16384
	ds_read_b128 v[182:185], v145 offset:17408
	ds_read_b128 v[186:189], v145 offset:18432
	ds_read_b128 v[190:193], v145 offset:19456
	ds_read_b128 v[194:197], v145 offset:20480
	ds_read_b128 v[198:201], v145 offset:21504
	ds_read_b128 v[202:205], v145 offset:22528
	ds_read_b128 v[206:209], v145 offset:23552
	global_load_lds_dwordx4 v[210:211], off
	s_add_i32 m0, s76, 0x2000
	s_add_u32 s76, s48, 0x40000
	v_lshl_add_u64 v[212:213], s[48:49], 0, v[134:135]
	s_addc_u32 s77, s49, 0
	s_add_i32 s78, s66, s33
	global_load_lds_dwordx4 v[212:213], off
	v_lshl_add_u64 v[214:215], s[76:77], 0, v[130:131]
	s_mov_b32 m0, s78
	v_lshl_add_u64 v[216:217], s[50:51], 0, v[132:133]
	global_load_lds_dwordx4 v[214:215], off
	v_lshl_add_u64 v[214:215], s[76:77], 0, v[134:135]
	s_add_i32 m0, s78, 0x2000
	s_nop 0
	global_load_lds_dwordx4 v[214:215], off
	v_lshl_add_u64 v[214:215], s[50:51], 0, v[128:129]
	s_mov_b32 m0, s52
	s_nop 0
	global_load_lds_dwordx4 v[214:215], off
	s_mov_b32 m0, s53
	s_nop 0
	global_load_lds_dwordx4 v[216:217], off
	s_waitcnt vmcnt(8)
	s_waitcnt lgkmcnt(0)
	s_barrier
; #define PG8_STAGE(bufoff, gbase, voff) do { _Pragma("unroll") for (int _i = 0; _i < 2; ++_i) \
;         __builtin_amdgcn_global_load_lds((const unsigned*)((const char*)(gbase) + (voff)[_i]), (PG8_LAS unsigned*)(lds + (bufoff) + ldsw + _i * 8192), 16, 0, 0); } while (0)
; #define PG8_STAGE_A(bufoff, gbase, h, nx) do { _Pragma("unroll") for (int _i = 0; _i < 2; ++_i) { \
;         const unsigned vo_ = GA ? ((nx) ? vgn[h][_i] : vgc[h][_i]) : voffA[_i]; \
;         __builtin_amdgcn_global_load_lds((const unsigned*)((const char*)(gbase) + vo_), (PG8_LAS unsigned*)(lds + (bufoff) + ldsw + _i * 8192), 16, 0, 0); } } while (0)
; #define PG8_LDA(dst, b, h) do { _Pragma("unroll") for (int m = 0; m < 4; ++m) _Pragma("unroll") for (int k = 0; k < 2; ++k) dst[m][k] = *(const PG8_LAS bf16x8*)(lds + PG8_SA(b, h) + aoff + m * 2048 + k * 1024); } while (0)
; #define PG8_LDB(dst, b, h) do { _Pragma("unroll") for (int n = 0; n < 2; ++n) _Pragma("unroll") for (int k = 0; k < 2; ++k) dst[n][k] = *(const PG8_LAS bf16x8*)(lds + PG8_SB(b, h) + boff + n * 2048 + k * 1024); } while (0)
; #define PG8_MMA(ai, bj, At, Bt) do { __builtin_amdgcn_s_setprio(1); _Pragma("unroll") for (int m = 0; m < 4; ++m) _Pragma("unroll") for (int n = 0; n < 2; ++n) _Pragma("unroll") for (int k = 0; k < 2; ++k) \
;         acc[ai][bj][m][n] = __builtin_amdgcn_mfma_f32_16x16x32_bf16(Bt[n][k], At[m][k], acc[ai][bj][m][n], 0, 0, 0); __builtin_amdgcn_s_setprio(0); } while (0)
; #define PG8_WAIT_V(n) asm volatile("s_waitcnt vmcnt(" #n ")" ::: "memory")
; #define PG8_BAR __builtin_amdgcn_s_barrier()
; template <class Epi, class Sched>
; __device__ __forceinline__ void gemm_phase(const int WID_, PG8_LAS unsigned char* lds, const Sched& S, const Epi& E) {
;     ...
;             PG8_WAIT_V(8); PG8_WAIT_L(0); PG8_BAR; PG8_MMA(1, 0, At, B0); PG8_MMA(1, 1, At, B1); PG8_BAR; PG8_SCHED;
;             PG8_LDB(B0, 1, 0); PG8_LDB(B1, 1, 1); PG8_SCHED; PG8_LDA(At, 1, 0); PG8_STAGE_A(PG8_SA(0, 1), a2 + hstepA, 1, last);
;             PG8_WAIT_V(8); PG8_WAIT_L(0); PG8_BAR; PG8_MMA(0, 0, At, B0); PG8_MMA(0, 1, At, B1); PG8_BAR; PG8_SCHED;
;             PG8_LDA(At, 1, 1); PG8_STAGE(PG8_SB(1, 0), b3, voffB); PG8_STAGE(PG8_SB(1, 1), b3 + hstepB, voffB); PG8_STAGE_A(PG8_SA(1, 0), a3, 0, last);
;             PG8_WAIT_V(8); PG8_WAIT_L(0); PG8_BAR; PG8_MMA(1, 0, At, B0); PG8_MMA(1, 1, At, B1); PG8_BAR; PG8_SCHED;
	s_setprio 1
	s_waitcnt lgkmcnt(0)
	v_mfma_f32_16x16x32_bf16 v[60:63], v[146:149], v[178:181], v[60:63]
	v_mfma_f32_16x16x32_bf16 v[56:59], v[154:157], v[178:181], v[56:59]
	v_mfma_f32_16x16x32_bf16 v[52:55], v[146:149], v[186:189], v[52:55]
	v_mfma_f32_16x16x32_bf16 v[48:51], v[154:157], v[186:189], v[48:51]
	v_mfma_f32_16x16x32_bf16 v[36:39], v[146:149], v[194:197], v[36:39]
	v_mfma_f32_16x16x32_bf16 v[32:35], v[154:157], v[194:197], v[32:35]
	v_mfma_f32_16x16x32_bf16 v[20:23], v[146:149], v[202:205], v[20:23]
	v_mfma_f32_16x16x32_bf16 v[16:19], v[154:157], v[202:205], v[16:19]
	v_mfma_f32_16x16x32_bf16 v[60:63], v[150:153], v[182:185], v[60:63]
	v_mfma_f32_16x16x32_bf16 v[56:59], v[158:161], v[182:185], v[56:59]
	v_mfma_f32_16x16x32_bf16 v[52:55], v[150:153], v[190:193], v[52:55]
	v_mfma_f32_16x16x32_bf16 v[48:51], v[158:161], v[190:193], v[48:51]
	v_mfma_f32_16x16x32_bf16 v[36:39], v[150:153], v[198:201], v[36:39]
	v_mfma_f32_16x16x32_bf16 v[32:35], v[158:161], v[198:201], v[32:35]
	v_mfma_f32_16x16x32_bf16 v[20:23], v[150:153], v[206:209], v[20:23]
	v_mfma_f32_16x16x32_bf16 v[16:19], v[158:161], v[206:209], v[16:19]
	s_setprio 0
	s_setprio 1
	v_mfma_f32_16x16x32_bf16 v[44:47], v[162:165], v[178:181], v[44:47]
	v_mfma_f32_16x16x32_bf16 v[40:43], v[170:173], v[178:181], v[40:43]
	v_mfma_f32_16x16x32_bf16 v[28:31], v[162:165], v[186:189], v[28:31]
	v_mfma_f32_16x16x32_bf16 v[24:27], v[170:173], v[186:189], v[24:27]
	v_mfma_f32_16x16x32_bf16 v[12:15], v[162:165], v[194:197], v[12:15]
	v_mfma_f32_16x16x32_bf16 v[8:11], v[170:173], v[194:197], v[8:11]
	v_mfma_f32_16x16x32_bf16 v[4:7], v[162:165], v[202:205], v[4:7]
	v_mfma_f32_16x16x32_bf16 v[0:3], v[170:173], v[202:205], v[0:3]
	v_mfma_f32_16x16x32_bf16 v[44:47], v[166:169], v[182:185], v[44:47]
	v_mfma_f32_16x16x32_bf16 v[40:43], v[174:177], v[182:185], v[40:43]
	v_mfma_f32_16x16x32_bf16 v[28:31], v[166:169], v[190:193], v[28:31]
	v_mfma_f32_16x16x32_bf16 v[24:27], v[174:177], v[190:193], v[24:27]
	v_mfma_f32_16x16x32_bf16 v[12:15], v[166:169], v[198:201], v[12:15]
	v_mfma_f32_16x16x32_bf16 v[8:11], v[174:177], v[198:201], v[8:11]
	v_mfma_f32_16x16x32_bf16 v[4:7], v[166:169], v[206:209], v[4:7]
	v_mfma_f32_16x16x32_bf16 v[0:3], v[174:177], v[206:209], v[0:3]
	s_setprio 0
	s_barrier
	s_add_i32 s76, 0, 0x18000
	s_add_i32 s77, 0, 0x1c000
	v_add_u32_e32 v158, s76, v141
	v_add_u32_e32 v174, s77, v141
	ds_read_b128 v[146:149], v158
	ds_read_b128 v[150:153], v158 offset:1024
	ds_read_b128 v[154:157], v158 offset:2048
	ds_read_b128 v[158:161], v158 offset:3072
	ds_read_b128 v[162:165], v174
	ds_read_b128 v[166:169], v174 offset:1024
	ds_read_b128 v[170:173], v174 offset:2048
	ds_read_b128 v[174:177], v174 offset:3072
	s_add_u32 s50, s50, 0x40000
	s_addc_u32 s51, s51, 0
	s_mov_b32 m0, s58
	v_lshl_add_u64 v[218:219], s[50:51], 0, v[128:129]
	ds_read_b128 v[178:181], v145 offset:32768
	ds_read_b128 v[182:185], v145 offset:33792
	ds_read_b128 v[186:189], v145 offset:34816
	ds_read_b128 v[190:193], v145 offset:35840
	ds_read_b128 v[194:197], v145 offset:36864
	ds_read_b128 v[198:201], v145 offset:37888
	ds_read_b128 v[202:205], v145 offset:38912
	ds_read_b128 v[206:209], v145 offset:39936
	global_load_lds_dwordx4 v[218:219], off
	v_lshl_add_u64 v[218:219], s[50:51], 0, v[132:133]
	s_mov_b32 m0, s59
	s_nop 0
	global_load_lds_dwordx4 v[218:219], off
	s_waitcnt vmcnt(8)
	s_waitcnt lgkmcnt(0)
	s_barrier
	s_setprio 1
	s_waitcnt lgkmcnt(0)
	v_mfma_f32_16x16x32_bf16 v[124:127], v[146:149], v[178:181], v[124:127]
	v_mfma_f32_16x16x32_bf16 v[120:123], v[154:157], v[178:181], v[120:123]
	v_mfma_f32_16x16x32_bf16 v[116:119], v[146:149], v[186:189], v[116:119]
	v_mfma_f32_16x16x32_bf16 v[112:115], v[154:157], v[186:189], v[112:115]
	v_mfma_f32_16x16x32_bf16 v[100:103], v[146:149], v[194:197], v[100:103]
	v_mfma_f32_16x16x32_bf16 v[96:99], v[154:157], v[194:197], v[96:99]
	v_mfma_f32_16x16x32_bf16 v[84:87], v[146:149], v[202:205], v[84:87]
	v_mfma_f32_16x16x32_bf16 v[80:83], v[154:157], v[202:205], v[80:83]
	v_mfma_f32_16x16x32_bf16 v[124:127], v[150:153], v[182:185], v[124:127]
	v_mfma_f32_16x16x32_bf16 v[120:123], v[158:161], v[182:185], v[120:123]
	v_mfma_f32_16x16x32_bf16 v[116:119], v[150:153], v[190:193], v[116:119]
	v_mfma_f32_16x16x32_bf16 v[112:115], v[158:161], v[190:193], v[112:115]
	v_mfma_f32_16x16x32_bf16 v[100:103], v[150:153], v[198:201], v[100:103]
	v_mfma_f32_16x16x32_bf16 v[96:99], v[158:161], v[198:201], v[96:99]
	v_mfma_f32_16x16x32_bf16 v[84:87], v[150:153], v[206:209], v[84:87]
	v_mfma_f32_16x16x32_bf16 v[80:83], v[158:161], v[206:209], v[80:83]
	s_setprio 0
	s_setprio 1
	v_mfma_f32_16x16x32_bf16 v[108:111], v[162:165], v[178:181], v[108:111]
	v_mfma_f32_16x16x32_bf16 v[104:107], v[170:173], v[178:181], v[104:107]
	v_mfma_f32_16x16x32_bf16 v[92:95], v[162:165], v[186:189], v[92:95]
	v_mfma_f32_16x16x32_bf16 v[88:91], v[170:173], v[186:189], v[88:91]
	v_mfma_f32_16x16x32_bf16 v[76:79], v[162:165], v[194:197], v[76:79]
	v_mfma_f32_16x16x32_bf16 v[72:75], v[170:173], v[194:197], v[72:75]
	v_mfma_f32_16x16x32_bf16 v[68:71], v[162:165], v[202:205], v[68:71]
	v_mfma_f32_16x16x32_bf16 v[64:67], v[170:173], v[202:205], v[64:67]
	v_mfma_f32_16x16x32_bf16 v[108:111], v[166:169], v[182:185], v[108:111]
	v_mfma_f32_16x16x32_bf16 v[104:107], v[174:177], v[182:185], v[104:107]
	v_mfma_f32_16x16x32_bf16 v[92:95], v[166:169], v[190:193], v[92:95]
	v_mfma_f32_16x16x32_bf16 v[88:91], v[174:177], v[190:193], v[88:91]
	v_mfma_f32_16x16x32_bf16 v[76:79], v[166:169], v[198:201], v[76:79]
	v_mfma_f32_16x16x32_bf16 v[72:75], v[174:177], v[198:201], v[72:75]
	v_mfma_f32_16x16x32_bf16 v[68:71], v[166:169], v[206:209], v[68:71]
	v_mfma_f32_16x16x32_bf16 v[64:67], v[174:177], v[206:209], v[64:67]
	s_setprio 0
	s_barrier
; #define PG8_STAGE(bufoff, gbase, voff) do { _Pragma("unroll") for (int _i = 0; _i < 2; ++_i) \
;         __builtin_amdgcn_global_load_lds((const unsigned*)((const char*)(gbase) + (voff)[_i]), (PG8_LAS unsigned*)(lds + (bufoff) + ldsw + _i * 8192), 16, 0, 0); } while (0)
; #define PG8_STAGE_A(bufoff, gbase, h, nx) do { _Pragma("unroll") for (int _i = 0; _i < 2; ++_i) { \
;         const unsigned vo_ = GA ? ((nx) ? vgn[h][_i] : vgc[h][_i]) : voffA[_i]; \
;         __builtin_amdgcn_global_load_lds((const unsigned*)((const char*)(gbase) + vo_), (PG8_LAS unsigned*)(lds + (bufoff) + ldsw + _i * 8192), 16, 0, 0); } } while (0)
; #define PG8_LDA(dst, b, h) do { _Pragma("unroll") for (int m = 0; m < 4; ++m) _Pragma("unroll") for (int k = 0; k < 2; ++k) dst[m][k] = *(const PG8_LAS bf16x8*)(lds + PG8_SA(b, h) + aoff + m * 2048 + k * 1024); } while (0)
; #define PG8_MMA(ai, bj, At, Bt) do { __builtin_amdgcn_s_setprio(1); _Pragma("unroll") for (int m = 0; m < 4; ++m) _Pragma("unroll") for (int n = 0; n < 2; ++n) _Pragma("unroll") for (int k = 0; k < 2; ++k) \
;         acc[ai][bj][m][n] = __builtin_amdgcn_mfma_f32_16x16x32_bf16(Bt[n][k], At[m][k], acc[ai][bj][m][n], 0, 0, 0); __builtin_amdgcn_s_setprio(0); } while (0)
; #define PG8_WAIT_V(n) asm volatile("s_waitcnt vmcnt(" #n ")" ::: "memory")
; #define PG8_WAIT_L(n) asm volatile("s_waitcnt lgkmcnt(" #n ")" ::: "memory")
; #define PG8_BAR __builtin_amdgcn_s_barrier()
; #define PG8_SCHED __builtin_amdgcn_sched_barrier(0)
; template <class Epi, class Sched>
; __device__ __forceinline__ void gemm_phase(const int WID_, PG8_LAS unsigned char* lds, const Sched& S, const Epi& E) {
;     ...
;             PG8_LDA(At, 1, 1); PG8_STAGE(PG8_SB(1, 0), b3, voffB); PG8_STAGE(PG8_SB(1, 1), b3 + hstepB, voffB); PG8_STAGE_A(PG8_SA(1, 0), a3, 0, last);
;             PG8_WAIT_V(8); PG8_WAIT_L(0); PG8_BAR; PG8_MMA(1, 0, At, B0); PG8_MMA(1, 1, At, B1); PG8_BAR; PG8_SCHED;
;         }
	s_add_i32 s50, s76, s33
	v_lshl_add_u64 v[210:211], v[210:211], 0, s[4:5]
	s_mov_b32 m0, s50
	ds_read_b128 v[178:181], v145 offset:49152
	ds_read_b128 v[182:185], v145 offset:50176
	ds_read_b128 v[186:189], v145 offset:51200
	ds_read_b128 v[190:193], v145 offset:52224
	ds_read_b128 v[194:197], v145 offset:53248
	ds_read_b128 v[198:201], v145 offset:54272
	ds_read_b128 v[202:205], v145 offset:55296
	ds_read_b128 v[206:209], v145 offset:56320
	global_load_lds_dwordx4 v[210:211], off
	s_add_i32 m0, s50, 0x2000
	s_add_u32 s48, s48, 0x40080
	v_lshl_add_u64 v[210:211], v[212:213], 0, s[4:5]
	s_addc_u32 s49, s49, 0
	s_add_i32 s50, s77, s33
	global_load_lds_dwordx4 v[210:211], off
	v_lshl_add_u64 v[210:211], s[48:49], 0, v[130:131]
	s_mov_b32 m0, s50
	s_nop 0
	global_load_lds_dwordx4 v[210:211], off
	v_lshl_add_u64 v[210:211], s[48:49], 0, v[134:135]
	s_add_i32 m0, s50, 0x2000
	s_nop 0
	global_load_lds_dwordx4 v[210:211], off
	v_lshl_add_u64 v[210:211], v[214:215], 0, s[4:5]
	s_mov_b32 m0, s60
	s_nop 0
	global_load_lds_dwordx4 v[210:211], off
	v_lshl_add_u64 v[210:211], v[216:217], 0, s[4:5]
	s_mov_b32 m0, s61
	s_nop 0
	global_load_lds_dwordx4 v[210:211], off
	s_waitcnt vmcnt(8)
	s_waitcnt lgkmcnt(0)
	s_barrier
	s_setprio 1
	s_waitcnt lgkmcnt(0)
	v_mfma_f32_16x16x32_bf16 v[60:63], v[146:149], v[178:181], v[60:63]
	v_mfma_f32_16x16x32_bf16 v[56:59], v[154:157], v[178:181], v[56:59]
	v_mfma_f32_16x16x32_bf16 v[52:55], v[146:149], v[186:189], v[52:55]
	v_mfma_f32_16x16x32_bf16 v[48:51], v[154:157], v[186:189], v[48:51]
	v_mfma_f32_16x16x32_bf16 v[36:39], v[146:149], v[194:197], v[36:39]
	v_mfma_f32_16x16x32_bf16 v[32:35], v[154:157], v[194:197], v[32:35]
	v_mfma_f32_16x16x32_bf16 v[20:23], v[146:149], v[202:205], v[20:23]
	v_mfma_f32_16x16x32_bf16 v[16:19], v[154:157], v[202:205], v[16:19]
	v_mfma_f32_16x16x32_bf16 v[60:63], v[150:153], v[182:185], v[60:63]
	v_mfma_f32_16x16x32_bf16 v[56:59], v[158:161], v[182:185], v[56:59]
	v_mfma_f32_16x16x32_bf16 v[52:55], v[150:153], v[190:193], v[52:55]
	v_mfma_f32_16x16x32_bf16 v[48:51], v[158:161], v[190:193], v[48:51]
	v_mfma_f32_16x16x32_bf16 v[36:39], v[150:153], v[198:201], v[36:39]
	v_mfma_f32_16x16x32_bf16 v[32:35], v[158:161], v[198:201], v[32:35]
	v_mfma_f32_16x16x32_bf16 v[20:23], v[150:153], v[206:209], v[20:23]
	v_mfma_f32_16x16x32_bf16 v[16:19], v[158:161], v[206:209], v[16:19]
	s_setprio 0
	s_setprio 1
	v_mfma_f32_16x16x32_bf16 v[44:47], v[162:165], v[178:181], v[44:47]
	v_mfma_f32_16x16x32_bf16 v[40:43], v[170:173], v[178:181], v[40:43]
	v_mfma_f32_16x16x32_bf16 v[28:31], v[162:165], v[186:189], v[28:31]
	v_mfma_f32_16x16x32_bf16 v[24:27], v[170:173], v[186:189], v[24:27]
	v_mfma_f32_16x16x32_bf16 v[12:15], v[162:165], v[194:197], v[12:15]
	v_mfma_f32_16x16x32_bf16 v[8:11], v[170:173], v[194:197], v[8:11]
	v_mfma_f32_16x16x32_bf16 v[4:7], v[162:165], v[202:205], v[4:7]
	v_mfma_f32_16x16x32_bf16 v[0:3], v[170:173], v[202:205], v[0:3]
	v_mfma_f32_16x16x32_bf16 v[44:47], v[166:169], v[182:185], v[44:47]
	v_mfma_f32_16x16x32_bf16 v[40:43], v[174:177], v[182:185], v[40:43]
	v_mfma_f32_16x16x32_bf16 v[28:31], v[166:169], v[190:193], v[28:31]
	v_mfma_f32_16x16x32_bf16 v[24:27], v[174:177], v[190:193], v[24:27]
	v_mfma_f32_16x16x32_bf16 v[12:15], v[166:169], v[198:201], v[12:15]
	v_mfma_f32_16x16x32_bf16 v[8:11], v[174:177], v[198:201], v[8:11]
	v_mfma_f32_16x16x32_bf16 v[4:7], v[166:169], v[206:209], v[4:7]
	v_mfma_f32_16x16x32_bf16 v[0:3], v[174:177], v[206:209], v[0:3]
	s_setprio 0
	s_add_i32 s71, s71, 2
	s_add_u32 s46, s46, 0x100
	s_addc_u32 s47, s47, 0
	s_add_u32 s69, s69, 0x100
	s_addc_u32 s70, s70, 0
	s_cmp_gt_u32 s71, 13
	s_barrier
	s_cbranch_scc0 .LBB0_1563
	s_and_b64 vcc, exec, s[18:19]
	s_cbranch_vccz .LBB0_1566
	s_barrier

; #define PG8_STAGE(bufoff, gbase, voff) do { _Pragma("unroll") for (int _i = 0; _i < 2; ++_i) \
;         __builtin_amdgcn_global_load_lds((const unsigned*)((const char*)(gbase) + (voff)[_i]), (PG8_LAS unsigned*)(lds + (bufoff) + ldsw + _i * 8192), 16, 0, 0); } while (0)
; #define PG8_STAGE_A(bufoff, gbase, h, nx) do { _Pragma("unroll") for (int _i = 0; _i < 2; ++_i) { \
;         const unsigned vo_ = GA ? ((nx) ? vgn[h][_i] : vgc[h][_i]) : voffA[_i]; \
;         __builtin_amdgcn_global_load_lds((const unsigned*)((const char*)(gbase) + vo_), (PG8_LAS unsigned*)(lds + (bufoff) + ldsw + _i * 8192), 16, 0, 0); } } while (0)
; #define PG8_LDA(dst, b, h) do { _Pragma("unroll") for (int m = 0; m < 4; ++m) _Pragma("unroll") for (int k = 0; k < 2; ++k) dst[m][k] = *(const PG8_LAS bf16x8*)(lds + PG8_SA(b, h) + aoff + m * 2048 + k * 1024); } while (0)
; #define PG8_LDB(dst, b, h) do { _Pragma("unroll") for (int n = 0; n < 2; ++n) _Pragma("unroll") for (int k = 0; k < 2; ++k) dst[n][k] = *(const PG8_LAS bf16x8*)(lds + PG8_SB(b, h) + boff + n * 2048 + k * 1024); } while (0)
; #define PG8_WAIT_V(n) asm volatile("s_waitcnt vmcnt(" #n ")" ::: "memory")
; #define PG8_WAIT_L(n) asm volatile("s_waitcnt lgkmcnt(" #n ")" ::: "memory")
; #define PG8_BAR __builtin_amdgcn_s_barrier()
; #define PG8_SCHED __builtin_amdgcn_sched_barrier(0)
; template <class Epi, class Sched>
; __device__ __forceinline__ void gemm_phase(const int WID_, PG8_LAS unsigned char* lds, const Sched& S, const Epi& E) {
;     ...
;         for (int t = 0; t < nt; t += 2) {
;             const bool last = (t == nt - 2);
;             const char* a1 = cA + (size_t)(t + 1) * kstep;
;             const char* a2 = last ? nA : cA + (size_t)(t + 2) * kstep; const char* b2 = last ? nB : cB + (size_t)(t + 2) * kstep;
;             const char* a3 = a2 + kstep; const char* b3 = b2 + kstep;
;             PG8_LDB(B0, 0, 0); PG8_LDB(B1, 0, 1); PG8_SCHED; PG8_LDA(At, 0, 0); PG8_STAGE_A(PG8_SA(1, 1), a1 + hstepA, 1, false);
;             PG8_WAIT_V(8); PG8_WAIT_L(0); PG8_BAR; PG8_MMA(0, 0, At, B0); PG8_MMA(0, 1, At, B1); PG8_BAR; PG8_SCHED;
;             PG8_LDA(At, 0, 1); PG8_STAGE(PG8_SB(0, 0), b2, voffB); PG8_STAGE(PG8_SB(0, 1), b2 + hstepB, voffB); PG8_STAGE_A(PG8_SA(0, 0), a2, 0, last);
;             PG8_WAIT_V(8); PG8_WAIT_L(0); PG8_BAR; PG8_MMA(1, 0, At, B0); PG8_MMA(1, 1, At, B1); PG8_BAR; PG8_SCHED;
.LBB0_1786:
	ds_read_b128 v[146:149], v143
	ds_read_b128 v[150:153], v143 offset:1024
	ds_read_b128 v[154:157], v143 offset:2048
	ds_read_b128 v[158:161], v143 offset:3072
	ds_read_b128 v[162:165], v144
	ds_read_b128 v[166:169], v144 offset:1024
	ds_read_b128 v[170:173], v144 offset:2048
	ds_read_b128 v[174:177], v144 offset:3072
	s_add_u32 s44, s42, 0xfffc0080
	s_addc_u32 s45, s43, -1
	s_cmp_eq_u32 s67, 12
	s_cselect_b32 s47, s37, s45
	s_cselect_b32 s46, s61, s44
	s_cselect_b32 s45, s23, s66
	s_cselect_b32 s44, s62, s63
	v_lshl_add_u64 v[210:211], s[42:43], 0, v[136:137]
	s_add_i32 m0, s33, 0xc000
	ds_read_b128 v[178:181], v145
	ds_read_b128 v[182:185], v145 offset:1024
	ds_read_b128 v[186:189], v145 offset:2048
	ds_read_b128 v[190:193], v145 offset:3072
	ds_read_b128 v[194:197], v145 offset:4096
	ds_read_b128 v[198:201], v145 offset:5120
	ds_read_b128 v[202:205], v145 offset:6144
	ds_read_b128 v[206:209], v145 offset:7168
	global_load_lds_dwordx4 v[210:211], off
	v_lshl_add_u64 v[210:211], s[42:43], 0, v[138:139]
	s_add_i32 m0, s33, 0xe000
	s_nop 0
	global_load_lds_dwordx4 v[210:211], off
	s_waitcnt vmcnt(8)
	s_waitcnt lgkmcnt(0)
	s_barrier
	s_setprio 1
	s_waitcnt lgkmcnt(0)
	v_mfma_f32_16x16x32_bf16 v[124:127], v[146:149], v[178:181], v[124:127]
	v_mfma_f32_16x16x32_bf16 v[120:123], v[154:157], v[178:181], v[120:123]
	v_mfma_f32_16x16x32_bf16 v[116:119], v[146:149], v[186:189], v[116:119]
	v_mfma_f32_16x16x32_bf16 v[112:115], v[154:157], v[186:189], v[112:115]
	v_mfma_f32_16x16x32_bf16 v[100:103], v[146:149], v[194:197], v[100:103]
	v_mfma_f32_16x16x32_bf16 v[96:99], v[154:157], v[194:197], v[96:99]
	v_mfma_f32_16x16x32_bf16 v[84:87], v[146:149], v[202:205], v[84:87]
	v_mfma_f32_16x16x32_bf16 v[80:83], v[154:157], v[202:205], v[80:83]
	v_mfma_f32_16x16x32_bf16 v[124:127], v[150:153], v[182:185], v[124:127]
	v_mfma_f32_16x16x32_bf16 v[120:123], v[158:161], v[182:185], v[120:123]
	v_mfma_f32_16x16x32_bf16 v[116:119], v[150:153], v[190:193], v[116:119]
	v_mfma_f32_16x16x32_bf16 v[112:115], v[158:161], v[190:193], v[112:115]
	v_mfma_f32_16x16x32_bf16 v[100:103], v[150:153], v[198:201], v[100:103]
	v_mfma_f32_16x16x32_bf16 v[96:99], v[158:161], v[198:201], v[96:99]
	v_mfma_f32_16x16x32_bf16 v[84:87], v[150:153], v[206:209], v[84:87]
	v_mfma_f32_16x16x32_bf16 v[80:83], v[158:161], v[206:209], v[80:83]
	s_setprio 0
	s_setprio 1
	v_mfma_f32_16x16x32_bf16 v[108:111], v[162:165], v[178:181], v[108:111]
	v_mfma_f32_16x16x32_bf16 v[104:107], v[170:173], v[178:181], v[104:107]
	v_mfma_f32_16x16x32_bf16 v[92:95], v[162:165], v[186:189], v[92:95]
	v_mfma_f32_16x16x32_bf16 v[88:91], v[170:173], v[186:189], v[88:91]
	v_mfma_f32_16x16x32_bf16 v[76:79], v[162:165], v[194:197], v[76:79]
	v_mfma_f32_16x16x32_bf16 v[72:75], v[170:173], v[194:197], v[72:75]
	v_mfma_f32_16x16x32_bf16 v[68:71], v[162:165], v[202:205], v[68:71]
	v_mfma_f32_16x16x32_bf16 v[64:67], v[170:173], v[202:205], v[64:67]
	v_mfma_f32_16x16x32_bf16 v[108:111], v[166:169], v[182:185], v[108:111]
	v_mfma_f32_16x16x32_bf16 v[104:107], v[174:177], v[182:185], v[104:107]
	v_mfma_f32_16x16x32_bf16 v[92:95], v[166:169], v[190:193], v[92:95]
	v_mfma_f32_16x16x32_bf16 v[88:91], v[174:177], v[190:193], v[88:91]
	v_mfma_f32_16x16x32_bf16 v[76:79], v[166:169], v[198:201], v[76:79]
	v_mfma_f32_16x16x32_bf16 v[72:75], v[174:177], v[198:201], v[72:75]
	v_mfma_f32_16x16x32_bf16 v[68:71], v[166:169], v[206:209], v[68:71]
	v_mfma_f32_16x16x32_bf16 v[64:67], v[174:177], v[206:209], v[64:67]
	s_setprio 0
	s_barrier
	s_add_i32 s68, s59, s9
	v_lshl_add_u64 v[210:211], s[44:45], 0, v[130:131]
	s_mov_b32 m0, s68
	ds_read_b128 v[178:181], v145 offset:16384
	ds_read_b128 v[182:185], v145 offset:17408
	ds_read_b128 v[186:189], v145 offset:18432
	ds_read_b128 v[190:193], v145 offset:19456
	ds_read_b128 v[194:197], v145 offset:20480
	ds_read_b128 v[198:201], v145 offset:21504
	ds_read_b128 v[202:205], v145 offset:22528
	ds_read_b128 v[206:209], v145 offset:23552
	global_load_lds_dwordx4 v[210:211], off
	s_add_i32 m0, s68, 0x2000
	s_add_u32 s68, s44, 0x40000
	v_lshl_add_u64 v[212:213], s[44:45], 0, v[134:135]
	s_addc_u32 s69, s45, 0
	s_add_i32 s70, s60, s9
	global_load_lds_dwordx4 v[212:213], off
	v_lshl_add_u64 v[214:215], s[68:69], 0, v[130:131]
	s_mov_b32 m0, s70
	v_lshl_add_u64 v[216:217], s[46:47], 0, v[132:133]
	global_load_lds_dwordx4 v[214:215], off
	v_lshl_add_u64 v[214:215], s[68:69], 0, v[134:135]
	s_add_i32 m0, s70, 0x2000
	s_nop 0
	global_load_lds_dwordx4 v[214:215], off
	v_lshl_add_u64 v[214:215], s[46:47], 0, v[128:129]
	s_mov_b32 m0, s33
	s_nop 0
	global_load_lds_dwordx4 v[214:215], off
	s_mov_b32 m0, s48
	s_nop 0
	global_load_lds_dwordx4 v[216:217], off
	s_waitcnt vmcnt(8)
	s_waitcnt lgkmcnt(0)
	s_barrier
; #define PG8_STAGE(bufoff, gbase, voff) do { _Pragma("unroll") for (int _i = 0; _i < 2; ++_i) \
;         __builtin_amdgcn_global_load_lds((const unsigned*)((const char*)(gbase) + (voff)[_i]), (PG8_LAS unsigned*)(lds + (bufoff) + ldsw + _i * 8192), 16, 0, 0); } while (0)
; #define PG8_STAGE_A(bufoff, gbase, h, nx) do { _Pragma("unroll") for (int _i = 0; _i < 2; ++_i) { \
;         const unsigned vo_ = GA ? ((nx) ? vgn[h][_i] : vgc[h][_i]) : voffA[_i]; \
;         __builtin_amdgcn_global_load_lds((const unsigned*)((const char*)(gbase) + vo_), (PG8_LAS unsigned*)(lds + (bufoff) + ldsw + _i * 8192), 16, 0, 0); } } while (0)
; #define PG8_LDA(dst, b, h) do { _Pragma("unroll") for (int m = 0; m < 4; ++m) _Pragma("unroll") for (int k = 0; k < 2; ++k) dst[m][k] = *(const PG8_LAS bf16x8*)(lds + PG8_SA(b, h) + aoff + m * 2048 + k * 1024); } while (0)
; #define PG8_LDB(dst, b, h) do { _Pragma("unroll") for (int n = 0; n < 2; ++n) _Pragma("unroll") for (int k = 0; k < 2; ++k) dst[n][k] = *(const PG8_LAS bf16x8*)(lds + PG8_SB(b, h) + boff + n * 2048 + k * 1024); } while (0)
; #define PG8_MMA(ai, bj, At, Bt) do { __builtin_amdgcn_s_setprio(1); _Pragma("unroll") for (int m = 0; m < 4; ++m) _Pragma("unroll") for (int n = 0; n < 2; ++n) _Pragma("unroll") for (int k = 0; k < 2; ++k) \
;         acc[ai][bj][m][n] = __builtin_amdgcn_mfma_f32_16x16x32_bf16(Bt[n][k], At[m][k], acc[ai][bj][m][n], 0, 0, 0); __builtin_amdgcn_s_setprio(0); } while (0)
; #define PG8_WAIT_V(n) asm volatile("s_waitcnt vmcnt(" #n ")" ::: "memory")
; #define PG8_BAR __builtin_amdgcn_s_barrier()
; template <class Epi, class Sched>
; __device__ __forceinline__ void gemm_phase(const int WID_, PG8_LAS unsigned char* lds, const Sched& S, const Epi& E) {
;     ...
;             PG8_WAIT_V(8); PG8_WAIT_L(0); PG8_BAR; PG8_MMA(1, 0, At, B0); PG8_MMA(1, 1, At, B1); PG8_BAR; PG8_SCHED;
;             PG8_LDB(B0, 1, 0); PG8_LDB(B1, 1, 1); PG8_SCHED; PG8_LDA(At, 1, 0); PG8_STAGE_A(PG8_SA(0, 1), a2 + hstepA, 1, last);
;             PG8_WAIT_V(8); PG8_WAIT_L(0); PG8_BAR; PG8_MMA(0, 0, At, B0); PG8_MMA(0, 1, At, B1); PG8_BAR; PG8_SCHED;
;             PG8_LDA(At, 1, 1); PG8_STAGE(PG8_SB(1, 0), b3, voffB); PG8_STAGE(PG8_SB(1, 1), b3 + hstepB, voffB); PG8_STAGE_A(PG8_SA(1, 0), a3, 0, last);
;             PG8_WAIT_V(8); PG8_WAIT_L(0); PG8_BAR; PG8_MMA(1, 0, At, B0); PG8_MMA(1, 1, At, B1); PG8_BAR; PG8_SCHED;
	s_setprio 1
	s_waitcnt lgkmcnt(0)
	v_mfma_f32_16x16x32_bf16 v[60:63], v[146:149], v[178:181], v[60:63]
	v_mfma_f32_16x16x32_bf16 v[56:59], v[154:157], v[178:181], v[56:59]
	v_mfma_f32_16x16x32_bf16 v[52:55], v[146:149], v[186:189], v[52:55]
	v_mfma_f32_16x16x32_bf16 v[48:51], v[154:157], v[186:189], v[48:51]
	v_mfma_f32_16x16x32_bf16 v[36:39], v[146:149], v[194:197], v[36:39]
	v_mfma_f32_16x16x32_bf16 v[32:35], v[154:157], v[194:197], v[32:35]
	v_mfma_f32_16x16x32_bf16 v[20:23], v[146:149], v[202:205], v[20:23]
	v_mfma_f32_16x16x32_bf16 v[16:19], v[154:157], v[202:205], v[16:19]
	v_mfma_f32_16x16x32_bf16 v[60:63], v[150:153], v[182:185], v[60:63]
	v_mfma_f32_16x16x32_bf16 v[56:59], v[158:161], v[182:185], v[56:59]
	v_mfma_f32_16x16x32_bf16 v[52:55], v[150:153], v[190:193], v[52:55]
	v_mfma_f32_16x16x32_bf16 v[48:51], v[158:161], v[190:193], v[48:51]
	v_mfma_f32_16x16x32_bf16 v[36:39], v[150:153], v[198:201], v[36:39]
	v_mfma_f32_16x16x32_bf16 v[32:35], v[158:161], v[198:201], v[32:35]
	v_mfma_f32_16x16x32_bf16 v[20:23], v[150:153], v[206:209], v[20:23]
	v_mfma_f32_16x16x32_bf16 v[16:19], v[158:161], v[206:209], v[16:19]
	s_setprio 0
	s_setprio 1
	v_mfma_f32_16x16x32_bf16 v[44:47], v[162:165], v[178:181], v[44:47]
	v_mfma_f32_16x16x32_bf16 v[40:43], v[170:173], v[178:181], v[40:43]
	v_mfma_f32_16x16x32_bf16 v[28:31], v[162:165], v[186:189], v[28:31]
	v_mfma_f32_16x16x32_bf16 v[24:27], v[170:173], v[186:189], v[24:27]
	v_mfma_f32_16x16x32_bf16 v[12:15], v[162:165], v[194:197], v[12:15]
	v_mfma_f32_16x16x32_bf16 v[8:11], v[170:173], v[194:197], v[8:11]
	v_mfma_f32_16x16x32_bf16 v[4:7], v[162:165], v[202:205], v[4:7]
	v_mfma_f32_16x16x32_bf16 v[0:3], v[170:173], v[202:205], v[0:3]
	v_mfma_f32_16x16x32_bf16 v[44:47], v[166:169], v[182:185], v[44:47]
	v_mfma_f32_16x16x32_bf16 v[40:43], v[174:177], v[182:185], v[40:43]
	v_mfma_f32_16x16x32_bf16 v[28:31], v[166:169], v[190:193], v[28:31]
	v_mfma_f32_16x16x32_bf16 v[24:27], v[174:177], v[190:193], v[24:27]
	v_mfma_f32_16x16x32_bf16 v[12:15], v[166:169], v[198:201], v[12:15]
	v_mfma_f32_16x16x32_bf16 v[8:11], v[174:177], v[198:201], v[8:11]
	v_mfma_f32_16x16x32_bf16 v[4:7], v[166:169], v[206:209], v[4:7]
	v_mfma_f32_16x16x32_bf16 v[0:3], v[174:177], v[206:209], v[0:3]
	s_setprio 0
	s_barrier
	s_add_i32 s68, 0, 0x18000
	s_add_i32 s69, 0, 0x1c000
	v_add_u32_e32 v158, s68, v141
	v_add_u32_e32 v174, s69, v141
	ds_read_b128 v[146:149], v158
	ds_read_b128 v[150:153], v158 offset:1024
	ds_read_b128 v[154:157], v158 offset:2048
	ds_read_b128 v[158:161], v158 offset:3072
	ds_read_b128 v[162:165], v174
	ds_read_b128 v[166:169], v174 offset:1024
	ds_read_b128 v[170:173], v174 offset:2048
	ds_read_b128 v[174:177], v174 offset:3072
	s_add_u32 s46, s46, 0x40000
	s_addc_u32 s47, s47, 0
	s_mov_b32 m0, s49
	v_lshl_add_u64 v[218:219], s[46:47], 0, v[128:129]
	ds_read_b128 v[178:181], v145 offset:32768
	ds_read_b128 v[182:185], v145 offset:33792
	ds_read_b128 v[186:189], v145 offset:34816
	ds_read_b128 v[190:193], v145 offset:35840
	ds_read_b128 v[194:197], v145 offset:36864
	ds_read_b128 v[198:201], v145 offset:37888
	ds_read_b128 v[202:205], v145 offset:38912
	ds_read_b128 v[206:209], v145 offset:39936
	global_load_lds_dwordx4 v[218:219], off
	v_lshl_add_u64 v[218:219], s[46:47], 0, v[132:133]
	s_mov_b32 m0, s50
	s_nop 0
	global_load_lds_dwordx4 v[218:219], off
	s_waitcnt vmcnt(8)
	s_waitcnt lgkmcnt(0)
	s_barrier
	s_setprio 1
	s_waitcnt lgkmcnt(0)
	v_mfma_f32_16x16x32_bf16 v[124:127], v[146:149], v[178:181], v[124:127]
	v_mfma_f32_16x16x32_bf16 v[120:123], v[154:157], v[178:181], v[120:123]
	v_mfma_f32_16x16x32_bf16 v[116:119], v[146:149], v[186:189], v[116:119]
	v_mfma_f32_16x16x32_bf16 v[112:115], v[154:157], v[186:189], v[112:115]
	v_mfma_f32_16x16x32_bf16 v[100:103], v[146:149], v[194:197], v[100:103]
	v_mfma_f32_16x16x32_bf16 v[96:99], v[154:157], v[194:197], v[96:99]
	v_mfma_f32_16x16x32_bf16 v[84:87], v[146:149], v[202:205], v[84:87]
	v_mfma_f32_16x16x32_bf16 v[80:83], v[154:157], v[202:205], v[80:83]
	v_mfma_f32_16x16x32_bf16 v[124:127], v[150:153], v[182:185], v[124:127]
	v_mfma_f32_16x16x32_bf16 v[120:123], v[158:161], v[182:185], v[120:123]
	v_mfma_f32_16x16x32_bf16 v[116:119], v[150:153], v[190:193], v[116:119]
	v_mfma_f32_16x16x32_bf16 v[112:115], v[158:161], v[190:193], v[112:115]
	v_mfma_f32_16x16x32_bf16 v[100:103], v[150:153], v[198:201], v[100:103]
	v_mfma_f32_16x16x32_bf16 v[96:99], v[158:161], v[198:201], v[96:99]
	v_mfma_f32_16x16x32_bf16 v[84:87], v[150:153], v[206:209], v[84:87]
	v_mfma_f32_16x16x32_bf16 v[80:83], v[158:161], v[206:209], v[80:83]
	s_setprio 0
	s_setprio 1
	v_mfma_f32_16x16x32_bf16 v[108:111], v[162:165], v[178:181], v[108:111]
	v_mfma_f32_16x16x32_bf16 v[104:107], v[170:173], v[178:181], v[104:107]
	v_mfma_f32_16x16x32_bf16 v[92:95], v[162:165], v[186:189], v[92:95]
	v_mfma_f32_16x16x32_bf16 v[88:91], v[170:173], v[186:189], v[88:91]
	v_mfma_f32_16x16x32_bf16 v[76:79], v[162:165], v[194:197], v[76:79]
	v_mfma_f32_16x16x32_bf16 v[72:75], v[170:173], v[194:197], v[72:75]
	v_mfma_f32_16x16x32_bf16 v[68:71], v[162:165], v[202:205], v[68:71]
	v_mfma_f32_16x16x32_bf16 v[64:67], v[170:173], v[202:205], v[64:67]
	v_mfma_f32_16x16x32_bf16 v[108:111], v[166:169], v[182:185], v[108:111]
	v_mfma_f32_16x16x32_bf16 v[104:107], v[174:177], v[182:185], v[104:107]
	v_mfma_f32_16x16x32_bf16 v[92:95], v[166:169], v[190:193], v[92:95]
	v_mfma_f32_16x16x32_bf16 v[88:91], v[174:177], v[190:193], v[88:91]
	v_mfma_f32_16x16x32_bf16 v[76:79], v[166:169], v[198:201], v[76:79]
	v_mfma_f32_16x16x32_bf16 v[72:75], v[174:177], v[198:201], v[72:75]
	v_mfma_f32_16x16x32_bf16 v[68:71], v[166:169], v[206:209], v[68:71]
	v_mfma_f32_16x16x32_bf16 v[64:67], v[174:177], v[206:209], v[64:67]
	s_setprio 0
	s_barrier
; #define PG8_STAGE(bufoff, gbase, voff) do { _Pragma("unroll") for (int _i = 0; _i < 2; ++_i) \
;         __builtin_amdgcn_global_load_lds((const unsigned*)((const char*)(gbase) + (voff)[_i]), (PG8_LAS unsigned*)(lds + (bufoff) + ldsw + _i * 8192), 16, 0, 0); } while (0)
; #define PG8_STAGE_A(bufoff, gbase, h, nx) do { _Pragma("unroll") for (int _i = 0; _i < 2; ++_i) { \
;         const unsigned vo_ = GA ? ((nx) ? vgn[h][_i] : vgc[h][_i]) : voffA[_i]; \
;         __builtin_amdgcn_global_load_lds((const unsigned*)((const char*)(gbase) + vo_), (PG8_LAS unsigned*)(lds + (bufoff) + ldsw + _i * 8192), 16, 0, 0); } } while (0)
; #define PG8_LDA(dst, b, h) do { _Pragma("unroll") for (int m = 0; m < 4; ++m) _Pragma("unroll") for (int k = 0; k < 2; ++k) dst[m][k] = *(const PG8_LAS bf16x8*)(lds + PG8_SA(b, h) + aoff + m * 2048 + k * 1024); } while (0)
; #define PG8_MMA(ai, bj, At, Bt) do { __builtin_amdgcn_s_setprio(1); _Pragma("unroll") for (int m = 0; m < 4; ++m) _Pragma("unroll") for (int n = 0; n < 2; ++n) _Pragma("unroll") for (int k = 0; k < 2; ++k) \
;         acc[ai][bj][m][n] = __builtin_amdgcn_mfma_f32_16x16x32_bf16(Bt[n][k], At[m][k], acc[ai][bj][m][n], 0, 0, 0); __builtin_amdgcn_s_setprio(0); } while (0)
; #define PG8_WAIT_V(n) asm volatile("s_waitcnt vmcnt(" #n ")" ::: "memory")
; #define PG8_WAIT_L(n) asm volatile("s_waitcnt lgkmcnt(" #n ")" ::: "memory")
; #define PG8_BAR __builtin_amdgcn_s_barrier()
; #define PG8_SCHED __builtin_amdgcn_sched_barrier(0)
; template <class Epi, class Sched>
; __device__ __forceinline__ void gemm_phase(const int WID_, PG8_LAS unsigned char* lds, const Sched& S, const Epi& E) {
;     ...
;             PG8_LDA(At, 1, 1); PG8_STAGE(PG8_SB(1, 0), b3, voffB); PG8_STAGE(PG8_SB(1, 1), b3 + hstepB, voffB); PG8_STAGE_A(PG8_SA(1, 0), a3, 0, last);
;             PG8_WAIT_V(8); PG8_WAIT_L(0); PG8_BAR; PG8_MMA(1, 0, At, B0); PG8_MMA(1, 1, At, B1); PG8_BAR; PG8_SCHED;
;         }
	s_add_i32 s46, s68, s9
	v_lshl_add_u64 v[210:211], v[210:211], 0, s[2:3]
	s_mov_b32 m0, s46
	ds_read_b128 v[178:181], v145 offset:49152
	ds_read_b128 v[182:185], v145 offset:50176
	ds_read_b128 v[186:189], v145 offset:51200
	ds_read_b128 v[190:193], v145 offset:52224
	ds_read_b128 v[194:197], v145 offset:53248
	ds_read_b128 v[198:201], v145 offset:54272
	ds_read_b128 v[202:205], v145 offset:55296
	ds_read_b128 v[206:209], v145 offset:56320
	global_load_lds_dwordx4 v[210:211], off
	s_add_i32 m0, s46, 0x2000
	s_add_u32 s44, s44, 0x40080
	v_lshl_add_u64 v[210:211], v[212:213], 0, s[2:3]
	s_addc_u32 s45, s45, 0
	s_add_i32 s46, s69, s9
	global_load_lds_dwordx4 v[210:211], off
	v_lshl_add_u64 v[210:211], s[44:45], 0, v[130:131]
	s_mov_b32 m0, s46
	s_nop 0
	global_load_lds_dwordx4 v[210:211], off
	v_lshl_add_u64 v[210:211], s[44:45], 0, v[134:135]
	s_add_i32 m0, s46, 0x2000
	s_nop 0
	global_load_lds_dwordx4 v[210:211], off
	v_lshl_add_u64 v[210:211], v[214:215], 0, s[2:3]
	s_mov_b32 m0, s52
	s_nop 0
	global_load_lds_dwordx4 v[210:211], off
	v_lshl_add_u64 v[210:211], v[216:217], 0, s[2:3]
	s_mov_b32 m0, s53
	s_nop 0
	global_load_lds_dwordx4 v[210:211], off
	s_waitcnt vmcnt(8)
	s_waitcnt lgkmcnt(0)
	s_barrier
	s_setprio 1
	s_waitcnt lgkmcnt(0)
	v_mfma_f32_16x16x32_bf16 v[60:63], v[146:149], v[178:181], v[60:63]
	v_mfma_f32_16x16x32_bf16 v[56:59], v[154:157], v[178:181], v[56:59]
	v_mfma_f32_16x16x32_bf16 v[52:55], v[146:149], v[186:189], v[52:55]
	v_mfma_f32_16x16x32_bf16 v[48:51], v[154:157], v[186:189], v[48:51]
	v_mfma_f32_16x16x32_bf16 v[36:39], v[146:149], v[194:197], v[36:39]
	v_mfma_f32_16x16x32_bf16 v[32:35], v[154:157], v[194:197], v[32:35]
	v_mfma_f32_16x16x32_bf16 v[20:23], v[146:149], v[202:205], v[20:23]
	v_mfma_f32_16x16x32_bf16 v[16:19], v[154:157], v[202:205], v[16:19]
	v_mfma_f32_16x16x32_bf16 v[60:63], v[150:153], v[182:185], v[60:63]
	v_mfma_f32_16x16x32_bf16 v[56:59], v[158:161], v[182:185], v[56:59]
	v_mfma_f32_16x16x32_bf16 v[52:55], v[150:153], v[190:193], v[52:55]
	v_mfma_f32_16x16x32_bf16 v[48:51], v[158:161], v[190:193], v[48:51]
	v_mfma_f32_16x16x32_bf16 v[36:39], v[150:153], v[198:201], v[36:39]
	v_mfma_f32_16x16x32_bf16 v[32:35], v[158:161], v[198:201], v[32:35]
	v_mfma_f32_16x16x32_bf16 v[20:23], v[150:153], v[206:209], v[20:23]
	v_mfma_f32_16x16x32_bf16 v[16:19], v[158:161], v[206:209], v[16:19]
	s_setprio 0
	s_setprio 1
	v_mfma_f32_16x16x32_bf16 v[44:47], v[162:165], v[178:181], v[44:47]
	v_mfma_f32_16x16x32_bf16 v[40:43], v[170:173], v[178:181], v[40:43]
	v_mfma_f32_16x16x32_bf16 v[28:31], v[162:165], v[186:189], v[28:31]
	v_mfma_f32_16x16x32_bf16 v[24:27], v[170:173], v[186:189], v[24:27]
	v_mfma_f32_16x16x32_bf16 v[12:15], v[162:165], v[194:197], v[12:15]
	v_mfma_f32_16x16x32_bf16 v[8:11], v[170:173], v[194:197], v[8:11]
	v_mfma_f32_16x16x32_bf16 v[4:7], v[162:165], v[202:205], v[4:7]
	v_mfma_f32_16x16x32_bf16 v[0:3], v[170:173], v[202:205], v[0:3]
	v_mfma_f32_16x16x32_bf16 v[44:47], v[166:169], v[182:185], v[44:47]
	v_mfma_f32_16x16x32_bf16 v[40:43], v[174:177], v[182:185], v[40:43]
	v_mfma_f32_16x16x32_bf16 v[28:31], v[166:169], v[190:193], v[28:31]
	v_mfma_f32_16x16x32_bf16 v[24:27], v[174:177], v[190:193], v[24:27]
	v_mfma_f32_16x16x32_bf16 v[12:15], v[166:169], v[198:201], v[12:15]
	v_mfma_f32_16x16x32_bf16 v[8:11], v[174:177], v[198:201], v[8:11]
	v_mfma_f32_16x16x32_bf16 v[4:7], v[166:169], v[206:209], v[4:7]
	v_mfma_f32_16x16x32_bf16 v[0:3], v[174:177], v[206:209], v[0:3]
	s_setprio 0
	s_add_i32 s67, s67, 2
	s_add_u32 s42, s42, 0x100
	s_addc_u32 s43, s43, 0
	s_add_u32 s63, s63, 0x100
	s_addc_u32 s66, s66, 0
	s_cmp_gt_u32 s67, 13
	s_barrier
	s_cbranch_scc0 .LBB0_1786
	s_and_b64 vcc, exec, s[4:5]
	s_cbranch_vccz .LBB0_1789
	s_barrier

; #define PG8_STAGE(bufoff, gbase, voff) do { _Pragma("unroll") for (int _i = 0; _i < 2; ++_i) \
;         __builtin_amdgcn_global_load_lds((const unsigned*)((const char*)(gbase) + (voff)[_i]), (PG8_LAS unsigned*)(lds + (bufoff) + ldsw + _i * 8192), 16, 0, 0); } while (0)
; #define PG8_STAGE_A(bufoff, gbase, h, nx) do { _Pragma("unroll") for (int _i = 0; _i < 2; ++_i) { \
;         const unsigned vo_ = GA ? ((nx) ? vgn[h][_i] : vgc[h][_i]) : voffA[_i]; \
;         __builtin_amdgcn_global_load_lds((const unsigned*)((const char*)(gbase) + vo_), (PG8_LAS unsigned*)(lds + (bufoff) + ldsw + _i * 8192), 16, 0, 0); } } while (0)
; #define PG8_LDA(dst, b, h) do { _Pragma("unroll") for (int m = 0; m < 4; ++m) _Pragma("unroll") for (int k = 0; k < 2; ++k) dst[m][k] = *(const PG8_LAS bf16x8*)(lds + PG8_SA(b, h) + aoff + m * 2048 + k * 1024); } while (0)
; #define PG8_LDB(dst, b, h) do { _Pragma("unroll") for (int n = 0; n < 2; ++n) _Pragma("unroll") for (int k = 0; k < 2; ++k) dst[n][k] = *(const PG8_LAS bf16x8*)(lds + PG8_SB(b, h) + boff + n * 2048 + k * 1024); } while (0)
; #define PG8_WAIT_V(n) asm volatile("s_waitcnt vmcnt(" #n ")" ::: "memory")
; #define PG8_WAIT_L(n) asm volatile("s_waitcnt lgkmcnt(" #n ")" ::: "memory")
; #define PG8_BAR __builtin_amdgcn_s_barrier()
; #define PG8_SCHED __builtin_amdgcn_sched_barrier(0)
; template <class Epi, class Sched>
; __device__ __forceinline__ void gemm_phase(const int WID_, PG8_LAS unsigned char* lds, const Sched& S, const Epi& E) {
;     ...
;         for (int t = 0; t < nt; t += 2) {
;             const bool last = (t == nt - 2);
;             const char* a1 = cA + (size_t)(t + 1) * kstep;
;             const char* a2 = last ? nA : cA + (size_t)(t + 2) * kstep; const char* b2 = last ? nB : cB + (size_t)(t + 2) * kstep;
;             const char* a3 = a2 + kstep; const char* b3 = b2 + kstep;
;             PG8_LDB(B0, 0, 0); PG8_LDB(B1, 0, 1); PG8_SCHED; PG8_LDA(At, 0, 0); PG8_STAGE_A(PG8_SA(1, 1), a1 + hstepA, 1, false);
;             PG8_WAIT_V(8); PG8_WAIT_L(0); PG8_BAR; PG8_MMA(0, 0, At, B0); PG8_MMA(0, 1, At, B1); PG8_BAR; PG8_SCHED;
;             PG8_LDA(At, 0, 1); PG8_STAGE(PG8_SB(0, 0), b2, voffB); PG8_STAGE(PG8_SB(0, 1), b2 + hstepB, voffB); PG8_STAGE_A(PG8_SA(0, 0), a2, 0, last);
;             PG8_WAIT_V(8); PG8_WAIT_L(0); PG8_BAR; PG8_MMA(1, 0, At, B0); PG8_MMA(1, 1, At, B1); PG8_BAR; PG8_SCHED;
.LBB0_1810:
	ds_read_b128 v[146:149], v143
	ds_read_b128 v[150:153], v143 offset:1024
	ds_read_b128 v[154:157], v143 offset:2048
	ds_read_b128 v[158:161], v143 offset:3072
	ds_read_b128 v[162:165], v144
	ds_read_b128 v[166:169], v144 offset:1024
	ds_read_b128 v[170:173], v144 offset:2048
	ds_read_b128 v[174:177], v144 offset:3072
	s_add_u32 s44, s42, 0xfffc0080
	s_addc_u32 s45, s43, -1
	s_cmp_eq_u32 s68, 12
	s_cselect_b32 s47, s37, s45
	s_cselect_b32 s46, s62, s44
	s_cselect_b32 s45, s23, s67
	s_cselect_b32 s44, s63, s66
	v_lshl_add_u64 v[210:211], s[42:43], 0, v[136:137]
	s_add_i32 m0, s48, 0xc000
	ds_read_b128 v[178:181], v145
	ds_read_b128 v[182:185], v145 offset:1024
	ds_read_b128 v[186:189], v145 offset:2048
	ds_read_b128 v[190:193], v145 offset:3072
	ds_read_b128 v[194:197], v145 offset:4096
	ds_read_b128 v[198:201], v145 offset:5120
	ds_read_b128 v[202:205], v145 offset:6144
	ds_read_b128 v[206:209], v145 offset:7168
	global_load_lds_dwordx4 v[210:211], off
	v_lshl_add_u64 v[210:211], s[42:43], 0, v[138:139]
	s_add_i32 m0, s48, 0xe000
	s_nop 0
	global_load_lds_dwordx4 v[210:211], off
	s_waitcnt vmcnt(8)
	s_waitcnt lgkmcnt(0)
	s_barrier
	s_setprio 1
	s_waitcnt lgkmcnt(0)
	v_mfma_f32_16x16x32_bf16 v[124:127], v[146:149], v[178:181], v[124:127]
	v_mfma_f32_16x16x32_bf16 v[120:123], v[154:157], v[178:181], v[120:123]
	v_mfma_f32_16x16x32_bf16 v[116:119], v[146:149], v[186:189], v[116:119]
	v_mfma_f32_16x16x32_bf16 v[112:115], v[154:157], v[186:189], v[112:115]
	v_mfma_f32_16x16x32_bf16 v[100:103], v[146:149], v[194:197], v[100:103]
	v_mfma_f32_16x16x32_bf16 v[96:99], v[154:157], v[194:197], v[96:99]
	v_mfma_f32_16x16x32_bf16 v[84:87], v[146:149], v[202:205], v[84:87]
	v_mfma_f32_16x16x32_bf16 v[80:83], v[154:157], v[202:205], v[80:83]
	v_mfma_f32_16x16x32_bf16 v[124:127], v[150:153], v[182:185], v[124:127]
	v_mfma_f32_16x16x32_bf16 v[120:123], v[158:161], v[182:185], v[120:123]
	v_mfma_f32_16x16x32_bf16 v[116:119], v[150:153], v[190:193], v[116:119]
	v_mfma_f32_16x16x32_bf16 v[112:115], v[158:161], v[190:193], v[112:115]
	v_mfma_f32_16x16x32_bf16 v[100:103], v[150:153], v[198:201], v[100:103]
	v_mfma_f32_16x16x32_bf16 v[96:99], v[158:161], v[198:201], v[96:99]
	v_mfma_f32_16x16x32_bf16 v[84:87], v[150:153], v[206:209], v[84:87]
	v_mfma_f32_16x16x32_bf16 v[80:83], v[158:161], v[206:209], v[80:83]
	s_setprio 0
	s_setprio 1
	v_mfma_f32_16x16x32_bf16 v[108:111], v[162:165], v[178:181], v[108:111]
	v_mfma_f32_16x16x32_bf16 v[104:107], v[170:173], v[178:181], v[104:107]
	v_mfma_f32_16x16x32_bf16 v[92:95], v[162:165], v[186:189], v[92:95]
	v_mfma_f32_16x16x32_bf16 v[88:91], v[170:173], v[186:189], v[88:91]
	v_mfma_f32_16x16x32_bf16 v[76:79], v[162:165], v[194:197], v[76:79]
	v_mfma_f32_16x16x32_bf16 v[72:75], v[170:173], v[194:197], v[72:75]
	v_mfma_f32_16x16x32_bf16 v[68:71], v[162:165], v[202:205], v[68:71]
	v_mfma_f32_16x16x32_bf16 v[64:67], v[170:173], v[202:205], v[64:67]
	v_mfma_f32_16x16x32_bf16 v[108:111], v[166:169], v[182:185], v[108:111]
	v_mfma_f32_16x16x32_bf16 v[104:107], v[174:177], v[182:185], v[104:107]
	v_mfma_f32_16x16x32_bf16 v[92:95], v[166:169], v[190:193], v[92:95]
	v_mfma_f32_16x16x32_bf16 v[88:91], v[174:177], v[190:193], v[88:91]
	v_mfma_f32_16x16x32_bf16 v[76:79], v[166:169], v[198:201], v[76:79]
	v_mfma_f32_16x16x32_bf16 v[72:75], v[174:177], v[198:201], v[72:75]
	v_mfma_f32_16x16x32_bf16 v[68:71], v[166:169], v[206:209], v[68:71]
	v_mfma_f32_16x16x32_bf16 v[64:67], v[174:177], v[206:209], v[64:67]
	s_setprio 0
	s_barrier
	s_add_i32 s69, s60, s33
	v_lshl_add_u64 v[210:211], s[44:45], 0, v[130:131]
	s_mov_b32 m0, s69
	ds_read_b128 v[178:181], v145 offset:16384
	ds_read_b128 v[182:185], v145 offset:17408
	ds_read_b128 v[186:189], v145 offset:18432
	ds_read_b128 v[190:193], v145 offset:19456
	ds_read_b128 v[194:197], v145 offset:20480
	ds_read_b128 v[198:201], v145 offset:21504
	ds_read_b128 v[202:205], v145 offset:22528
	ds_read_b128 v[206:209], v145 offset:23552
	global_load_lds_dwordx4 v[210:211], off
	s_add_i32 m0, s69, 0x2000
	s_add_u32 s70, s44, 0x40000
	v_lshl_add_u64 v[212:213], s[44:45], 0, v[134:135]
	s_addc_u32 s71, s45, 0
	s_add_i32 s69, s61, s33
	global_load_lds_dwordx4 v[212:213], off
	v_lshl_add_u64 v[214:215], s[70:71], 0, v[130:131]
	s_mov_b32 m0, s69
	v_lshl_add_u64 v[216:217], s[46:47], 0, v[132:133]
	global_load_lds_dwordx4 v[214:215], off
	v_lshl_add_u64 v[214:215], s[70:71], 0, v[134:135]
	s_add_i32 m0, s69, 0x2000
	s_nop 0
	global_load_lds_dwordx4 v[214:215], off
	v_lshl_add_u64 v[214:215], s[46:47], 0, v[128:129]
	s_mov_b32 m0, s48
	s_nop 0
	global_load_lds_dwordx4 v[214:215], off
	s_mov_b32 m0, s49
	s_nop 0
	global_load_lds_dwordx4 v[216:217], off
	s_waitcnt vmcnt(8)
	s_waitcnt lgkmcnt(0)
	s_barrier
; #define PG8_STAGE_A(bufoff, gbase, h, nx) do { _Pragma("unroll") for (int _i = 0; _i < 2; ++_i) { \
;         const unsigned vo_ = GA ? ((nx) ? vgn[h][_i] : vgc[h][_i]) : voffA[_i]; \
;         __builtin_amdgcn_global_load_lds((const unsigned*)((const char*)(gbase) + vo_), (PG8_LAS unsigned*)(lds + (bufoff) + ldsw + _i * 8192), 16, 0, 0); } } while (0)
; #define PG8_LDA(dst, b, h) do { _Pragma("unroll") for (int m = 0; m < 4; ++m) _Pragma("unroll") for (int k = 0; k < 2; ++k) dst[m][k] = *(const PG8_LAS bf16x8*)(lds + PG8_SA(b, h) + aoff + m * 2048 + k * 1024); } while (0)
; #define PG8_LDB(dst, b, h) do { _Pragma("unroll") for (int n = 0; n < 2; ++n) _Pragma("unroll") for (int k = 0; k < 2; ++k) dst[n][k] = *(const PG8_LAS bf16x8*)(lds + PG8_SB(b, h) + boff + n * 2048 + k * 1024); } while (0)
; #define PG8_MMA(ai, bj, At, Bt) do { __builtin_amdgcn_s_setprio(1); _Pragma("unroll") for (int m = 0; m < 4; ++m) _Pragma("unroll") for (int n = 0; n < 2; ++n) _Pragma("unroll") for (int k = 0; k < 2; ++k) \
;         acc[ai][bj][m][n] = __builtin_amdgcn_mfma_f32_16x16x32_bf16(Bt[n][k], At[m][k], acc[ai][bj][m][n], 0, 0, 0); __builtin_amdgcn_s_setprio(0); } while (0)
; #define PG8_WAIT_V(n) asm volatile("s_waitcnt vmcnt(" #n ")" ::: "memory")
; #define PG8_WAIT_L(n) asm volatile("s_waitcnt lgkmcnt(" #n ")" ::: "memory")
; #define PG8_BAR __builtin_amdgcn_s_barrier()
; #define PG8_SCHED __builtin_amdgcn_sched_barrier(0)
; template <class Epi, class Sched>
; __device__ __forceinline__ void gemm_phase(const int WID_, PG8_LAS unsigned char* lds, const Sched& S, const Epi& E) {
;     ...
;             PG8_WAIT_V(8); PG8_WAIT_L(0); PG8_BAR; PG8_MMA(1, 0, At, B0); PG8_MMA(1, 1, At, B1); PG8_BAR; PG8_SCHED;
;             PG8_LDB(B0, 1, 0); PG8_LDB(B1, 1, 1); PG8_SCHED; PG8_LDA(At, 1, 0); PG8_STAGE_A(PG8_SA(0, 1), a2 + hstepA, 1, last);
;             PG8_WAIT_V(8); PG8_WAIT_L(0); PG8_BAR; PG8_MMA(0, 0, At, B0); PG8_MMA(0, 1, At, B1); PG8_BAR; PG8_SCHED;
	s_setprio 1
	s_waitcnt lgkmcnt(0)
	v_mfma_f32_16x16x32_bf16 v[60:63], v[146:149], v[178:181], v[60:63]
	v_mfma_f32_16x16x32_bf16 v[56:59], v[154:157], v[178:181], v[56:59]
	v_mfma_f32_16x16x32_bf16 v[52:55], v[146:149], v[186:189], v[52:55]
	v_mfma_f32_16x16x32_bf16 v[48:51], v[154:157], v[186:189], v[48:51]
	v_mfma_f32_16x16x32_bf16 v[36:39], v[146:149], v[194:197], v[36:39]
	v_mfma_f32_16x16x32_bf16 v[32:35], v[154:157], v[194:197], v[32:35]
	v_mfma_f32_16x16x32_bf16 v[20:23], v[146:149], v[202:205], v[20:23]
	v_mfma_f32_16x16x32_bf16 v[16:19], v[154:157], v[202:205], v[16:19]
	v_mfma_f32_16x16x32_bf16 v[60:63], v[150:153], v[182:185], v[60:63]
	v_mfma_f32_16x16x32_bf16 v[56:59], v[158:161], v[182:185], v[56:59]
	v_mfma_f32_16x16x32_bf16 v[52:55], v[150:153], v[190:193], v[52:55]
	v_mfma_f32_16x16x32_bf16 v[48:51], v[158:161], v[190:193], v[48:51]
	v_mfma_f32_16x16x32_bf16 v[36:39], v[150:153], v[198:201], v[36:39]
	v_mfma_f32_16x16x32_bf16 v[32:35], v[158:161], v[198:201], v[32:35]
	v_mfma_f32_16x16x32_bf16 v[20:23], v[150:153], v[206:209], v[20:23]
	v_mfma_f32_16x16x32_bf16 v[16:19], v[158:161], v[206:209], v[16:19]
	s_setprio 0
	s_setprio 1
	v_mfma_f32_16x16x32_bf16 v[44:47], v[162:165], v[178:181], v[44:47]
	v_mfma_f32_16x16x32_bf16 v[40:43], v[170:173], v[178:181], v[40:43]
	v_mfma_f32_16x16x32_bf16 v[28:31], v[162:165], v[186:189], v[28:31]
	v_mfma_f32_16x16x32_bf16 v[24:27], v[170:173], v[186:189], v[24:27]
	v_mfma_f32_16x16x32_bf16 v[12:15], v[162:165], v[194:197], v[12:15]
	v_mfma_f32_16x16x32_bf16 v[8:11], v[170:173], v[194:197], v[8:11]
	v_mfma_f32_16x16x32_bf16 v[4:7], v[162:165], v[202:205], v[4:7]
	v_mfma_f32_16x16x32_bf16 v[0:3], v[170:173], v[202:205], v[0:3]
	v_mfma_f32_16x16x32_bf16 v[44:47], v[166:169], v[182:185], v[44:47]
	v_mfma_f32_16x16x32_bf16 v[40:43], v[174:177], v[182:185], v[40:43]
	v_mfma_f32_16x16x32_bf16 v[28:31], v[166:169], v[190:193], v[28:31]
	v_mfma_f32_16x16x32_bf16 v[24:27], v[174:177], v[190:193], v[24:27]
	v_mfma_f32_16x16x32_bf16 v[12:15], v[166:169], v[198:201], v[12:15]
	v_mfma_f32_16x16x32_bf16 v[8:11], v[174:177], v[198:201], v[8:11]
	v_mfma_f32_16x16x32_bf16 v[4:7], v[166:169], v[206:209], v[4:7]
	v_mfma_f32_16x16x32_bf16 v[0:3], v[174:177], v[206:209], v[0:3]
	s_setprio 0
	s_barrier
	s_add_i32 s69, 0, 0x18000
	s_add_i32 s70, 0, 0x1c000
	v_add_u32_e32 v158, s69, v141
	v_add_u32_e32 v174, s70, v141
	ds_read_b128 v[146:149], v158
	ds_read_b128 v[150:153], v158 offset:1024
	ds_read_b128 v[154:157], v158 offset:2048
	ds_read_b128 v[158:161], v158 offset:3072
	ds_read_b128 v[162:165], v174
	ds_read_b128 v[166:169], v174 offset:1024
	ds_read_b128 v[170:173], v174 offset:2048
	ds_read_b128 v[174:177], v174 offset:3072
	s_add_u32 s46, s46, 0x40000
	s_addc_u32 s47, s47, 0
	s_mov_b32 m0, s50
	v_lshl_add_u64 v[218:219], s[46:47], 0, v[128:129]
	ds_read_b128 v[178:181], v145 offset:32768
	ds_read_b128 v[182:185], v145 offset:33792
	ds_read_b128 v[186:189], v145 offset:34816
	ds_read_b128 v[190:193], v145 offset:35840
	ds_read_b128 v[194:197], v145 offset:36864
	ds_read_b128 v[198:201], v145 offset:37888
	ds_read_b128 v[202:205], v145 offset:38912
	ds_read_b128 v[206:209], v145 offset:39936
	global_load_lds_dwordx4 v[218:219], off
	v_lshl_add_u64 v[218:219], s[46:47], 0, v[132:133]
	s_mov_b32 m0, s51
	s_nop 0
	global_load_lds_dwordx4 v[218:219], off
	s_waitcnt vmcnt(8)
	s_waitcnt lgkmcnt(0)
	s_barrier
	s_setprio 1
	s_waitcnt lgkmcnt(0)
	v_mfma_f32_16x16x32_bf16 v[124:127], v[146:149], v[178:181], v[124:127]
	v_mfma_f32_16x16x32_bf16 v[120:123], v[154:157], v[178:181], v[120:123]
	v_mfma_f32_16x16x32_bf16 v[116:119], v[146:149], v[186:189], v[116:119]
	v_mfma_f32_16x16x32_bf16 v[112:115], v[154:157], v[186:189], v[112:115]
	v_mfma_f32_16x16x32_bf16 v[100:103], v[146:149], v[194:197], v[100:103]
	v_mfma_f32_16x16x32_bf16 v[96:99], v[154:157], v[194:197], v[96:99]
	v_mfma_f32_16x16x32_bf16 v[84:87], v[146:149], v[202:205], v[84:87]
	v_mfma_f32_16x16x32_bf16 v[80:83], v[154:157], v[202:205], v[80:83]
	v_mfma_f32_16x16x32_bf16 v[124:127], v[150:153], v[182:185], v[124:127]
	v_mfma_f32_16x16x32_bf16 v[120:123], v[158:161], v[182:185], v[120:123]
	v_mfma_f32_16x16x32_bf16 v[116:119], v[150:153], v[190:193], v[116:119]
	v_mfma_f32_16x16x32_bf16 v[112:115], v[158:161], v[190:193], v[112:115]
	v_mfma_f32_16x16x32_bf16 v[100:103], v[150:153], v[198:201], v[100:103]
	v_mfma_f32_16x16x32_bf16 v[96:99], v[158:161], v[198:201], v[96:99]
	v_mfma_f32_16x16x32_bf16 v[84:87], v[150:153], v[206:209], v[84:87]
	v_mfma_f32_16x16x32_bf16 v[80:83], v[158:161], v[206:209], v[80:83]
	s_setprio 0
	s_setprio 1
	v_mfma_f32_16x16x32_bf16 v[108:111], v[162:165], v[178:181], v[108:111]
	v_mfma_f32_16x16x32_bf16 v[104:107], v[170:173], v[178:181], v[104:107]
	v_mfma_f32_16x16x32_bf16 v[92:95], v[162:165], v[186:189], v[92:95]
	v_mfma_f32_16x16x32_bf16 v[88:91], v[170:173], v[186:189], v[88:91]
	v_mfma_f32_16x16x32_bf16 v[76:79], v[162:165], v[194:197], v[76:79]
	v_mfma_f32_16x16x32_bf16 v[72:75], v[170:173], v[194:197], v[72:75]
	v_mfma_f32_16x16x32_bf16 v[68:71], v[162:165], v[202:205], v[68:71]
	v_mfma_f32_16x16x32_bf16 v[64:67], v[170:173], v[202:205], v[64:67]
	v_mfma_f32_16x16x32_bf16 v[108:111], v[166:169], v[182:185], v[108:111]
	v_mfma_f32_16x16x32_bf16 v[104:107], v[174:177], v[182:185], v[104:107]
	v_mfma_f32_16x16x32_bf16 v[92:95], v[166:169], v[190:193], v[92:95]
	v_mfma_f32_16x16x32_bf16 v[88:91], v[174:177], v[190:193], v[88:91]
	v_mfma_f32_16x16x32_bf16 v[76:79], v[166:169], v[198:201], v[76:79]
	v_mfma_f32_16x16x32_bf16 v[72:75], v[174:177], v[198:201], v[72:75]
	v_mfma_f32_16x16x32_bf16 v[68:71], v[166:169], v[206:209], v[68:71]
	v_mfma_f32_16x16x32_bf16 v[64:67], v[174:177], v[206:209], v[64:67]
	s_setprio 0
	s_barrier
; #define PG8_STAGE(bufoff, gbase, voff) do { _Pragma("unroll") for (int _i = 0; _i < 2; ++_i) \
;         __builtin_amdgcn_global_load_lds((const unsigned*)((const char*)(gbase) + (voff)[_i]), (PG8_LAS unsigned*)(lds + (bufoff) + ldsw + _i * 8192), 16, 0, 0); } while (0)
; #define PG8_STAGE_A(bufoff, gbase, h, nx) do { _Pragma("unroll") for (int _i = 0; _i < 2; ++_i) { \
;         const unsigned vo_ = GA ? ((nx) ? vgn[h][_i] : vgc[h][_i]) : voffA[_i]; \
;         __builtin_amdgcn_global_load_lds((const unsigned*)((const char*)(gbase) + vo_), (PG8_LAS unsigned*)(lds + (bufoff) + ldsw + _i * 8192), 16, 0, 0); } } while (0)
; #define PG8_LDA(dst, b, h) do { _Pragma("unroll") for (int m = 0; m < 4; ++m) _Pragma("unroll") for (int k = 0; k < 2; ++k) dst[m][k] = *(const PG8_LAS bf16x8*)(lds + PG8_SA(b, h) + aoff + m * 2048 + k * 1024); } while (0)
; #define PG8_MMA(ai, bj, At, Bt) do { __builtin_amdgcn_s_setprio(1); _Pragma("unroll") for (int m = 0; m < 4; ++m) _Pragma("unroll") for (int n = 0; n < 2; ++n) _Pragma("unroll") for (int k = 0; k < 2; ++k) \
;         acc[ai][bj][m][n] = __builtin_amdgcn_mfma_f32_16x16x32_bf16(Bt[n][k], At[m][k], acc[ai][bj][m][n], 0, 0, 0); __builtin_amdgcn_s_setprio(0); } while (0)
; #define PG8_WAIT_V(n) asm volatile("s_waitcnt vmcnt(" #n ")" ::: "memory")
; #define PG8_WAIT_L(n) asm volatile("s_waitcnt lgkmcnt(" #n ")" ::: "memory")
; #define PG8_BAR __builtin_amdgcn_s_barrier()
; #define PG8_SCHED __builtin_amdgcn_sched_barrier(0)
; template <class Epi, class Sched>
; __device__ __forceinline__ void gemm_phase(const int WID_, PG8_LAS unsigned char* lds, const Sched& S, const Epi& E) {
;     ...
;             PG8_LDA(At, 1, 1); PG8_STAGE(PG8_SB(1, 0), b3, voffB); PG8_STAGE(PG8_SB(1, 1), b3 + hstepB, voffB); PG8_STAGE_A(PG8_SA(1, 0), a3, 0, last);
;             PG8_WAIT_V(8); PG8_WAIT_L(0); PG8_BAR; PG8_MMA(1, 0, At, B0); PG8_MMA(1, 1, At, B1); PG8_BAR; PG8_SCHED;
;         }
;         if (wr == 0) PG8_BAR;
	s_add_i32 s46, s69, s33
	v_lshl_add_u64 v[210:211], v[210:211], 0, s[2:3]
	s_mov_b32 m0, s46
	ds_read_b128 v[178:181], v145 offset:49152
	ds_read_b128 v[182:185], v145 offset:50176
	ds_read_b128 v[186:189], v145 offset:51200
	ds_read_b128 v[190:193], v145 offset:52224
	ds_read_b128 v[194:197], v145 offset:53248
	ds_read_b128 v[198:201], v145 offset:54272
	ds_read_b128 v[202:205], v145 offset:55296
	ds_read_b128 v[206:209], v145 offset:56320
	global_load_lds_dwordx4 v[210:211], off
	s_add_i32 m0, s46, 0x2000
	s_add_u32 s44, s44, 0x40080
	v_lshl_add_u64 v[210:211], v[212:213], 0, s[2:3]
	s_addc_u32 s45, s45, 0
	s_add_i32 s46, s70, s33
	global_load_lds_dwordx4 v[210:211], off
	v_lshl_add_u64 v[210:211], s[44:45], 0, v[130:131]
	s_mov_b32 m0, s46
	s_nop 0
	global_load_lds_dwordx4 v[210:211], off
	v_lshl_add_u64 v[210:211], s[44:45], 0, v[134:135]
	s_add_i32 m0, s46, 0x2000
	s_nop 0
	global_load_lds_dwordx4 v[210:211], off
	v_lshl_add_u64 v[210:211], v[214:215], 0, s[2:3]
	s_mov_b32 m0, s53
	s_nop 0
	global_load_lds_dwordx4 v[210:211], off
	v_lshl_add_u64 v[210:211], v[216:217], 0, s[2:3]
	s_mov_b32 m0, s58
	s_nop 0
	global_load_lds_dwordx4 v[210:211], off
	s_waitcnt vmcnt(8)
	s_waitcnt lgkmcnt(0)
	s_barrier
	s_setprio 1
	s_waitcnt lgkmcnt(0)
	v_mfma_f32_16x16x32_bf16 v[60:63], v[146:149], v[178:181], v[60:63]
	v_mfma_f32_16x16x32_bf16 v[56:59], v[154:157], v[178:181], v[56:59]
	v_mfma_f32_16x16x32_bf16 v[52:55], v[146:149], v[186:189], v[52:55]
	v_mfma_f32_16x16x32_bf16 v[48:51], v[154:157], v[186:189], v[48:51]
	v_mfma_f32_16x16x32_bf16 v[36:39], v[146:149], v[194:197], v[36:39]
	v_mfma_f32_16x16x32_bf16 v[32:35], v[154:157], v[194:197], v[32:35]
	v_mfma_f32_16x16x32_bf16 v[20:23], v[146:149], v[202:205], v[20:23]
	v_mfma_f32_16x16x32_bf16 v[16:19], v[154:157], v[202:205], v[16:19]
	v_mfma_f32_16x16x32_bf16 v[60:63], v[150:153], v[182:185], v[60:63]
	v_mfma_f32_16x16x32_bf16 v[56:59], v[158:161], v[182:185], v[56:59]
	v_mfma_f32_16x16x32_bf16 v[52:55], v[150:153], v[190:193], v[52:55]
	v_mfma_f32_16x16x32_bf16 v[48:51], v[158:161], v[190:193], v[48:51]
	v_mfma_f32_16x16x32_bf16 v[36:39], v[150:153], v[198:201], v[36:39]
	v_mfma_f32_16x16x32_bf16 v[32:35], v[158:161], v[198:201], v[32:35]
	v_mfma_f32_16x16x32_bf16 v[20:23], v[150:153], v[206:209], v[20:23]
	v_mfma_f32_16x16x32_bf16 v[16:19], v[158:161], v[206:209], v[16:19]
	s_setprio 0
	s_setprio 1
	v_mfma_f32_16x16x32_bf16 v[44:47], v[162:165], v[178:181], v[44:47]
	v_mfma_f32_16x16x32_bf16 v[40:43], v[170:173], v[178:181], v[40:43]
	v_mfma_f32_16x16x32_bf16 v[28:31], v[162:165], v[186:189], v[28:31]
	v_mfma_f32_16x16x32_bf16 v[24:27], v[170:173], v[186:189], v[24:27]
	v_mfma_f32_16x16x32_bf16 v[12:15], v[162:165], v[194:197], v[12:15]
	v_mfma_f32_16x16x32_bf16 v[8:11], v[170:173], v[194:197], v[8:11]
	v_mfma_f32_16x16x32_bf16 v[4:7], v[162:165], v[202:205], v[4:7]
	v_mfma_f32_16x16x32_bf16 v[0:3], v[170:173], v[202:205], v[0:3]
	v_mfma_f32_16x16x32_bf16 v[44:47], v[166:169], v[182:185], v[44:47]
	v_mfma_f32_16x16x32_bf16 v[40:43], v[174:177], v[182:185], v[40:43]
	v_mfma_f32_16x16x32_bf16 v[28:31], v[166:169], v[190:193], v[28:31]
	v_mfma_f32_16x16x32_bf16 v[24:27], v[174:177], v[190:193], v[24:27]
	v_mfma_f32_16x16x32_bf16 v[12:15], v[166:169], v[198:201], v[12:15]
	v_mfma_f32_16x16x32_bf16 v[8:11], v[174:177], v[198:201], v[8:11]
	v_mfma_f32_16x16x32_bf16 v[4:7], v[166:169], v[206:209], v[4:7]
	v_mfma_f32_16x16x32_bf16 v[0:3], v[174:177], v[206:209], v[0:3]
	s_setprio 0
	s_add_i32 s68, s68, 2
	s_add_u32 s42, s42, 0x100
	s_addc_u32 s43, s43, 0
	s_add_u32 s66, s66, 0x100
	s_addc_u32 s67, s67, 0
	s_cmp_gt_u32 s68, 13
	s_barrier
	s_cbranch_scc0 .LBB0_1810
	s_and_b64 vcc, exec, s[4:5]
	s_cbranch_vccz .LBB0_1813
	s_barrier

; #define PG8_STAGE(bufoff, gbase, voff) do { _Pragma("unroll") for (int _i = 0; _i < 2; ++_i) \
;         __builtin_amdgcn_global_load_lds((const unsigned*)((const char*)(gbase) + (voff)[_i]), (PG8_LAS unsigned*)(lds + (bufoff) + ldsw + _i * 8192), 16, 0, 0); } while (0)
; #define PG8_STAGE_A(bufoff, gbase, h, nx) do { _Pragma("unroll") for (int _i = 0; _i < 2; ++_i) { \
;         const unsigned vo_ = GA ? ((nx) ? vgn[h][_i] : vgc[h][_i]) : voffA[_i]; \
;         __builtin_amdgcn_global_load_lds((const unsigned*)((const char*)(gbase) + vo_), (PG8_LAS unsigned*)(lds + (bufoff) + ldsw + _i * 8192), 16, 0, 0); } } while (0)
; #define PG8_LDA(dst, b, h) do { _Pragma("unroll") for (int m = 0; m < 4; ++m) _Pragma("unroll") for (int k = 0; k < 2; ++k) dst[m][k] = *(const PG8_LAS bf16x8*)(lds + PG8_SA(b, h) + aoff + m * 2048 + k * 1024); } while (0)
; #define PG8_LDB(dst, b, h) do { _Pragma("unroll") for (int n = 0; n < 2; ++n) _Pragma("unroll") for (int k = 0; k < 2; ++k) dst[n][k] = *(const PG8_LAS bf16x8*)(lds + PG8_SB(b, h) + boff + n * 2048 + k * 1024); } while (0)
; #define PG8_WAIT_V(n) asm volatile("s_waitcnt vmcnt(" #n ")" ::: "memory")
; #define PG8_WAIT_L(n) asm volatile("s_waitcnt lgkmcnt(" #n ")" ::: "memory")
; #define PG8_BAR __builtin_amdgcn_s_barrier()
; #define PG8_SCHED __builtin_amdgcn_sched_barrier(0)
; template <class Epi, class Sched>
; __device__ __forceinline__ void gemm_phase(const int WID_, PG8_LAS unsigned char* lds, const Sched& S, const Epi& E) {
;     ...
;         for (int t = 0; t < nt; t += 2) {
;             const bool last = (t == nt - 2);
;             const char* a1 = cA + (size_t)(t + 1) * kstep;
;             const char* a2 = last ? nA : cA + (size_t)(t + 2) * kstep; const char* b2 = last ? nB : cB + (size_t)(t + 2) * kstep;
;             const char* a3 = a2 + kstep; const char* b3 = b2 + kstep;
;             PG8_LDB(B0, 0, 0); PG8_LDB(B1, 0, 1); PG8_SCHED; PG8_LDA(At, 0, 0); PG8_STAGE_A(PG8_SA(1, 1), a1 + hstepA, 1, false);
;             PG8_WAIT_V(8); PG8_WAIT_L(0); PG8_BAR; PG8_MMA(0, 0, At, B0); PG8_MMA(0, 1, At, B1); PG8_BAR; PG8_SCHED;
;             PG8_LDA(At, 0, 1); PG8_STAGE(PG8_SB(0, 0), b2, voffB); PG8_STAGE(PG8_SB(0, 1), b2 + hstepB, voffB); PG8_STAGE_A(PG8_SA(0, 0), a2, 0, last);
;             PG8_WAIT_V(8); PG8_WAIT_L(0); PG8_BAR; PG8_MMA(1, 0, At, B0); PG8_MMA(1, 1, At, B1); PG8_BAR; PG8_SCHED;
.LBB0_2018:
	s_add_u32 s18, s16, 0xfffe0080
	s_addc_u32 s19, s17, -1
	s_add_i32 s43, 0, 0x10000
	s_cmp_eq_u32 s60, 4
	s_cselect_b32 s21, s9, s19
	s_cselect_b32 s20, s33, s18
	v_add_u32_e32 v148, s43, v151
	s_cselect_b32 s19, s44, s51
	s_cselect_b32 s18, s49, s50
	s_add_i32 s67, 0, 0x14000
	ds_read_b128 v[140:143], v148
	ds_read_b128 v[144:147], v148 offset:1024
	ds_read_b128 v[154:157], v148 offset:2048
	ds_read_b128 v[158:161], v148 offset:3072
	v_add_u32_e32 v148, s67, v151
	ds_read_b128 v[162:165], v148
	ds_read_b128 v[166:169], v148 offset:1024
	ds_read_b128 v[170:173], v148 offset:2048
	ds_read_b128 v[174:177], v148 offset:3072
	v_lshl_add_u64 v[148:149], s[16:17], 0, v[136:137]
	s_add_i32 m0, s23, 0xc000
	ds_read_b128 v[178:181], v153
	ds_read_b128 v[182:185], v153 offset:1024
	ds_read_b128 v[186:189], v153 offset:2048
	ds_read_b128 v[190:193], v153 offset:3072
	ds_read_b128 v[198:201], v153 offset:4096
	ds_read_b128 v[202:205], v153 offset:5120
	ds_read_b128 v[206:209], v153 offset:6144
	ds_read_b128 v[210:213], v153 offset:7168
	global_load_lds_dwordx4 v[148:149], off
	v_lshl_add_u64 v[148:149], s[16:17], 0, v[138:139]
	s_add_i32 m0, s23, 0xe000
	s_nop 0
	global_load_lds_dwordx4 v[148:149], off
	s_waitcnt vmcnt(8)
	s_waitcnt lgkmcnt(0)
	s_barrier
	s_setprio 1
	s_waitcnt lgkmcnt(0)
	v_mfma_f32_16x16x32_bf16 v[124:127], v[140:143], v[178:181], v[124:127]
	v_mfma_f32_16x16x32_bf16 v[120:123], v[154:157], v[178:181], v[120:123]
	v_mfma_f32_16x16x32_bf16 v[108:111], v[140:143], v[186:189], v[108:111]
	v_mfma_f32_16x16x32_bf16 v[104:107], v[154:157], v[186:189], v[104:107]
	v_mfma_f32_16x16x32_bf16 v[92:95], v[140:143], v[198:201], v[92:95]
	v_mfma_f32_16x16x32_bf16 v[88:91], v[154:157], v[198:201], v[88:91]
	v_mfma_f32_16x16x32_bf16 v[76:79], v[140:143], v[206:209], v[76:79]
	v_mfma_f32_16x16x32_bf16 v[72:75], v[154:157], v[206:209], v[72:75]
	v_mfma_f32_16x16x32_bf16 v[124:127], v[144:147], v[182:185], v[124:127]
	v_mfma_f32_16x16x32_bf16 v[120:123], v[158:161], v[182:185], v[120:123]
	v_mfma_f32_16x16x32_bf16 v[108:111], v[144:147], v[190:193], v[108:111]
	v_mfma_f32_16x16x32_bf16 v[104:107], v[158:161], v[190:193], v[104:107]
	v_mfma_f32_16x16x32_bf16 v[92:95], v[144:147], v[202:205], v[92:95]
	v_mfma_f32_16x16x32_bf16 v[88:91], v[158:161], v[202:205], v[88:91]
	v_mfma_f32_16x16x32_bf16 v[76:79], v[144:147], v[210:213], v[76:79]
	v_mfma_f32_16x16x32_bf16 v[72:75], v[158:161], v[210:213], v[72:75]
	s_setprio 0
	s_setprio 1
	v_mfma_f32_16x16x32_bf16 v[116:119], v[162:165], v[178:181], v[116:119]
	v_mfma_f32_16x16x32_bf16 v[112:115], v[170:173], v[178:181], v[112:115]
	v_mfma_f32_16x16x32_bf16 v[100:103], v[162:165], v[186:189], v[100:103]
	v_mfma_f32_16x16x32_bf16 v[96:99], v[170:173], v[186:189], v[96:99]
	v_mfma_f32_16x16x32_bf16 v[84:87], v[162:165], v[198:201], v[84:87]
	v_mfma_f32_16x16x32_bf16 v[80:83], v[170:173], v[198:201], v[80:83]
	v_mfma_f32_16x16x32_bf16 v[68:71], v[162:165], v[206:209], v[68:71]
	v_mfma_f32_16x16x32_bf16 v[64:67], v[170:173], v[206:209], v[64:67]
	v_mfma_f32_16x16x32_bf16 v[116:119], v[166:169], v[182:185], v[116:119]
	v_mfma_f32_16x16x32_bf16 v[112:115], v[174:177], v[182:185], v[112:115]
	v_mfma_f32_16x16x32_bf16 v[100:103], v[166:169], v[190:193], v[100:103]
	v_mfma_f32_16x16x32_bf16 v[96:99], v[174:177], v[190:193], v[96:99]
	v_mfma_f32_16x16x32_bf16 v[84:87], v[166:169], v[202:205], v[84:87]
	v_mfma_f32_16x16x32_bf16 v[80:83], v[174:177], v[202:205], v[80:83]
	v_mfma_f32_16x16x32_bf16 v[68:71], v[166:169], v[210:213], v[68:71]
	v_mfma_f32_16x16x32_bf16 v[64:67], v[174:177], v[210:213], v[64:67]
	s_setprio 0
	s_barrier
	s_add_i32 s46, s43, s22
	v_lshl_add_u64 v[148:149], s[18:19], 0, v[128:129]
	s_mov_b32 m0, s46
	ds_read_b128 v[178:181], v153 offset:16384
	ds_read_b128 v[182:185], v153 offset:17408
	ds_read_b128 v[186:189], v153 offset:18432
	ds_read_b128 v[190:193], v153 offset:19456
	ds_read_b128 v[198:201], v153 offset:20480
	ds_read_b128 v[202:205], v153 offset:21504
	ds_read_b128 v[206:209], v153 offset:22528
	ds_read_b128 v[210:213], v153 offset:23552
	global_load_lds_dwordx4 v[148:149], off
	s_add_i32 m0, s46, 0x2000
	s_add_u32 s62, s18, 0x20000
	v_lshl_add_u64 v[214:215], s[18:19], 0, v[130:131]
	s_addc_u32 s63, s19, 0
	s_add_i32 s46, s67, s22
	global_load_lds_dwordx4 v[214:215], off
	v_lshl_add_u64 v[216:217], s[62:63], 0, v[128:129]
	s_mov_b32 m0, s46
	v_lshl_add_u64 v[218:219], s[20:21], 0, v[132:133]
	global_load_lds_dwordx4 v[216:217], off
	v_lshl_add_u64 v[216:217], s[62:63], 0, v[130:131]
	s_add_i32 m0, s46, 0x2000
	s_nop 0
	global_load_lds_dwordx4 v[216:217], off
	v_lshl_add_u64 v[216:217], s[20:21], 0, v[134:135]
	s_mov_b32 m0, s23
	s_nop 0
	global_load_lds_dwordx4 v[216:217], off
	s_mov_b32 m0, s78
	s_nop 0
	global_load_lds_dwordx4 v[218:219], off
	s_waitcnt vmcnt(8)
	s_waitcnt lgkmcnt(0)
	s_barrier
; #define PG8_STAGE_A(bufoff, gbase, h, nx) do { _Pragma("unroll") for (int _i = 0; _i < 2; ++_i) { \
;         const unsigned vo_ = GA ? ((nx) ? vgn[h][_i] : vgc[h][_i]) : voffA[_i]; \
;         __builtin_amdgcn_global_load_lds((const unsigned*)((const char*)(gbase) + vo_), (PG8_LAS unsigned*)(lds + (bufoff) + ldsw + _i * 8192), 16, 0, 0); } } while (0)
; #define PG8_LDA(dst, b, h) do { _Pragma("unroll") for (int m = 0; m < 4; ++m) _Pragma("unroll") for (int k = 0; k < 2; ++k) dst[m][k] = *(const PG8_LAS bf16x8*)(lds + PG8_SA(b, h) + aoff + m * 2048 + k * 1024); } while (0)
; #define PG8_LDB(dst, b, h) do { _Pragma("unroll") for (int n = 0; n < 2; ++n) _Pragma("unroll") for (int k = 0; k < 2; ++k) dst[n][k] = *(const PG8_LAS bf16x8*)(lds + PG8_SB(b, h) + boff + n * 2048 + k * 1024); } while (0)
; #define PG8_MMA(ai, bj, At, Bt) do { __builtin_amdgcn_s_setprio(1); _Pragma("unroll") for (int m = 0; m < 4; ++m) _Pragma("unroll") for (int n = 0; n < 2; ++n) _Pragma("unroll") for (int k = 0; k < 2; ++k) \
;         acc[ai][bj][m][n] = __builtin_amdgcn_mfma_f32_16x16x32_bf16(Bt[n][k], At[m][k], acc[ai][bj][m][n], 0, 0, 0); __builtin_amdgcn_s_setprio(0); } while (0)
; #define PG8_WAIT_V(n) asm volatile("s_waitcnt vmcnt(" #n ")" ::: "memory")
; #define PG8_WAIT_L(n) asm volatile("s_waitcnt lgkmcnt(" #n ")" ::: "memory")
; #define PG8_BAR __builtin_amdgcn_s_barrier()
; #define PG8_SCHED __builtin_amdgcn_sched_barrier(0)
; template <class Epi, class Sched>
; __device__ __forceinline__ void gemm_phase(const int WID_, PG8_LAS unsigned char* lds, const Sched& S, const Epi& E) {
;     ...
;             PG8_WAIT_V(8); PG8_WAIT_L(0); PG8_BAR; PG8_MMA(1, 0, At, B0); PG8_MMA(1, 1, At, B1); PG8_BAR; PG8_SCHED;
;             PG8_LDB(B0, 1, 0); PG8_LDB(B1, 1, 1); PG8_SCHED; PG8_LDA(At, 1, 0); PG8_STAGE_A(PG8_SA(0, 1), a2 + hstepA, 1, last);
;             PG8_WAIT_V(8); PG8_WAIT_L(0); PG8_BAR; PG8_MMA(0, 0, At, B0); PG8_MMA(0, 1, At, B1); PG8_BAR; PG8_SCHED;
	s_setprio 1
	s_waitcnt lgkmcnt(0)
	v_mfma_f32_16x16x32_bf16 v[60:63], v[140:143], v[178:181], v[60:63]
	v_mfma_f32_16x16x32_bf16 v[56:59], v[154:157], v[178:181], v[56:59]
	v_mfma_f32_16x16x32_bf16 v[44:47], v[140:143], v[186:189], v[44:47]
	v_mfma_f32_16x16x32_bf16 v[40:43], v[154:157], v[186:189], v[40:43]
	v_mfma_f32_16x16x32_bf16 v[28:31], v[140:143], v[198:201], v[28:31]
	v_mfma_f32_16x16x32_bf16 v[24:27], v[154:157], v[198:201], v[24:27]
	v_mfma_f32_16x16x32_bf16 v[12:15], v[140:143], v[206:209], v[12:15]
	v_mfma_f32_16x16x32_bf16 v[8:11], v[154:157], v[206:209], v[8:11]
	v_mfma_f32_16x16x32_bf16 v[60:63], v[144:147], v[182:185], v[60:63]
	v_mfma_f32_16x16x32_bf16 v[56:59], v[158:161], v[182:185], v[56:59]
	v_mfma_f32_16x16x32_bf16 v[44:47], v[144:147], v[190:193], v[44:47]
	v_mfma_f32_16x16x32_bf16 v[40:43], v[158:161], v[190:193], v[40:43]
	v_mfma_f32_16x16x32_bf16 v[28:31], v[144:147], v[202:205], v[28:31]
	v_mfma_f32_16x16x32_bf16 v[24:27], v[158:161], v[202:205], v[24:27]
	v_mfma_f32_16x16x32_bf16 v[12:15], v[144:147], v[210:213], v[12:15]
	v_mfma_f32_16x16x32_bf16 v[8:11], v[158:161], v[210:213], v[8:11]
	s_setprio 0
	s_setprio 1
	v_mfma_f32_16x16x32_bf16 v[52:55], v[162:165], v[178:181], v[52:55]
	v_mfma_f32_16x16x32_bf16 v[48:51], v[170:173], v[178:181], v[48:51]
	v_mfma_f32_16x16x32_bf16 v[36:39], v[162:165], v[186:189], v[36:39]
	v_mfma_f32_16x16x32_bf16 v[32:35], v[170:173], v[186:189], v[32:35]
	v_mfma_f32_16x16x32_bf16 v[20:23], v[162:165], v[198:201], v[20:23]
	v_mfma_f32_16x16x32_bf16 v[16:19], v[170:173], v[198:201], v[16:19]
	v_mfma_f32_16x16x32_bf16 v[0:3], v[162:165], v[206:209], v[0:3]
	v_mfma_f32_16x16x32_bf16 v[4:7], v[170:173], v[206:209], v[4:7]
	v_mfma_f32_16x16x32_bf16 v[52:55], v[166:169], v[182:185], v[52:55]
	v_mfma_f32_16x16x32_bf16 v[48:51], v[174:177], v[182:185], v[48:51]
	v_mfma_f32_16x16x32_bf16 v[36:39], v[166:169], v[190:193], v[36:39]
	v_mfma_f32_16x16x32_bf16 v[32:35], v[174:177], v[190:193], v[32:35]
	v_mfma_f32_16x16x32_bf16 v[20:23], v[166:169], v[202:205], v[20:23]
	v_mfma_f32_16x16x32_bf16 v[16:19], v[174:177], v[202:205], v[16:19]
	v_mfma_f32_16x16x32_bf16 v[0:3], v[166:169], v[210:213], v[0:3]
	v_mfma_f32_16x16x32_bf16 v[4:7], v[174:177], v[210:213], v[4:7]
	s_setprio 0
	s_barrier
	s_add_i32 s82, 0, 0x18000
	s_add_i32 s83, 0, 0x1c000
	v_add_u32_e32 v158, s82, v151
	v_add_u32_e32 v174, s83, v151
	ds_read_b128 v[140:143], v158
	ds_read_b128 v[144:147], v158 offset:1024
	ds_read_b128 v[154:157], v158 offset:2048
	ds_read_b128 v[158:161], v158 offset:3072
	ds_read_b128 v[162:165], v174
	ds_read_b128 v[166:169], v174 offset:1024
	ds_read_b128 v[170:173], v174 offset:2048
	ds_read_b128 v[174:177], v174 offset:3072
	s_add_u32 s20, s20, 0x20000
	s_addc_u32 s21, s21, 0
	s_mov_b32 m0, s79
	v_lshl_add_u64 v[220:221], s[20:21], 0, v[134:135]
	ds_read_b128 v[178:181], v153 offset:32768
	ds_read_b128 v[182:185], v153 offset:33792
	ds_read_b128 v[186:189], v153 offset:34816
	ds_read_b128 v[190:193], v153 offset:35840
	ds_read_b128 v[198:201], v153 offset:36864
	ds_read_b128 v[202:205], v153 offset:37888
	ds_read_b128 v[206:209], v153 offset:38912
	ds_read_b128 v[210:213], v153 offset:39936
	global_load_lds_dwordx4 v[220:221], off
	v_lshl_add_u64 v[220:221], s[20:21], 0, v[132:133]
	s_mov_b32 m0, s80
	s_nop 0
	global_load_lds_dwordx4 v[220:221], off
	s_waitcnt vmcnt(8)
	s_waitcnt lgkmcnt(0)
	s_barrier
	s_setprio 1
	s_waitcnt lgkmcnt(0)
	v_mfma_f32_16x16x32_bf16 v[124:127], v[140:143], v[178:181], v[124:127]
	v_mfma_f32_16x16x32_bf16 v[120:123], v[154:157], v[178:181], v[120:123]
	v_mfma_f32_16x16x32_bf16 v[108:111], v[140:143], v[186:189], v[108:111]
	v_mfma_f32_16x16x32_bf16 v[104:107], v[154:157], v[186:189], v[104:107]
	v_mfma_f32_16x16x32_bf16 v[92:95], v[140:143], v[198:201], v[92:95]
	v_mfma_f32_16x16x32_bf16 v[88:91], v[154:157], v[198:201], v[88:91]
	v_mfma_f32_16x16x32_bf16 v[76:79], v[140:143], v[206:209], v[76:79]
	v_mfma_f32_16x16x32_bf16 v[72:75], v[154:157], v[206:209], v[72:75]
	v_mfma_f32_16x16x32_bf16 v[124:127], v[144:147], v[182:185], v[124:127]
	v_mfma_f32_16x16x32_bf16 v[120:123], v[158:161], v[182:185], v[120:123]
	v_mfma_f32_16x16x32_bf16 v[108:111], v[144:147], v[190:193], v[108:111]
	v_mfma_f32_16x16x32_bf16 v[104:107], v[158:161], v[190:193], v[104:107]
	v_mfma_f32_16x16x32_bf16 v[92:95], v[144:147], v[202:205], v[92:95]
	v_mfma_f32_16x16x32_bf16 v[88:91], v[158:161], v[202:205], v[88:91]
	v_mfma_f32_16x16x32_bf16 v[76:79], v[144:147], v[210:213], v[76:79]
	v_mfma_f32_16x16x32_bf16 v[72:75], v[158:161], v[210:213], v[72:75]
	s_setprio 0
	s_setprio 1
	v_mfma_f32_16x16x32_bf16 v[116:119], v[162:165], v[178:181], v[116:119]
	v_mfma_f32_16x16x32_bf16 v[112:115], v[170:173], v[178:181], v[112:115]
	v_mfma_f32_16x16x32_bf16 v[100:103], v[162:165], v[186:189], v[100:103]
	v_mfma_f32_16x16x32_bf16 v[96:99], v[170:173], v[186:189], v[96:99]
	v_mfma_f32_16x16x32_bf16 v[84:87], v[162:165], v[198:201], v[84:87]
	v_mfma_f32_16x16x32_bf16 v[80:83], v[170:173], v[198:201], v[80:83]
	v_mfma_f32_16x16x32_bf16 v[68:71], v[162:165], v[206:209], v[68:71]
	v_mfma_f32_16x16x32_bf16 v[64:67], v[170:173], v[206:209], v[64:67]
	v_mfma_f32_16x16x32_bf16 v[116:119], v[166:169], v[182:185], v[116:119]
	v_mfma_f32_16x16x32_bf16 v[112:115], v[174:177], v[182:185], v[112:115]
	v_mfma_f32_16x16x32_bf16 v[100:103], v[166:169], v[190:193], v[100:103]
	v_mfma_f32_16x16x32_bf16 v[96:99], v[174:177], v[190:193], v[96:99]
	v_mfma_f32_16x16x32_bf16 v[84:87], v[166:169], v[202:205], v[84:87]
	v_mfma_f32_16x16x32_bf16 v[80:83], v[174:177], v[202:205], v[80:83]
	v_mfma_f32_16x16x32_bf16 v[68:71], v[166:169], v[210:213], v[68:71]
	v_mfma_f32_16x16x32_bf16 v[64:67], v[174:177], v[210:213], v[64:67]
	s_setprio 0
	s_barrier
; #define PG8_STAGE(bufoff, gbase, voff) do { _Pragma("unroll") for (int _i = 0; _i < 2; ++_i) \
;         __builtin_amdgcn_global_load_lds((const unsigned*)((const char*)(gbase) + (voff)[_i]), (PG8_LAS unsigned*)(lds + (bufoff) + ldsw + _i * 8192), 16, 0, 0); } while (0)
; #define PG8_STAGE_A(bufoff, gbase, h, nx) do { _Pragma("unroll") for (int _i = 0; _i < 2; ++_i) { \
;         const unsigned vo_ = GA ? ((nx) ? vgn[h][_i] : vgc[h][_i]) : voffA[_i]; \
;         __builtin_amdgcn_global_load_lds((const unsigned*)((const char*)(gbase) + vo_), (PG8_LAS unsigned*)(lds + (bufoff) + ldsw + _i * 8192), 16, 0, 0); } } while (0)
; #define PG8_LDA(dst, b, h) do { _Pragma("unroll") for (int m = 0; m < 4; ++m) _Pragma("unroll") for (int k = 0; k < 2; ++k) dst[m][k] = *(const PG8_LAS bf16x8*)(lds + PG8_SA(b, h) + aoff + m * 2048 + k * 1024); } while (0)
; #define PG8_MMA(ai, bj, At, Bt) do { __builtin_amdgcn_s_setprio(1); _Pragma("unroll") for (int m = 0; m < 4; ++m) _Pragma("unroll") for (int n = 0; n < 2; ++n) _Pragma("unroll") for (int k = 0; k < 2; ++k) \
;         acc[ai][bj][m][n] = __builtin_amdgcn_mfma_f32_16x16x32_bf16(Bt[n][k], At[m][k], acc[ai][bj][m][n], 0, 0, 0); __builtin_amdgcn_s_setprio(0); } while (0)
; #define PG8_WAIT_V(n) asm volatile("s_waitcnt vmcnt(" #n ")" ::: "memory")
; #define PG8_WAIT_L(n) asm volatile("s_waitcnt lgkmcnt(" #n ")" ::: "memory")
; #define PG8_BAR __builtin_amdgcn_s_barrier()
; #define PG8_SCHED __builtin_amdgcn_sched_barrier(0)
; template <class Epi, class Sched>
; __device__ __forceinline__ void gemm_phase(const int WID_, PG8_LAS unsigned char* lds, const Sched& S, const Epi& E) {
;     ...
;             PG8_LDA(At, 1, 1); PG8_STAGE(PG8_SB(1, 0), b3, voffB); PG8_STAGE(PG8_SB(1, 1), b3 + hstepB, voffB); PG8_STAGE_A(PG8_SA(1, 0), a3, 0, last);
;             PG8_WAIT_V(8); PG8_WAIT_L(0); PG8_BAR; PG8_MMA(1, 0, At, B0); PG8_MMA(1, 1, At, B1); PG8_BAR; PG8_SCHED;
;         }
;         if (wr == 0) PG8_BAR;
	s_add_i32 s20, s82, s22
	v_lshl_add_u64 v[148:149], v[148:149], 0, s[68:69]
	s_mov_b32 m0, s20
	ds_read_b128 v[178:181], v153 offset:49152
	ds_read_b128 v[182:185], v153 offset:50176
	ds_read_b128 v[186:189], v153 offset:51200
	ds_read_b128 v[190:193], v153 offset:52224
	ds_read_b128 v[198:201], v153 offset:53248
	ds_read_b128 v[202:205], v153 offset:54272
	ds_read_b128 v[206:209], v153 offset:55296
	ds_read_b128 v[210:213], v153 offset:56320
	global_load_lds_dwordx4 v[148:149], off
	s_add_i32 m0, s20, 0x2000
	s_add_u32 s18, s18, 0x20080
	v_lshl_add_u64 v[148:149], v[214:215], 0, s[68:69]
	s_addc_u32 s19, s19, 0
	s_add_i32 s20, s83, s22
	global_load_lds_dwordx4 v[148:149], off
	v_lshl_add_u64 v[148:149], s[18:19], 0, v[128:129]
	s_mov_b32 m0, s20
	s_nop 0
	global_load_lds_dwordx4 v[148:149], off
	v_lshl_add_u64 v[148:149], s[18:19], 0, v[130:131]
	s_add_i32 m0, s20, 0x2000
	s_nop 0
	global_load_lds_dwordx4 v[148:149], off
	v_lshl_add_u64 v[148:149], v[216:217], 0, s[68:69]
	s_mov_b32 m0, s81
	s_nop 0
	global_load_lds_dwordx4 v[148:149], off
	v_lshl_add_u64 v[148:149], v[218:219], 0, s[68:69]
	s_mov_b32 m0, s48
	s_nop 0
	global_load_lds_dwordx4 v[148:149], off
	s_waitcnt vmcnt(8)
	s_waitcnt lgkmcnt(0)
	s_barrier
	s_setprio 1
	s_waitcnt lgkmcnt(0)
	v_mfma_f32_16x16x32_bf16 v[60:63], v[140:143], v[178:181], v[60:63]
	v_mfma_f32_16x16x32_bf16 v[56:59], v[154:157], v[178:181], v[56:59]
	v_mfma_f32_16x16x32_bf16 v[44:47], v[140:143], v[186:189], v[44:47]
	v_mfma_f32_16x16x32_bf16 v[40:43], v[154:157], v[186:189], v[40:43]
	v_mfma_f32_16x16x32_bf16 v[28:31], v[140:143], v[198:201], v[28:31]
	v_mfma_f32_16x16x32_bf16 v[24:27], v[154:157], v[198:201], v[24:27]
	v_mfma_f32_16x16x32_bf16 v[12:15], v[140:143], v[206:209], v[12:15]
	v_mfma_f32_16x16x32_bf16 v[8:11], v[154:157], v[206:209], v[8:11]
	v_mfma_f32_16x16x32_bf16 v[60:63], v[144:147], v[182:185], v[60:63]
	v_mfma_f32_16x16x32_bf16 v[56:59], v[158:161], v[182:185], v[56:59]
	v_mfma_f32_16x16x32_bf16 v[44:47], v[144:147], v[190:193], v[44:47]
	v_mfma_f32_16x16x32_bf16 v[40:43], v[158:161], v[190:193], v[40:43]
	v_mfma_f32_16x16x32_bf16 v[28:31], v[144:147], v[202:205], v[28:31]
	v_mfma_f32_16x16x32_bf16 v[24:27], v[158:161], v[202:205], v[24:27]
	v_mfma_f32_16x16x32_bf16 v[12:15], v[144:147], v[210:213], v[12:15]
	v_mfma_f32_16x16x32_bf16 v[8:11], v[158:161], v[210:213], v[8:11]
	s_setprio 0
	s_setprio 1
	v_mfma_f32_16x16x32_bf16 v[52:55], v[162:165], v[178:181], v[52:55]
	v_mfma_f32_16x16x32_bf16 v[48:51], v[170:173], v[178:181], v[48:51]
	v_mfma_f32_16x16x32_bf16 v[36:39], v[162:165], v[186:189], v[36:39]
	v_mfma_f32_16x16x32_bf16 v[32:35], v[170:173], v[186:189], v[32:35]
	v_mfma_f32_16x16x32_bf16 v[20:23], v[162:165], v[198:201], v[20:23]
	v_mfma_f32_16x16x32_bf16 v[16:19], v[170:173], v[198:201], v[16:19]
	v_mfma_f32_16x16x32_bf16 v[0:3], v[162:165], v[206:209], v[0:3]
	v_mfma_f32_16x16x32_bf16 v[4:7], v[170:173], v[206:209], v[4:7]
	v_mfma_f32_16x16x32_bf16 v[52:55], v[166:169], v[182:185], v[52:55]
	v_mfma_f32_16x16x32_bf16 v[48:51], v[174:177], v[182:185], v[48:51]
	v_mfma_f32_16x16x32_bf16 v[36:39], v[166:169], v[190:193], v[36:39]
	v_mfma_f32_16x16x32_bf16 v[32:35], v[174:177], v[190:193], v[32:35]
	v_mfma_f32_16x16x32_bf16 v[20:23], v[166:169], v[202:205], v[20:23]
	v_mfma_f32_16x16x32_bf16 v[16:19], v[174:177], v[202:205], v[16:19]
	v_mfma_f32_16x16x32_bf16 v[0:3], v[166:169], v[210:213], v[0:3]
	v_mfma_f32_16x16x32_bf16 v[4:7], v[174:177], v[210:213], v[4:7]
	s_setprio 0
	s_add_i32 s60, s60, 2
	s_add_u32 s16, s16, 0x100
	s_addc_u32 s17, s17, 0
	s_add_u32 s50, s50, 0x100
	s_addc_u32 s51, s51, 0
	s_cmp_gt_u32 s60, 5
	s_barrier
	s_cbranch_scc0 .LBB0_2018
	s_and_b64 vcc, exec, s[28:29]
	s_cbranch_vccz .LBB0_2021
	s_barrier

; #define PG8_STAGE(bufoff, gbase, voff) do { _Pragma("unroll") for (int _i = 0; _i < 2; ++_i) \
;         __builtin_amdgcn_global_load_lds((const unsigned*)((const char*)(gbase) + (voff)[_i]), (PG8_LAS unsigned*)(lds + (bufoff) + ldsw + _i * 8192), 16, 0, 0); } while (0)
; #define PG8_STAGE_A(bufoff, gbase, h, nx) do { _Pragma("unroll") for (int _i = 0; _i < 2; ++_i) { \
;         const unsigned vo_ = GA ? ((nx) ? vgn[h][_i] : vgc[h][_i]) : voffA[_i]; \
;         __builtin_amdgcn_global_load_lds((const unsigned*)((const char*)(gbase) + vo_), (PG8_LAS unsigned*)(lds + (bufoff) + ldsw + _i * 8192), 16, 0, 0); } } while (0)
; #define PG8_LDA(dst, b, h) do { _Pragma("unroll") for (int m = 0; m < 4; ++m) _Pragma("unroll") for (int k = 0; k < 2; ++k) dst[m][k] = *(const PG8_LAS bf16x8*)(lds + PG8_SA(b, h) + aoff + m * 2048 + k * 1024); } while (0)
; #define PG8_LDB(dst, b, h) do { _Pragma("unroll") for (int n = 0; n < 2; ++n) _Pragma("unroll") for (int k = 0; k < 2; ++k) dst[n][k] = *(const PG8_LAS bf16x8*)(lds + PG8_SB(b, h) + boff + n * 2048 + k * 1024); } while (0)
; #define PG8_WAIT_V(n) asm volatile("s_waitcnt vmcnt(" #n ")" ::: "memory")
; #define PG8_WAIT_L(n) asm volatile("s_waitcnt lgkmcnt(" #n ")" ::: "memory")
; #define PG8_BAR __builtin_amdgcn_s_barrier()
; #define PG8_SCHED __builtin_amdgcn_sched_barrier(0)
; template <class Epi, class Sched>
; __device__ __forceinline__ void gemm_phase(const int WID_, PG8_LAS unsigned char* lds, const Sched& S, const Epi& E) {
;     ...
;         for (int t = 0; t < nt; t += 2) {
;             const bool last = (t == nt - 2);
;             const char* a1 = cA + (size_t)(t + 1) * kstep;
;             const char* a2 = last ? nA : cA + (size_t)(t + 2) * kstep; const char* b2 = last ? nB : cB + (size_t)(t + 2) * kstep;
;             const char* a3 = a2 + kstep; const char* b3 = b2 + kstep;
;             PG8_LDB(B0, 0, 0); PG8_LDB(B1, 0, 1); PG8_SCHED; PG8_LDA(At, 0, 0); PG8_STAGE_A(PG8_SA(1, 1), a1 + hstepA, 1, false);
;             PG8_WAIT_V(8); PG8_WAIT_L(0); PG8_BAR; PG8_MMA(0, 0, At, B0); PG8_MMA(0, 1, At, B1); PG8_BAR; PG8_SCHED;
;             PG8_LDA(At, 0, 1); PG8_STAGE(PG8_SB(0, 0), b2, voffB); PG8_STAGE(PG8_SB(0, 1), b2 + hstepB, voffB); PG8_STAGE_A(PG8_SA(0, 0), a2, 0, last);
;             PG8_WAIT_V(8); PG8_WAIT_L(0); PG8_BAR; PG8_MMA(1, 0, At, B0); PG8_MMA(1, 1, At, B1); PG8_BAR; PG8_SCHED;
.LBB0_2036:
	v_add_u32_e32 v149, s43, v145
	ds_read_b128 v[140:143], v149
	ds_read_b128 v[150:153], v149 offset:1024
	ds_read_b128 v[154:157], v149 offset:2048
	ds_read_b128 v[158:161], v149 offset:3072
	v_add_u32_e32 v149, s67, v145
	ds_read_b128 v[162:165], v149
	ds_read_b128 v[166:169], v149 offset:1024
	ds_read_b128 v[170:173], v149 offset:2048
	ds_read_b128 v[174:177], v149 offset:3072
	s_add_u32 s20, s18, 0xfffc0080
	s_addc_u32 s21, s19, -1
	s_cmp_eq_u32 s63, 12
	s_cselect_b32 s23, s13, s21
	s_cselect_b32 s22, s12, s20
	s_cselect_b32 s21, s15, s11
	s_cselect_b32 s20, s14, s9
	v_lshl_add_u64 v[214:215], s[18:19], 0, v[136:137]
	s_add_i32 m0, s44, 0xc000
	ds_read_b128 v[178:181], v148
	ds_read_b128 v[182:185], v148 offset:1024
	ds_read_b128 v[186:189], v148 offset:2048
	ds_read_b128 v[190:193], v148 offset:3072
	ds_read_b128 v[198:201], v148 offset:4096
	ds_read_b128 v[202:205], v148 offset:5120
	ds_read_b128 v[206:209], v148 offset:6144
	ds_read_b128 v[210:213], v148 offset:7168
	global_load_lds_dwordx4 v[214:215], off
	v_lshl_add_u64 v[214:215], s[18:19], 0, v[138:139]
	s_add_i32 m0, s44, 0xe000
	s_nop 0
	global_load_lds_dwordx4 v[214:215], off
	s_waitcnt vmcnt(8)
	s_waitcnt lgkmcnt(0)
	s_barrier
	s_setprio 1
	s_waitcnt lgkmcnt(0)
	v_mfma_f32_16x16x32_bf16 v[124:127], v[140:143], v[178:181], v[124:127]
	v_mfma_f32_16x16x32_bf16 v[120:123], v[154:157], v[178:181], v[120:123]
	v_mfma_f32_16x16x32_bf16 v[108:111], v[140:143], v[186:189], v[108:111]
	v_mfma_f32_16x16x32_bf16 v[104:107], v[154:157], v[186:189], v[104:107]
	v_mfma_f32_16x16x32_bf16 v[92:95], v[140:143], v[198:201], v[92:95]
	v_mfma_f32_16x16x32_bf16 v[88:91], v[154:157], v[198:201], v[88:91]
	v_mfma_f32_16x16x32_bf16 v[76:79], v[140:143], v[206:209], v[76:79]
	v_mfma_f32_16x16x32_bf16 v[72:75], v[154:157], v[206:209], v[72:75]
	v_mfma_f32_16x16x32_bf16 v[124:127], v[150:153], v[182:185], v[124:127]
	v_mfma_f32_16x16x32_bf16 v[120:123], v[158:161], v[182:185], v[120:123]
	v_mfma_f32_16x16x32_bf16 v[108:111], v[150:153], v[190:193], v[108:111]
	v_mfma_f32_16x16x32_bf16 v[104:107], v[158:161], v[190:193], v[104:107]
	v_mfma_f32_16x16x32_bf16 v[92:95], v[150:153], v[202:205], v[92:95]
	v_mfma_f32_16x16x32_bf16 v[88:91], v[158:161], v[202:205], v[88:91]
	v_mfma_f32_16x16x32_bf16 v[76:79], v[150:153], v[210:213], v[76:79]
	v_mfma_f32_16x16x32_bf16 v[72:75], v[158:161], v[210:213], v[72:75]
	s_setprio 0
	s_setprio 1
	v_mfma_f32_16x16x32_bf16 v[116:119], v[162:165], v[178:181], v[116:119]
	v_mfma_f32_16x16x32_bf16 v[112:115], v[170:173], v[178:181], v[112:115]
	v_mfma_f32_16x16x32_bf16 v[100:103], v[162:165], v[186:189], v[100:103]
	v_mfma_f32_16x16x32_bf16 v[96:99], v[170:173], v[186:189], v[96:99]
	v_mfma_f32_16x16x32_bf16 v[84:87], v[162:165], v[198:201], v[84:87]
	v_mfma_f32_16x16x32_bf16 v[80:83], v[170:173], v[198:201], v[80:83]
	v_mfma_f32_16x16x32_bf16 v[68:71], v[162:165], v[206:209], v[68:71]
	v_mfma_f32_16x16x32_bf16 v[64:67], v[170:173], v[206:209], v[64:67]
	v_mfma_f32_16x16x32_bf16 v[116:119], v[166:169], v[182:185], v[116:119]
	v_mfma_f32_16x16x32_bf16 v[112:115], v[174:177], v[182:185], v[112:115]
	v_mfma_f32_16x16x32_bf16 v[100:103], v[166:169], v[190:193], v[100:103]
	v_mfma_f32_16x16x32_bf16 v[96:99], v[174:177], v[190:193], v[96:99]
	v_mfma_f32_16x16x32_bf16 v[84:87], v[166:169], v[202:205], v[84:87]
	v_mfma_f32_16x16x32_bf16 v[80:83], v[174:177], v[202:205], v[80:83]
	v_mfma_f32_16x16x32_bf16 v[68:71], v[166:169], v[210:213], v[68:71]
	v_mfma_f32_16x16x32_bf16 v[64:67], v[174:177], v[210:213], v[64:67]
	s_setprio 0
	s_barrier
	s_add_i32 s46, s43, s33
	v_lshl_add_u64 v[214:215], s[20:21], 0, v[128:129]
	s_mov_b32 m0, s46
	ds_read_b128 v[178:181], v148 offset:16384
	ds_read_b128 v[182:185], v148 offset:17408
	ds_read_b128 v[186:189], v148 offset:18432
	ds_read_b128 v[190:193], v148 offset:19456
	ds_read_b128 v[198:201], v148 offset:20480
	ds_read_b128 v[202:205], v148 offset:21504
	ds_read_b128 v[206:209], v148 offset:22528
	ds_read_b128 v[210:213], v148 offset:23552
	global_load_lds_dwordx4 v[214:215], off
	s_add_i32 m0, s46, 0x2000
	s_add_u32 s78, s20, 0x40000
	v_lshl_add_u64 v[216:217], s[20:21], 0, v[134:135]
	s_addc_u32 s79, s21, 0
	s_add_i32 s46, s67, s33
	global_load_lds_dwordx4 v[216:217], off
	v_lshl_add_u64 v[218:219], s[78:79], 0, v[128:129]
	s_mov_b32 m0, s46
	v_lshl_add_u64 v[220:221], s[22:23], 0, v[132:133]
	global_load_lds_dwordx4 v[218:219], off
	v_lshl_add_u64 v[218:219], s[78:79], 0, v[134:135]
	s_add_i32 m0, s46, 0x2000
	s_nop 0
	global_load_lds_dwordx4 v[218:219], off
	v_lshl_add_u64 v[218:219], s[22:23], 0, v[130:131]
	s_mov_b32 m0, s44
	s_nop 0
	global_load_lds_dwordx4 v[218:219], off
	s_mov_b32 m0, s48
	s_nop 0
	global_load_lds_dwordx4 v[220:221], off
	s_waitcnt vmcnt(8)
	s_waitcnt lgkmcnt(0)
	s_barrier
; #define PG8_STAGE_A(bufoff, gbase, h, nx) do { _Pragma("unroll") for (int _i = 0; _i < 2; ++_i) { \
;         const unsigned vo_ = GA ? ((nx) ? vgn[h][_i] : vgc[h][_i]) : voffA[_i]; \
;         __builtin_amdgcn_global_load_lds((const unsigned*)((const char*)(gbase) + vo_), (PG8_LAS unsigned*)(lds + (bufoff) + ldsw + _i * 8192), 16, 0, 0); } } while (0)
; #define PG8_LDA(dst, b, h) do { _Pragma("unroll") for (int m = 0; m < 4; ++m) _Pragma("unroll") for (int k = 0; k < 2; ++k) dst[m][k] = *(const PG8_LAS bf16x8*)(lds + PG8_SA(b, h) + aoff + m * 2048 + k * 1024); } while (0)
; #define PG8_LDB(dst, b, h) do { _Pragma("unroll") for (int n = 0; n < 2; ++n) _Pragma("unroll") for (int k = 0; k < 2; ++k) dst[n][k] = *(const PG8_LAS bf16x8*)(lds + PG8_SB(b, h) + boff + n * 2048 + k * 1024); } while (0)
; #define PG8_MMA(ai, bj, At, Bt) do { __builtin_amdgcn_s_setprio(1); _Pragma("unroll") for (int m = 0; m < 4; ++m) _Pragma("unroll") for (int n = 0; n < 2; ++n) _Pragma("unroll") for (int k = 0; k < 2; ++k) \
;         acc[ai][bj][m][n] = __builtin_amdgcn_mfma_f32_16x16x32_bf16(Bt[n][k], At[m][k], acc[ai][bj][m][n], 0, 0, 0); __builtin_amdgcn_s_setprio(0); } while (0)
; #define PG8_WAIT_V(n) asm volatile("s_waitcnt vmcnt(" #n ")" ::: "memory")
; #define PG8_WAIT_L(n) asm volatile("s_waitcnt lgkmcnt(" #n ")" ::: "memory")
; #define PG8_BAR __builtin_amdgcn_s_barrier()
; #define PG8_SCHED __builtin_amdgcn_sched_barrier(0)
; template <class Epi, class Sched>
; __device__ __forceinline__ void gemm_phase(const int WID_, PG8_LAS unsigned char* lds, const Sched& S, const Epi& E) {
;     ...
;             PG8_WAIT_V(8); PG8_WAIT_L(0); PG8_BAR; PG8_MMA(1, 0, At, B0); PG8_MMA(1, 1, At, B1); PG8_BAR; PG8_SCHED;
;             PG8_LDB(B0, 1, 0); PG8_LDB(B1, 1, 1); PG8_SCHED; PG8_LDA(At, 1, 0); PG8_STAGE_A(PG8_SA(0, 1), a2 + hstepA, 1, last);
;             PG8_WAIT_V(8); PG8_WAIT_L(0); PG8_BAR; PG8_MMA(0, 0, At, B0); PG8_MMA(0, 1, At, B1); PG8_BAR; PG8_SCHED;
	s_setprio 1
	s_waitcnt lgkmcnt(0)
	v_mfma_f32_16x16x32_bf16 v[60:63], v[140:143], v[178:181], v[60:63]
	v_mfma_f32_16x16x32_bf16 v[56:59], v[154:157], v[178:181], v[56:59]
	v_mfma_f32_16x16x32_bf16 v[44:47], v[140:143], v[186:189], v[44:47]
	v_mfma_f32_16x16x32_bf16 v[40:43], v[154:157], v[186:189], v[40:43]
	v_mfma_f32_16x16x32_bf16 v[28:31], v[140:143], v[198:201], v[28:31]
	v_mfma_f32_16x16x32_bf16 v[24:27], v[154:157], v[198:201], v[24:27]
	v_mfma_f32_16x16x32_bf16 v[12:15], v[140:143], v[206:209], v[12:15]
	v_mfma_f32_16x16x32_bf16 v[8:11], v[154:157], v[206:209], v[8:11]
	v_mfma_f32_16x16x32_bf16 v[60:63], v[150:153], v[182:185], v[60:63]
	v_mfma_f32_16x16x32_bf16 v[56:59], v[158:161], v[182:185], v[56:59]
	v_mfma_f32_16x16x32_bf16 v[44:47], v[150:153], v[190:193], v[44:47]
	v_mfma_f32_16x16x32_bf16 v[40:43], v[158:161], v[190:193], v[40:43]
	v_mfma_f32_16x16x32_bf16 v[28:31], v[150:153], v[202:205], v[28:31]
	v_mfma_f32_16x16x32_bf16 v[24:27], v[158:161], v[202:205], v[24:27]
	v_mfma_f32_16x16x32_bf16 v[12:15], v[150:153], v[210:213], v[12:15]
	v_mfma_f32_16x16x32_bf16 v[8:11], v[158:161], v[210:213], v[8:11]
	s_setprio 0
	s_setprio 1
	v_mfma_f32_16x16x32_bf16 v[52:55], v[162:165], v[178:181], v[52:55]
	v_mfma_f32_16x16x32_bf16 v[48:51], v[170:173], v[178:181], v[48:51]
	v_mfma_f32_16x16x32_bf16 v[36:39], v[162:165], v[186:189], v[36:39]
	v_mfma_f32_16x16x32_bf16 v[32:35], v[170:173], v[186:189], v[32:35]
	v_mfma_f32_16x16x32_bf16 v[20:23], v[162:165], v[198:201], v[20:23]
	v_mfma_f32_16x16x32_bf16 v[16:19], v[170:173], v[198:201], v[16:19]
	v_mfma_f32_16x16x32_bf16 v[4:7], v[162:165], v[206:209], v[4:7]
	v_mfma_f32_16x16x32_bf16 v[0:3], v[170:173], v[206:209], v[0:3]
	v_mfma_f32_16x16x32_bf16 v[52:55], v[166:169], v[182:185], v[52:55]
	v_mfma_f32_16x16x32_bf16 v[48:51], v[174:177], v[182:185], v[48:51]
	v_mfma_f32_16x16x32_bf16 v[36:39], v[166:169], v[190:193], v[36:39]
	v_mfma_f32_16x16x32_bf16 v[32:35], v[174:177], v[190:193], v[32:35]
	v_mfma_f32_16x16x32_bf16 v[20:23], v[166:169], v[202:205], v[20:23]
	v_mfma_f32_16x16x32_bf16 v[16:19], v[174:177], v[202:205], v[16:19]
	v_mfma_f32_16x16x32_bf16 v[4:7], v[166:169], v[210:213], v[4:7]
	v_mfma_f32_16x16x32_bf16 v[0:3], v[174:177], v[210:213], v[0:3]
	s_setprio 0
	s_barrier
	v_add_u32_e32 v149, s82, v145
	ds_read_b128 v[140:143], v149
	ds_read_b128 v[150:153], v149 offset:1024
	ds_read_b128 v[154:157], v149 offset:2048
	ds_read_b128 v[158:161], v149 offset:3072
	v_add_u32_e32 v149, s83, v145
	ds_read_b128 v[162:165], v149
	ds_read_b128 v[166:169], v149 offset:1024
	ds_read_b128 v[170:173], v149 offset:2048
	ds_read_b128 v[174:177], v149 offset:3072
	s_add_u32 s22, s22, 0x40000
	s_addc_u32 s23, s23, 0
	s_mov_b32 m0, s49
	v_lshl_add_u64 v[222:223], s[22:23], 0, v[130:131]
	ds_read_b128 v[178:181], v148 offset:32768
	ds_read_b128 v[182:185], v148 offset:33792
	ds_read_b128 v[186:189], v148 offset:34816
	ds_read_b128 v[190:193], v148 offset:35840
	ds_read_b128 v[198:201], v148 offset:36864
	ds_read_b128 v[202:205], v148 offset:37888
	ds_read_b128 v[206:209], v148 offset:38912
	ds_read_b128 v[210:213], v148 offset:39936
	global_load_lds_dwordx4 v[222:223], off
	v_lshl_add_u64 v[222:223], s[22:23], 0, v[132:133]
	s_mov_b32 m0, s50
	s_nop 0
	global_load_lds_dwordx4 v[222:223], off
	s_waitcnt vmcnt(8)
	s_waitcnt lgkmcnt(0)
	s_barrier
	s_setprio 1
	s_waitcnt lgkmcnt(0)
	v_mfma_f32_16x16x32_bf16 v[124:127], v[140:143], v[178:181], v[124:127]
	v_mfma_f32_16x16x32_bf16 v[120:123], v[154:157], v[178:181], v[120:123]
	v_mfma_f32_16x16x32_bf16 v[108:111], v[140:143], v[186:189], v[108:111]
	v_mfma_f32_16x16x32_bf16 v[104:107], v[154:157], v[186:189], v[104:107]
	v_mfma_f32_16x16x32_bf16 v[92:95], v[140:143], v[198:201], v[92:95]
	v_mfma_f32_16x16x32_bf16 v[88:91], v[154:157], v[198:201], v[88:91]
	v_mfma_f32_16x16x32_bf16 v[76:79], v[140:143], v[206:209], v[76:79]
	v_mfma_f32_16x16x32_bf16 v[72:75], v[154:157], v[206:209], v[72:75]
	v_mfma_f32_16x16x32_bf16 v[124:127], v[150:153], v[182:185], v[124:127]
	v_mfma_f32_16x16x32_bf16 v[120:123], v[158:161], v[182:185], v[120:123]
	v_mfma_f32_16x16x32_bf16 v[108:111], v[150:153], v[190:193], v[108:111]
	v_mfma_f32_16x16x32_bf16 v[104:107], v[158:161], v[190:193], v[104:107]
	v_mfma_f32_16x16x32_bf16 v[92:95], v[150:153], v[202:205], v[92:95]
	v_mfma_f32_16x16x32_bf16 v[88:91], v[158:161], v[202:205], v[88:91]
	v_mfma_f32_16x16x32_bf16 v[76:79], v[150:153], v[210:213], v[76:79]
	v_mfma_f32_16x16x32_bf16 v[72:75], v[158:161], v[210:213], v[72:75]
	s_setprio 0
	s_setprio 1
	v_mfma_f32_16x16x32_bf16 v[116:119], v[162:165], v[178:181], v[116:119]
	v_mfma_f32_16x16x32_bf16 v[112:115], v[170:173], v[178:181], v[112:115]
	v_mfma_f32_16x16x32_bf16 v[100:103], v[162:165], v[186:189], v[100:103]
	v_mfma_f32_16x16x32_bf16 v[96:99], v[170:173], v[186:189], v[96:99]
	v_mfma_f32_16x16x32_bf16 v[84:87], v[162:165], v[198:201], v[84:87]
	v_mfma_f32_16x16x32_bf16 v[80:83], v[170:173], v[198:201], v[80:83]
	v_mfma_f32_16x16x32_bf16 v[68:71], v[162:165], v[206:209], v[68:71]
	v_mfma_f32_16x16x32_bf16 v[64:67], v[170:173], v[206:209], v[64:67]
	v_mfma_f32_16x16x32_bf16 v[116:119], v[166:169], v[182:185], v[116:119]
	v_mfma_f32_16x16x32_bf16 v[112:115], v[174:177], v[182:185], v[112:115]
	v_mfma_f32_16x16x32_bf16 v[100:103], v[166:169], v[190:193], v[100:103]
	v_mfma_f32_16x16x32_bf16 v[96:99], v[174:177], v[190:193], v[96:99]
	v_mfma_f32_16x16x32_bf16 v[84:87], v[166:169], v[202:205], v[84:87]
	v_mfma_f32_16x16x32_bf16 v[80:83], v[174:177], v[202:205], v[80:83]
	v_mfma_f32_16x16x32_bf16 v[68:71], v[166:169], v[210:213], v[68:71]
	v_mfma_f32_16x16x32_bf16 v[64:67], v[174:177], v[210:213], v[64:67]
	s_setprio 0
	s_barrier
; #define PG8_STAGE(bufoff, gbase, voff) do { _Pragma("unroll") for (int _i = 0; _i < 2; ++_i) \
;         __builtin_amdgcn_global_load_lds((const unsigned*)((const char*)(gbase) + (voff)[_i]), (PG8_LAS unsigned*)(lds + (bufoff) + ldsw + _i * 8192), 16, 0, 0); } while (0)
; #define PG8_STAGE_A(bufoff, gbase, h, nx) do { _Pragma("unroll") for (int _i = 0; _i < 2; ++_i) { \
;         const unsigned vo_ = GA ? ((nx) ? vgn[h][_i] : vgc[h][_i]) : voffA[_i]; \
;         __builtin_amdgcn_global_load_lds((const unsigned*)((const char*)(gbase) + vo_), (PG8_LAS unsigned*)(lds + (bufoff) + ldsw + _i * 8192), 16, 0, 0); } } while (0)
; #define PG8_LDA(dst, b, h) do { _Pragma("unroll") for (int m = 0; m < 4; ++m) _Pragma("unroll") for (int k = 0; k < 2; ++k) dst[m][k] = *(const PG8_LAS bf16x8*)(lds + PG8_SA(b, h) + aoff + m * 2048 + k * 1024); } while (0)
; #define PG8_MMA(ai, bj, At, Bt) do { __builtin_amdgcn_s_setprio(1); _Pragma("unroll") for (int m = 0; m < 4; ++m) _Pragma("unroll") for (int n = 0; n < 2; ++n) _Pragma("unroll") for (int k = 0; k < 2; ++k) \
;         acc[ai][bj][m][n] = __builtin_amdgcn_mfma_f32_16x16x32_bf16(Bt[n][k], At[m][k], acc[ai][bj][m][n], 0, 0, 0); __builtin_amdgcn_s_setprio(0); } while (0)
; #define PG8_WAIT_V(n) asm volatile("s_waitcnt vmcnt(" #n ")" ::: "memory")
; #define PG8_WAIT_L(n) asm volatile("s_waitcnt lgkmcnt(" #n ")" ::: "memory")
; #define PG8_BAR __builtin_amdgcn_s_barrier()
; #define PG8_SCHED __builtin_amdgcn_sched_barrier(0)
; template <class Epi, class Sched>
; __device__ __forceinline__ void gemm_phase(const int WID_, PG8_LAS unsigned char* lds, const Sched& S, const Epi& E) {
;     ...
;             PG8_LDA(At, 1, 1); PG8_STAGE(PG8_SB(1, 0), b3, voffB); PG8_STAGE(PG8_SB(1, 1), b3 + hstepB, voffB); PG8_STAGE_A(PG8_SA(1, 0), a3, 0, last);
;             PG8_WAIT_V(8); PG8_WAIT_L(0); PG8_BAR; PG8_MMA(1, 0, At, B0); PG8_MMA(1, 1, At, B1); PG8_BAR; PG8_SCHED;
;         }
;         if (wr == 0) PG8_BAR;
	s_add_i32 s22, s82, s33
	v_lshl_add_u64 v[214:215], v[214:215], 0, s[68:69]
	s_mov_b32 m0, s22
	ds_read_b128 v[178:181], v148 offset:49152
	ds_read_b128 v[182:185], v148 offset:50176
	ds_read_b128 v[186:189], v148 offset:51200
	ds_read_b128 v[190:193], v148 offset:52224
	ds_read_b128 v[198:201], v148 offset:53248
	ds_read_b128 v[202:205], v148 offset:54272
	ds_read_b128 v[206:209], v148 offset:55296
	ds_read_b128 v[210:213], v148 offset:56320
	global_load_lds_dwordx4 v[214:215], off
	s_add_i32 m0, s22, 0x2000
	s_add_u32 s20, s20, 0x40080
	v_lshl_add_u64 v[214:215], v[216:217], 0, s[68:69]
	s_addc_u32 s21, s21, 0
	s_add_i32 s22, s83, s33
	global_load_lds_dwordx4 v[214:215], off
	v_lshl_add_u64 v[214:215], s[20:21], 0, v[128:129]
	s_mov_b32 m0, s22
	s_nop 0
	global_load_lds_dwordx4 v[214:215], off
	v_lshl_add_u64 v[214:215], s[20:21], 0, v[134:135]
	s_add_i32 m0, s22, 0x2000
	s_nop 0
	global_load_lds_dwordx4 v[214:215], off
	v_lshl_add_u64 v[214:215], v[218:219], 0, s[68:69]
	s_mov_b32 m0, s51
	s_nop 0
	global_load_lds_dwordx4 v[214:215], off
	v_lshl_add_u64 v[214:215], v[220:221], 0, s[68:69]
	s_mov_b32 m0, s60
	s_nop 0
	global_load_lds_dwordx4 v[214:215], off
	s_waitcnt vmcnt(8)
	s_waitcnt lgkmcnt(0)
	s_barrier
	s_setprio 1
	s_waitcnt lgkmcnt(0)
	v_mfma_f32_16x16x32_bf16 v[60:63], v[140:143], v[178:181], v[60:63]
	v_mfma_f32_16x16x32_bf16 v[56:59], v[154:157], v[178:181], v[56:59]
	v_mfma_f32_16x16x32_bf16 v[44:47], v[140:143], v[186:189], v[44:47]
	v_mfma_f32_16x16x32_bf16 v[40:43], v[154:157], v[186:189], v[40:43]
	v_mfma_f32_16x16x32_bf16 v[28:31], v[140:143], v[198:201], v[28:31]
	v_mfma_f32_16x16x32_bf16 v[24:27], v[154:157], v[198:201], v[24:27]
	v_mfma_f32_16x16x32_bf16 v[12:15], v[140:143], v[206:209], v[12:15]
	v_mfma_f32_16x16x32_bf16 v[8:11], v[154:157], v[206:209], v[8:11]
	v_mfma_f32_16x16x32_bf16 v[60:63], v[150:153], v[182:185], v[60:63]
	v_mfma_f32_16x16x32_bf16 v[56:59], v[158:161], v[182:185], v[56:59]
	v_mfma_f32_16x16x32_bf16 v[44:47], v[150:153], v[190:193], v[44:47]
	v_mfma_f32_16x16x32_bf16 v[40:43], v[158:161], v[190:193], v[40:43]
	v_mfma_f32_16x16x32_bf16 v[28:31], v[150:153], v[202:205], v[28:31]
	v_mfma_f32_16x16x32_bf16 v[24:27], v[158:161], v[202:205], v[24:27]
	v_mfma_f32_16x16x32_bf16 v[12:15], v[150:153], v[210:213], v[12:15]
	v_mfma_f32_16x16x32_bf16 v[8:11], v[158:161], v[210:213], v[8:11]
	s_setprio 0
	s_setprio 1
	v_mfma_f32_16x16x32_bf16 v[52:55], v[162:165], v[178:181], v[52:55]
	v_mfma_f32_16x16x32_bf16 v[48:51], v[170:173], v[178:181], v[48:51]
	v_mfma_f32_16x16x32_bf16 v[36:39], v[162:165], v[186:189], v[36:39]
	v_mfma_f32_16x16x32_bf16 v[32:35], v[170:173], v[186:189], v[32:35]
	v_mfma_f32_16x16x32_bf16 v[20:23], v[162:165], v[198:201], v[20:23]
	v_mfma_f32_16x16x32_bf16 v[16:19], v[170:173], v[198:201], v[16:19]
	v_mfma_f32_16x16x32_bf16 v[4:7], v[162:165], v[206:209], v[4:7]
	v_mfma_f32_16x16x32_bf16 v[0:3], v[170:173], v[206:209], v[0:3]
	v_mfma_f32_16x16x32_bf16 v[52:55], v[166:169], v[182:185], v[52:55]
	v_mfma_f32_16x16x32_bf16 v[48:51], v[174:177], v[182:185], v[48:51]
	v_mfma_f32_16x16x32_bf16 v[36:39], v[166:169], v[190:193], v[36:39]
	v_mfma_f32_16x16x32_bf16 v[32:35], v[174:177], v[190:193], v[32:35]
	v_mfma_f32_16x16x32_bf16 v[20:23], v[166:169], v[202:205], v[20:23]
	v_mfma_f32_16x16x32_bf16 v[16:19], v[174:177], v[202:205], v[16:19]
	v_mfma_f32_16x16x32_bf16 v[4:7], v[166:169], v[210:213], v[4:7]
	v_mfma_f32_16x16x32_bf16 v[0:3], v[174:177], v[210:213], v[0:3]
	s_setprio 0
	s_add_i32 s63, s63, 2
	s_add_u32 s18, s18, 0x100
	s_addc_u32 s19, s19, 0
	s_add_u32 s9, s9, 0x100
	s_addc_u32 s11, s11, 0
	s_cmp_gt_u32 s63, 13
	s_barrier
	s_cbranch_scc0 .LBB0_2036
	s_and_b64 vcc, exec, s[6:7]
	s_cbranch_vccz .LBB0_2039
	s_barrier

; #define PG8_STAGE(bufoff, gbase, voff) do { _Pragma("unroll") for (int _i = 0; _i < 2; ++_i) \
;         __builtin_amdgcn_global_load_lds((const unsigned*)((const char*)(gbase) + (voff)[_i]), (PG8_LAS unsigned*)(lds + (bufoff) + ldsw + _i * 8192), 16, 0, 0); } while (0)
; #define PG8_STAGE_A(bufoff, gbase, h, nx) do { _Pragma("unroll") for (int _i = 0; _i < 2; ++_i) { \
;         const unsigned vo_ = GA ? ((nx) ? vgn[h][_i] : vgc[h][_i]) : voffA[_i]; \
;         __builtin_amdgcn_global_load_lds((const unsigned*)((const char*)(gbase) + vo_), (PG8_LAS unsigned*)(lds + (bufoff) + ldsw + _i * 8192), 16, 0, 0); } } while (0)
; #define PG8_LDA(dst, b, h) do { _Pragma("unroll") for (int m = 0; m < 4; ++m) _Pragma("unroll") for (int k = 0; k < 2; ++k) dst[m][k] = *(const PG8_LAS bf16x8*)(lds + PG8_SA(b, h) + aoff + m * 2048 + k * 1024); } while (0)
; #define PG8_LDB(dst, b, h) do { _Pragma("unroll") for (int n = 0; n < 2; ++n) _Pragma("unroll") for (int k = 0; k < 2; ++k) dst[n][k] = *(const PG8_LAS bf16x8*)(lds + PG8_SB(b, h) + boff + n * 2048 + k * 1024); } while (0)
; #define PG8_WAIT_V(n) asm volatile("s_waitcnt vmcnt(" #n ")" ::: "memory")
; #define PG8_WAIT_L(n) asm volatile("s_waitcnt lgkmcnt(" #n ")" ::: "memory")
; #define PG8_BAR __builtin_amdgcn_s_barrier()
; #define PG8_SCHED __builtin_amdgcn_sched_barrier(0)
; template <class Epi, class Sched>
; __device__ __forceinline__ void gemm_phase(const int WID_, PG8_LAS unsigned char* lds, const Sched& S, const Epi& E) {
;     ...
;         for (int t = 0; t < nt; t += 2) {
;             const bool last = (t == nt - 2);
;             const char* a1 = cA + (size_t)(t + 1) * kstep;
;             const char* a2 = last ? nA : cA + (size_t)(t + 2) * kstep; const char* b2 = last ? nB : cB + (size_t)(t + 2) * kstep;
;             const char* a3 = a2 + kstep; const char* b3 = b2 + kstep;
;             PG8_LDB(B0, 0, 0); PG8_LDB(B1, 0, 1); PG8_SCHED; PG8_LDA(At, 0, 0); PG8_STAGE_A(PG8_SA(1, 1), a1 + hstepA, 1, false);
;             PG8_WAIT_V(8); PG8_WAIT_L(0); PG8_BAR; PG8_MMA(0, 0, At, B0); PG8_MMA(0, 1, At, B1); PG8_BAR; PG8_SCHED;
;             PG8_LDA(At, 0, 1); PG8_STAGE(PG8_SB(0, 0), b2, voffB); PG8_STAGE(PG8_SB(0, 1), b2 + hstepB, voffB); PG8_STAGE_A(PG8_SA(0, 0), a2, 0, last);
;             PG8_WAIT_V(8); PG8_WAIT_L(0); PG8_BAR; PG8_MMA(1, 0, At, B0); PG8_MMA(1, 1, At, B1); PG8_BAR; PG8_SCHED;
.LBB0_2070:
	v_add_u32_e32 v152, s43, v199
	v_add_u32_e32 v168, s67, v199
	ds_read_b128 v[140:143], v152
	ds_read_b128 v[144:147], v152 offset:1024
	ds_read_b128 v[148:151], v152 offset:2048
	ds_read_b128 v[152:155], v152 offset:3072
	ds_read_b128 v[156:159], v168
	ds_read_b128 v[160:163], v168 offset:1024
	ds_read_b128 v[164:167], v168 offset:2048
	ds_read_b128 v[168:171], v168 offset:3072
	s_add_u32 s46, s22, 0xfffc0080
	s_addc_u32 s47, s23, -1
	s_cmp_eq_u32 vcc_lo, 12
	s_cselect_b32 s81, s17, s47
	s_cselect_b32 s80, s16, s46
	s_cselect_b32 s79, s19, s15
	s_cselect_b32 s78, s18, s13
	v_lshl_add_u64 v[192:193], s[22:23], 0, v[136:137]
	s_add_i32 m0, s51, 0xc000
	ds_read_b128 v[172:175], v219
	ds_read_b128 v[176:179], v219 offset:1024
	ds_read_b128 v[180:183], v219 offset:2048
	ds_read_b128 v[184:187], v219 offset:3072
	ds_read_b128 v[188:191], v219 offset:4096
	ds_read_b128 v[222:225], v219 offset:5120
	ds_read_b128 v[226:229], v219 offset:6144
	ds_read_b128 v[230:233], v219 offset:7168
	global_load_lds_dwordx4 v[192:193], off
	v_lshl_add_u64 v[192:193], s[22:23], 0, v[138:139]
	s_add_i32 m0, s51, 0xe000
	s_nop 0
	global_load_lds_dwordx4 v[192:193], off
	s_waitcnt vmcnt(8)
	s_waitcnt lgkmcnt(0)
	s_barrier
	s_setprio 1
	s_waitcnt lgkmcnt(0)
	v_mfma_f32_16x16x32_bf16 v[124:127], v[140:143], v[172:175], v[124:127]
	v_mfma_f32_16x16x32_bf16 v[120:123], v[148:151], v[172:175], v[120:123]
	v_mfma_f32_16x16x32_bf16 v[108:111], v[140:143], v[180:183], v[108:111]
	v_mfma_f32_16x16x32_bf16 v[104:107], v[148:151], v[180:183], v[104:107]
	v_mfma_f32_16x16x32_bf16 v[92:95], v[140:143], v[188:191], v[92:95]
	v_mfma_f32_16x16x32_bf16 v[88:91], v[148:151], v[188:191], v[88:91]
	v_mfma_f32_16x16x32_bf16 v[76:79], v[140:143], v[226:229], v[76:79]
	v_mfma_f32_16x16x32_bf16 v[72:75], v[148:151], v[226:229], v[72:75]
	v_mfma_f32_16x16x32_bf16 v[124:127], v[144:147], v[176:179], v[124:127]
	v_mfma_f32_16x16x32_bf16 v[120:123], v[152:155], v[176:179], v[120:123]
	v_mfma_f32_16x16x32_bf16 v[108:111], v[144:147], v[184:187], v[108:111]
	v_mfma_f32_16x16x32_bf16 v[104:107], v[152:155], v[184:187], v[104:107]
	v_mfma_f32_16x16x32_bf16 v[92:95], v[144:147], v[222:225], v[92:95]
	v_mfma_f32_16x16x32_bf16 v[88:91], v[152:155], v[222:225], v[88:91]
	v_mfma_f32_16x16x32_bf16 v[76:79], v[144:147], v[230:233], v[76:79]
	v_mfma_f32_16x16x32_bf16 v[72:75], v[152:155], v[230:233], v[72:75]
	s_setprio 0
	s_setprio 1
	v_mfma_f32_16x16x32_bf16 v[116:119], v[156:159], v[172:175], v[116:119]
	v_mfma_f32_16x16x32_bf16 v[112:115], v[164:167], v[172:175], v[112:115]
	v_mfma_f32_16x16x32_bf16 v[100:103], v[156:159], v[180:183], v[100:103]
	v_mfma_f32_16x16x32_bf16 v[96:99], v[164:167], v[180:183], v[96:99]
	v_mfma_f32_16x16x32_bf16 v[84:87], v[156:159], v[188:191], v[84:87]
	v_mfma_f32_16x16x32_bf16 v[80:83], v[164:167], v[188:191], v[80:83]
	v_mfma_f32_16x16x32_bf16 v[68:71], v[156:159], v[226:229], v[68:71]
	v_mfma_f32_16x16x32_bf16 v[64:67], v[164:167], v[226:229], v[64:67]
	v_mfma_f32_16x16x32_bf16 v[116:119], v[160:163], v[176:179], v[116:119]
	v_mfma_f32_16x16x32_bf16 v[112:115], v[168:171], v[176:179], v[112:115]
	v_mfma_f32_16x16x32_bf16 v[100:103], v[160:163], v[184:187], v[100:103]
	v_mfma_f32_16x16x32_bf16 v[96:99], v[168:171], v[184:187], v[96:99]
	v_mfma_f32_16x16x32_bf16 v[84:87], v[160:163], v[222:225], v[84:87]
	v_mfma_f32_16x16x32_bf16 v[80:83], v[168:171], v[222:225], v[80:83]
	v_mfma_f32_16x16x32_bf16 v[68:71], v[160:163], v[230:233], v[68:71]
	v_mfma_f32_16x16x32_bf16 v[64:67], v[168:171], v[230:233], v[64:67]
	s_setprio 0
	s_barrier
	s_add_i32 s46, s43, s50
	v_lshl_add_u64 v[192:193], s[78:79], 0, v[128:129]
	s_mov_b32 m0, s46
	ds_read_b128 v[172:175], v219 offset:16384
	ds_read_b128 v[176:179], v219 offset:17408
	ds_read_b128 v[180:183], v219 offset:18432
	ds_read_b128 v[184:187], v219 offset:19456
	ds_read_b128 v[188:191], v219 offset:20480
	ds_read_b128 v[222:225], v219 offset:21504
	ds_read_b128 v[226:229], v219 offset:22528
	ds_read_b128 v[230:233], v219 offset:23552
	global_load_lds_dwordx4 v[192:193], off
	s_add_i32 m0, s46, 0x2000
	s_add_u32 s46, s78, 0x40000
	v_lshl_add_u64 v[234:235], s[78:79], 0, v[134:135]
	s_addc_u32 s47, s79, 0
	s_add_i32 vcc_hi, s67, s50
	global_load_lds_dwordx4 v[234:235], off
	v_lshl_add_u64 v[236:237], s[46:47], 0, v[128:129]
	s_mov_b32 m0, vcc_hi
	v_lshl_add_u64 v[238:239], s[80:81], 0, v[132:133]
	global_load_lds_dwordx4 v[236:237], off
	v_lshl_add_u64 v[236:237], s[46:47], 0, v[134:135]
	s_add_i32 m0, vcc_hi, 0x2000
	s_nop 0
	global_load_lds_dwordx4 v[236:237], off
	v_lshl_add_u64 v[236:237], s[80:81], 0, v[130:131]
	s_mov_b32 m0, s51
	s_nop 0
	global_load_lds_dwordx4 v[236:237], off
	s_mov_b32 m0, s60
	s_nop 0
	global_load_lds_dwordx4 v[238:239], off
	s_waitcnt vmcnt(8)
	s_waitcnt lgkmcnt(0)
	s_barrier
; #define PG8_STAGE_A(bufoff, gbase, h, nx) do { _Pragma("unroll") for (int _i = 0; _i < 2; ++_i) { \
;         const unsigned vo_ = GA ? ((nx) ? vgn[h][_i] : vgc[h][_i]) : voffA[_i]; \
;         __builtin_amdgcn_global_load_lds((const unsigned*)((const char*)(gbase) + vo_), (PG8_LAS unsigned*)(lds + (bufoff) + ldsw + _i * 8192), 16, 0, 0); } } while (0)
; #define PG8_LDA(dst, b, h) do { _Pragma("unroll") for (int m = 0; m < 4; ++m) _Pragma("unroll") for (int k = 0; k < 2; ++k) dst[m][k] = *(const PG8_LAS bf16x8*)(lds + PG8_SA(b, h) + aoff + m * 2048 + k * 1024); } while (0)
; #define PG8_LDB(dst, b, h) do { _Pragma("unroll") for (int n = 0; n < 2; ++n) _Pragma("unroll") for (int k = 0; k < 2; ++k) dst[n][k] = *(const PG8_LAS bf16x8*)(lds + PG8_SB(b, h) + boff + n * 2048 + k * 1024); } while (0)
; #define PG8_MMA(ai, bj, At, Bt) do { __builtin_amdgcn_s_setprio(1); _Pragma("unroll") for (int m = 0; m < 4; ++m) _Pragma("unroll") for (int n = 0; n < 2; ++n) _Pragma("unroll") for (int k = 0; k < 2; ++k) \
;         acc[ai][bj][m][n] = __builtin_amdgcn_mfma_f32_16x16x32_bf16(Bt[n][k], At[m][k], acc[ai][bj][m][n], 0, 0, 0); __builtin_amdgcn_s_setprio(0); } while (0)
; #define PG8_WAIT_V(n) asm volatile("s_waitcnt vmcnt(" #n ")" ::: "memory")
; #define PG8_WAIT_L(n) asm volatile("s_waitcnt lgkmcnt(" #n ")" ::: "memory")
; #define PG8_BAR __builtin_amdgcn_s_barrier()
; #define PG8_SCHED __builtin_amdgcn_sched_barrier(0)
; template <class Epi, class Sched>
; __device__ __forceinline__ void gemm_phase(const int WID_, PG8_LAS unsigned char* lds, const Sched& S, const Epi& E) {
;     ...
;             PG8_WAIT_V(8); PG8_WAIT_L(0); PG8_BAR; PG8_MMA(1, 0, At, B0); PG8_MMA(1, 1, At, B1); PG8_BAR; PG8_SCHED;
;             PG8_LDB(B0, 1, 0); PG8_LDB(B1, 1, 1); PG8_SCHED; PG8_LDA(At, 1, 0); PG8_STAGE_A(PG8_SA(0, 1), a2 + hstepA, 1, last);
;             PG8_WAIT_V(8); PG8_WAIT_L(0); PG8_BAR; PG8_MMA(0, 0, At, B0); PG8_MMA(0, 1, At, B1); PG8_BAR; PG8_SCHED;
	s_setprio 1
	s_waitcnt lgkmcnt(0)
	v_mfma_f32_16x16x32_bf16 v[60:63], v[140:143], v[172:175], v[60:63]
	v_mfma_f32_16x16x32_bf16 v[56:59], v[148:151], v[172:175], v[56:59]
	v_mfma_f32_16x16x32_bf16 v[44:47], v[140:143], v[180:183], v[44:47]
	v_mfma_f32_16x16x32_bf16 v[40:43], v[148:151], v[180:183], v[40:43]
	v_mfma_f32_16x16x32_bf16 v[28:31], v[140:143], v[188:191], v[28:31]
	v_mfma_f32_16x16x32_bf16 v[24:27], v[148:151], v[188:191], v[24:27]
	v_mfma_f32_16x16x32_bf16 v[12:15], v[140:143], v[226:229], v[12:15]
	v_mfma_f32_16x16x32_bf16 v[8:11], v[148:151], v[226:229], v[8:11]
	v_mfma_f32_16x16x32_bf16 v[60:63], v[144:147], v[176:179], v[60:63]
	v_mfma_f32_16x16x32_bf16 v[56:59], v[152:155], v[176:179], v[56:59]
	v_mfma_f32_16x16x32_bf16 v[44:47], v[144:147], v[184:187], v[44:47]
	v_mfma_f32_16x16x32_bf16 v[40:43], v[152:155], v[184:187], v[40:43]
	v_mfma_f32_16x16x32_bf16 v[28:31], v[144:147], v[222:225], v[28:31]
	v_mfma_f32_16x16x32_bf16 v[24:27], v[152:155], v[222:225], v[24:27]
	v_mfma_f32_16x16x32_bf16 v[12:15], v[144:147], v[230:233], v[12:15]
	v_mfma_f32_16x16x32_bf16 v[8:11], v[152:155], v[230:233], v[8:11]
	s_setprio 0
	s_setprio 1
	v_mfma_f32_16x16x32_bf16 v[52:55], v[156:159], v[172:175], v[52:55]
	v_mfma_f32_16x16x32_bf16 v[48:51], v[164:167], v[172:175], v[48:51]
	v_mfma_f32_16x16x32_bf16 v[36:39], v[156:159], v[180:183], v[36:39]
	v_mfma_f32_16x16x32_bf16 v[32:35], v[164:167], v[180:183], v[32:35]
	v_mfma_f32_16x16x32_bf16 v[20:23], v[156:159], v[188:191], v[20:23]
	v_mfma_f32_16x16x32_bf16 v[16:19], v[164:167], v[188:191], v[16:19]
	v_mfma_f32_16x16x32_bf16 v[4:7], v[156:159], v[226:229], v[4:7]
	v_mfma_f32_16x16x32_bf16 v[0:3], v[164:167], v[226:229], v[0:3]
	v_mfma_f32_16x16x32_bf16 v[52:55], v[160:163], v[176:179], v[52:55]
	v_mfma_f32_16x16x32_bf16 v[48:51], v[168:171], v[176:179], v[48:51]
	v_mfma_f32_16x16x32_bf16 v[36:39], v[160:163], v[184:187], v[36:39]
	v_mfma_f32_16x16x32_bf16 v[32:35], v[168:171], v[184:187], v[32:35]
	v_mfma_f32_16x16x32_bf16 v[20:23], v[160:163], v[222:225], v[20:23]
	v_mfma_f32_16x16x32_bf16 v[16:19], v[168:171], v[222:225], v[16:19]
	v_mfma_f32_16x16x32_bf16 v[4:7], v[160:163], v[230:233], v[4:7]
	v_mfma_f32_16x16x32_bf16 v[0:3], v[168:171], v[230:233], v[0:3]
	s_setprio 0
	s_barrier
	v_add_u32_e32 v152, s82, v199
	v_add_u32_e32 v168, s83, v199
	ds_read_b128 v[140:143], v152
	ds_read_b128 v[144:147], v152 offset:1024
	ds_read_b128 v[148:151], v152 offset:2048
	ds_read_b128 v[152:155], v152 offset:3072
	ds_read_b128 v[156:159], v168
	ds_read_b128 v[160:163], v168 offset:1024
	ds_read_b128 v[164:167], v168 offset:2048
	ds_read_b128 v[168:171], v168 offset:3072
	s_add_u32 s46, s80, 0x40000
	s_addc_u32 s47, s81, 0
	s_mov_b32 m0, s61
	v_lshl_add_u64 v[240:241], s[46:47], 0, v[130:131]
	ds_read_b128 v[172:175], v219 offset:32768
	ds_read_b128 v[176:179], v219 offset:33792
	ds_read_b128 v[180:183], v219 offset:34816
	ds_read_b128 v[184:187], v219 offset:35840
	ds_read_b128 v[188:191], v219 offset:36864
	ds_read_b128 v[222:225], v219 offset:37888
	ds_read_b128 v[226:229], v219 offset:38912
	ds_read_b128 v[230:233], v219 offset:39936
	global_load_lds_dwordx4 v[240:241], off
	v_lshl_add_u64 v[240:241], s[46:47], 0, v[132:133]
	s_mov_b32 m0, s62
	s_nop 0
	global_load_lds_dwordx4 v[240:241], off
	s_waitcnt vmcnt(8)
	s_waitcnt lgkmcnt(0)
	s_barrier
	s_setprio 1
	s_waitcnt lgkmcnt(0)
	v_mfma_f32_16x16x32_bf16 v[124:127], v[140:143], v[172:175], v[124:127]
	v_mfma_f32_16x16x32_bf16 v[120:123], v[148:151], v[172:175], v[120:123]
	v_mfma_f32_16x16x32_bf16 v[108:111], v[140:143], v[180:183], v[108:111]
	v_mfma_f32_16x16x32_bf16 v[104:107], v[148:151], v[180:183], v[104:107]
	v_mfma_f32_16x16x32_bf16 v[92:95], v[140:143], v[188:191], v[92:95]
	v_mfma_f32_16x16x32_bf16 v[88:91], v[148:151], v[188:191], v[88:91]
	v_mfma_f32_16x16x32_bf16 v[76:79], v[140:143], v[226:229], v[76:79]
	v_mfma_f32_16x16x32_bf16 v[72:75], v[148:151], v[226:229], v[72:75]
	v_mfma_f32_16x16x32_bf16 v[124:127], v[144:147], v[176:179], v[124:127]
	v_mfma_f32_16x16x32_bf16 v[120:123], v[152:155], v[176:179], v[120:123]
	v_mfma_f32_16x16x32_bf16 v[108:111], v[144:147], v[184:187], v[108:111]
	v_mfma_f32_16x16x32_bf16 v[104:107], v[152:155], v[184:187], v[104:107]
	v_mfma_f32_16x16x32_bf16 v[92:95], v[144:147], v[222:225], v[92:95]
	v_mfma_f32_16x16x32_bf16 v[88:91], v[152:155], v[222:225], v[88:91]
	v_mfma_f32_16x16x32_bf16 v[76:79], v[144:147], v[230:233], v[76:79]
	v_mfma_f32_16x16x32_bf16 v[72:75], v[152:155], v[230:233], v[72:75]
	s_setprio 0
	s_setprio 1
	v_mfma_f32_16x16x32_bf16 v[116:119], v[156:159], v[172:175], v[116:119]
	v_mfma_f32_16x16x32_bf16 v[112:115], v[164:167], v[172:175], v[112:115]
	v_mfma_f32_16x16x32_bf16 v[100:103], v[156:159], v[180:183], v[100:103]
	v_mfma_f32_16x16x32_bf16 v[96:99], v[164:167], v[180:183], v[96:99]
	v_mfma_f32_16x16x32_bf16 v[84:87], v[156:159], v[188:191], v[84:87]
	v_mfma_f32_16x16x32_bf16 v[80:83], v[164:167], v[188:191], v[80:83]
	v_mfma_f32_16x16x32_bf16 v[68:71], v[156:159], v[226:229], v[68:71]
	v_mfma_f32_16x16x32_bf16 v[64:67], v[164:167], v[226:229], v[64:67]
	v_mfma_f32_16x16x32_bf16 v[116:119], v[160:163], v[176:179], v[116:119]
	v_mfma_f32_16x16x32_bf16 v[112:115], v[168:171], v[176:179], v[112:115]
	v_mfma_f32_16x16x32_bf16 v[100:103], v[160:163], v[184:187], v[100:103]
	v_mfma_f32_16x16x32_bf16 v[96:99], v[168:171], v[184:187], v[96:99]
	v_mfma_f32_16x16x32_bf16 v[84:87], v[160:163], v[222:225], v[84:87]
	v_mfma_f32_16x16x32_bf16 v[80:83], v[168:171], v[222:225], v[80:83]
	v_mfma_f32_16x16x32_bf16 v[68:71], v[160:163], v[230:233], v[68:71]
	v_mfma_f32_16x16x32_bf16 v[64:67], v[168:171], v[230:233], v[64:67]
	s_setprio 0
	s_barrier
; #define PG8_STAGE(bufoff, gbase, voff) do { _Pragma("unroll") for (int _i = 0; _i < 2; ++_i) \
;         __builtin_amdgcn_global_load_lds((const unsigned*)((const char*)(gbase) + (voff)[_i]), (PG8_LAS unsigned*)(lds + (bufoff) + ldsw + _i * 8192), 16, 0, 0); } while (0)
; #define PG8_STAGE_A(bufoff, gbase, h, nx) do { _Pragma("unroll") for (int _i = 0; _i < 2; ++_i) { \
;         const unsigned vo_ = GA ? ((nx) ? vgn[h][_i] : vgc[h][_i]) : voffA[_i]; \
;         __builtin_amdgcn_global_load_lds((const unsigned*)((const char*)(gbase) + vo_), (PG8_LAS unsigned*)(lds + (bufoff) + ldsw + _i * 8192), 16, 0, 0); } } while (0)
; #define PG8_LDA(dst, b, h) do { _Pragma("unroll") for (int m = 0; m < 4; ++m) _Pragma("unroll") for (int k = 0; k < 2; ++k) dst[m][k] = *(const PG8_LAS bf16x8*)(lds + PG8_SA(b, h) + aoff + m * 2048 + k * 1024); } while (0)
; #define PG8_MMA(ai, bj, At, Bt) do { __builtin_amdgcn_s_setprio(1); _Pragma("unroll") for (int m = 0; m < 4; ++m) _Pragma("unroll") for (int n = 0; n < 2; ++n) _Pragma("unroll") for (int k = 0; k < 2; ++k) \
;         acc[ai][bj][m][n] = __builtin_amdgcn_mfma_f32_16x16x32_bf16(Bt[n][k], At[m][k], acc[ai][bj][m][n], 0, 0, 0); __builtin_amdgcn_s_setprio(0); } while (0)
; #define PG8_WAIT_V(n) asm volatile("s_waitcnt vmcnt(" #n ")" ::: "memory")
; #define PG8_WAIT_L(n) asm volatile("s_waitcnt lgkmcnt(" #n ")" ::: "memory")
; #define PG8_BAR __builtin_amdgcn_s_barrier()
; #define PG8_SCHED __builtin_amdgcn_sched_barrier(0)
; template <class Epi, class Sched>
; __device__ __forceinline__ void gemm_phase(const int WID_, PG8_LAS unsigned char* lds, const Sched& S, const Epi& E) {
;     ...
;             PG8_LDA(At, 1, 1); PG8_STAGE(PG8_SB(1, 0), b3, voffB); PG8_STAGE(PG8_SB(1, 1), b3 + hstepB, voffB); PG8_STAGE_A(PG8_SA(1, 0), a3, 0, last);
;             PG8_WAIT_V(8); PG8_WAIT_L(0); PG8_BAR; PG8_MMA(1, 0, At, B0); PG8_MMA(1, 1, At, B1); PG8_BAR; PG8_SCHED;
;         }
;         if (wr == 0) PG8_BAR;
	s_add_i32 s46, s82, s50
	v_lshl_add_u64 v[192:193], v[192:193], 0, s[68:69]
	s_mov_b32 m0, s46
	ds_read_b128 v[172:175], v219 offset:49152
	ds_read_b128 v[176:179], v219 offset:50176
	ds_read_b128 v[180:183], v219 offset:51200
	ds_read_b128 v[184:187], v219 offset:52224
	ds_read_b128 v[188:191], v219 offset:53248
	ds_read_b128 v[222:225], v219 offset:54272
	ds_read_b128 v[226:229], v219 offset:55296
	ds_read_b128 v[230:233], v219 offset:56320
	global_load_lds_dwordx4 v[192:193], off
	s_add_i32 m0, s46, 0x2000
	s_add_u32 s46, s78, 0x40080
	v_lshl_add_u64 v[192:193], v[234:235], 0, s[68:69]
	s_addc_u32 s47, s79, 0
	s_add_i32 s78, s83, s50
	global_load_lds_dwordx4 v[192:193], off
	v_lshl_add_u64 v[192:193], s[46:47], 0, v[128:129]
	s_mov_b32 m0, s78
	s_nop 0
	global_load_lds_dwordx4 v[192:193], off
	v_lshl_add_u64 v[192:193], s[46:47], 0, v[134:135]
	s_add_i32 m0, s78, 0x2000
	s_nop 0
	global_load_lds_dwordx4 v[192:193], off
	v_lshl_add_u64 v[192:193], v[236:237], 0, s[68:69]
	s_mov_b32 m0, s63
	s_nop 0
	global_load_lds_dwordx4 v[192:193], off
	v_lshl_add_u64 v[192:193], v[238:239], 0, s[68:69]
	s_mov_b32 m0, s86
	s_nop 0
	global_load_lds_dwordx4 v[192:193], off
	s_waitcnt vmcnt(8)
	s_waitcnt lgkmcnt(0)
	s_barrier
	s_setprio 1
	s_waitcnt lgkmcnt(0)
	v_mfma_f32_16x16x32_bf16 v[60:63], v[140:143], v[172:175], v[60:63]
	v_mfma_f32_16x16x32_bf16 v[56:59], v[148:151], v[172:175], v[56:59]
	v_mfma_f32_16x16x32_bf16 v[44:47], v[140:143], v[180:183], v[44:47]
	v_mfma_f32_16x16x32_bf16 v[40:43], v[148:151], v[180:183], v[40:43]
	v_mfma_f32_16x16x32_bf16 v[28:31], v[140:143], v[188:191], v[28:31]
	v_mfma_f32_16x16x32_bf16 v[24:27], v[148:151], v[188:191], v[24:27]
	v_mfma_f32_16x16x32_bf16 v[12:15], v[140:143], v[226:229], v[12:15]
	v_mfma_f32_16x16x32_bf16 v[8:11], v[148:151], v[226:229], v[8:11]
	v_mfma_f32_16x16x32_bf16 v[60:63], v[144:147], v[176:179], v[60:63]
	v_mfma_f32_16x16x32_bf16 v[56:59], v[152:155], v[176:179], v[56:59]
	v_mfma_f32_16x16x32_bf16 v[44:47], v[144:147], v[184:187], v[44:47]
	v_mfma_f32_16x16x32_bf16 v[40:43], v[152:155], v[184:187], v[40:43]
	v_mfma_f32_16x16x32_bf16 v[28:31], v[144:147], v[222:225], v[28:31]
	v_mfma_f32_16x16x32_bf16 v[24:27], v[152:155], v[222:225], v[24:27]
	v_mfma_f32_16x16x32_bf16 v[12:15], v[144:147], v[230:233], v[12:15]
	v_mfma_f32_16x16x32_bf16 v[8:11], v[152:155], v[230:233], v[8:11]
	s_setprio 0
	s_setprio 1
	v_mfma_f32_16x16x32_bf16 v[52:55], v[156:159], v[172:175], v[52:55]
	v_mfma_f32_16x16x32_bf16 v[48:51], v[164:167], v[172:175], v[48:51]
	v_mfma_f32_16x16x32_bf16 v[36:39], v[156:159], v[180:183], v[36:39]
	v_mfma_f32_16x16x32_bf16 v[32:35], v[164:167], v[180:183], v[32:35]
	v_mfma_f32_16x16x32_bf16 v[20:23], v[156:159], v[188:191], v[20:23]
	v_mfma_f32_16x16x32_bf16 v[16:19], v[164:167], v[188:191], v[16:19]
	v_mfma_f32_16x16x32_bf16 v[4:7], v[156:159], v[226:229], v[4:7]
	v_mfma_f32_16x16x32_bf16 v[0:3], v[164:167], v[226:229], v[0:3]
	v_mfma_f32_16x16x32_bf16 v[52:55], v[160:163], v[176:179], v[52:55]
	v_mfma_f32_16x16x32_bf16 v[48:51], v[168:171], v[176:179], v[48:51]
	v_mfma_f32_16x16x32_bf16 v[36:39], v[160:163], v[184:187], v[36:39]
	v_mfma_f32_16x16x32_bf16 v[32:35], v[168:171], v[184:187], v[32:35]
	v_mfma_f32_16x16x32_bf16 v[20:23], v[160:163], v[222:225], v[20:23]
	v_mfma_f32_16x16x32_bf16 v[16:19], v[168:171], v[222:225], v[16:19]
	v_mfma_f32_16x16x32_bf16 v[4:7], v[160:163], v[230:233], v[4:7]
	v_mfma_f32_16x16x32_bf16 v[0:3], v[168:171], v[230:233], v[0:3]
	s_setprio 0
	s_add_i32 vcc_lo, vcc_lo, 2
	s_add_u32 s22, s22, 0x100
	s_addc_u32 s23, s23, 0
	s_add_u32 s13, s13, 0x100
	s_addc_u32 s15, s15, 0
	s_cmp_gt_u32 vcc_lo, 13
	s_barrier
	s_cbranch_scc0 .LBB0_2070
	s_and_b64 vcc, exec, s[10:11]
	s_cbranch_vccz .LBB0_2073
	s_barrier

; #define PG8_STAGE(bufoff, gbase, voff) do { _Pragma("unroll") for (int _i = 0; _i < 2; ++_i) \
;         __builtin_amdgcn_global_load_lds((const unsigned*)((const char*)(gbase) + (voff)[_i]), (PG8_LAS unsigned*)(lds + (bufoff) + ldsw + _i * 8192), 16, 0, 0); } while (0)
; #define PG8_STAGE_A(bufoff, gbase, h, nx) do { _Pragma("unroll") for (int _i = 0; _i < 2; ++_i) { \
;         const unsigned vo_ = GA ? ((nx) ? vgn[h][_i] : vgc[h][_i]) : voffA[_i]; \
;         __builtin_amdgcn_global_load_lds((const unsigned*)((const char*)(gbase) + vo_), (PG8_LAS unsigned*)(lds + (bufoff) + ldsw + _i * 8192), 16, 0, 0); } } while (0)
; #define PG8_LDA(dst, b, h) do { _Pragma("unroll") for (int m = 0; m < 4; ++m) _Pragma("unroll") for (int k = 0; k < 2; ++k) dst[m][k] = *(const PG8_LAS bf16x8*)(lds + PG8_SA(b, h) + aoff + m * 2048 + k * 1024); } while (0)
; #define PG8_LDB(dst, b, h) do { _Pragma("unroll") for (int n = 0; n < 2; ++n) _Pragma("unroll") for (int k = 0; k < 2; ++k) dst[n][k] = *(const PG8_LAS bf16x8*)(lds + PG8_SB(b, h) + boff + n * 2048 + k * 1024); } while (0)
; #define PG8_WAIT_V(n) asm volatile("s_waitcnt vmcnt(" #n ")" ::: "memory")
; #define PG8_WAIT_L(n) asm volatile("s_waitcnt lgkmcnt(" #n ")" ::: "memory")
; #define PG8_BAR __builtin_amdgcn_s_barrier()
; #define PG8_SCHED __builtin_amdgcn_sched_barrier(0)
; template <class Epi, class Sched>
; __device__ __forceinline__ void gemm_phase(const int WID_, PG8_LAS unsigned char* lds, const Sched& S, const Epi& E) {
;     ...
;         for (int t = 0; t < nt; t += 2) {
;             const bool last = (t == nt - 2);
;             const char* a1 = cA + (size_t)(t + 1) * kstep;
;             const char* a2 = last ? nA : cA + (size_t)(t + 2) * kstep; const char* b2 = last ? nB : cB + (size_t)(t + 2) * kstep;
;             const char* a3 = a2 + kstep; const char* b3 = b2 + kstep;
;             PG8_LDB(B0, 0, 0); PG8_LDB(B1, 0, 1); PG8_SCHED; PG8_LDA(At, 0, 0); PG8_STAGE_A(PG8_SA(1, 1), a1 + hstepA, 1, false);
;             PG8_WAIT_V(8); PG8_WAIT_L(0); PG8_BAR; PG8_MMA(0, 0, At, B0); PG8_MMA(0, 1, At, B1); PG8_BAR; PG8_SCHED;
;             PG8_LDA(At, 0, 1); PG8_STAGE(PG8_SB(0, 0), b2, voffB); PG8_STAGE(PG8_SB(0, 1), b2 + hstepB, voffB); PG8_STAGE_A(PG8_SA(0, 0), a2, 0, last);
;             PG8_WAIT_V(8); PG8_WAIT_L(0); PG8_BAR; PG8_MMA(1, 0, At, B0); PG8_MMA(1, 1, At, B1); PG8_BAR; PG8_SCHED;
.LBB0_2120:
	v_add_u32_e32 v144, s43, v147
	ds_read_b128 v[140:143], v144
	ds_read_b128 v[150:153], v144 offset:1024
	ds_read_b128 v[154:157], v144 offset:2048
	ds_read_b128 v[158:161], v144 offset:3072
	v_add_u32_e32 v144, s67, v147
	ds_read_b128 v[162:165], v144
	ds_read_b128 v[166:169], v144 offset:1024
	ds_read_b128 v[170:173], v144 offset:2048
	ds_read_b128 v[174:177], v144 offset:3072
	s_add_u32 s20, s18, 0xfffc0080
	s_addc_u32 s21, s19, -1
	s_cmp_eq_u32 s79, 12
	s_cselect_b32 s23, s13, s21
	s_cselect_b32 s22, s12, s20
	s_cselect_b32 s21, s15, s11
	s_cselect_b32 s20, s14, s9
	v_lshl_add_u64 v[144:145], s[18:19], 0, v[136:137]
	s_add_i32 m0, s49, 0xc000
	ds_read_b128 v[178:181], v149
	ds_read_b128 v[182:185], v149 offset:1024
	ds_read_b128 v[186:189], v149 offset:2048
	ds_read_b128 v[190:193], v149 offset:3072
	ds_read_b128 v[198:201], v149 offset:4096
	ds_read_b128 v[202:205], v149 offset:5120
	ds_read_b128 v[206:209], v149 offset:6144
	ds_read_b128 v[210:213], v149 offset:7168
	global_load_lds_dwordx4 v[144:145], off
	v_lshl_add_u64 v[144:145], s[18:19], 0, v[138:139]
	s_add_i32 m0, s49, 0xe000
	s_nop 0
	global_load_lds_dwordx4 v[144:145], off
	s_waitcnt vmcnt(8)
	s_waitcnt lgkmcnt(0)
	s_barrier
	s_setprio 1
	s_waitcnt lgkmcnt(0)
	v_mfma_f32_16x16x32_bf16 v[124:127], v[140:143], v[178:181], v[124:127]
	v_mfma_f32_16x16x32_bf16 v[120:123], v[154:157], v[178:181], v[120:123]
	v_mfma_f32_16x16x32_bf16 v[108:111], v[140:143], v[186:189], v[108:111]
	v_mfma_f32_16x16x32_bf16 v[104:107], v[154:157], v[186:189], v[104:107]
	v_mfma_f32_16x16x32_bf16 v[92:95], v[140:143], v[198:201], v[92:95]
	v_mfma_f32_16x16x32_bf16 v[88:91], v[154:157], v[198:201], v[88:91]
	v_mfma_f32_16x16x32_bf16 v[76:79], v[140:143], v[206:209], v[76:79]
	v_mfma_f32_16x16x32_bf16 v[72:75], v[154:157], v[206:209], v[72:75]
	v_mfma_f32_16x16x32_bf16 v[124:127], v[150:153], v[182:185], v[124:127]
	v_mfma_f32_16x16x32_bf16 v[120:123], v[158:161], v[182:185], v[120:123]
	v_mfma_f32_16x16x32_bf16 v[108:111], v[150:153], v[190:193], v[108:111]
	v_mfma_f32_16x16x32_bf16 v[104:107], v[158:161], v[190:193], v[104:107]
	v_mfma_f32_16x16x32_bf16 v[92:95], v[150:153], v[202:205], v[92:95]
	v_mfma_f32_16x16x32_bf16 v[88:91], v[158:161], v[202:205], v[88:91]
	v_mfma_f32_16x16x32_bf16 v[76:79], v[150:153], v[210:213], v[76:79]
	v_mfma_f32_16x16x32_bf16 v[72:75], v[158:161], v[210:213], v[72:75]
	s_setprio 0
	s_setprio 1
	v_mfma_f32_16x16x32_bf16 v[116:119], v[162:165], v[178:181], v[116:119]
	v_mfma_f32_16x16x32_bf16 v[112:115], v[170:173], v[178:181], v[112:115]
	v_mfma_f32_16x16x32_bf16 v[100:103], v[162:165], v[186:189], v[100:103]
	v_mfma_f32_16x16x32_bf16 v[96:99], v[170:173], v[186:189], v[96:99]
	v_mfma_f32_16x16x32_bf16 v[84:87], v[162:165], v[198:201], v[84:87]
	v_mfma_f32_16x16x32_bf16 v[80:83], v[170:173], v[198:201], v[80:83]
	v_mfma_f32_16x16x32_bf16 v[68:71], v[162:165], v[206:209], v[68:71]
	v_mfma_f32_16x16x32_bf16 v[64:67], v[170:173], v[206:209], v[64:67]
	v_mfma_f32_16x16x32_bf16 v[116:119], v[166:169], v[182:185], v[116:119]
	v_mfma_f32_16x16x32_bf16 v[112:115], v[174:177], v[182:185], v[112:115]
	v_mfma_f32_16x16x32_bf16 v[100:103], v[166:169], v[190:193], v[100:103]
	v_mfma_f32_16x16x32_bf16 v[96:99], v[174:177], v[190:193], v[96:99]
	v_mfma_f32_16x16x32_bf16 v[84:87], v[166:169], v[202:205], v[84:87]
	v_mfma_f32_16x16x32_bf16 v[80:83], v[174:177], v[202:205], v[80:83]
	v_mfma_f32_16x16x32_bf16 v[68:71], v[166:169], v[210:213], v[68:71]
	v_mfma_f32_16x16x32_bf16 v[64:67], v[174:177], v[210:213], v[64:67]
	s_setprio 0
	s_barrier
	s_add_i32 s46, s43, s48
	v_lshl_add_u64 v[144:145], s[20:21], 0, v[128:129]
	s_mov_b32 m0, s46
	ds_read_b128 v[178:181], v149 offset:16384
	ds_read_b128 v[182:185], v149 offset:17408
	ds_read_b128 v[186:189], v149 offset:18432
	ds_read_b128 v[190:193], v149 offset:19456
	ds_read_b128 v[198:201], v149 offset:20480
	ds_read_b128 v[202:205], v149 offset:21504
	ds_read_b128 v[206:209], v149 offset:22528
	ds_read_b128 v[210:213], v149 offset:23552
	global_load_lds_dwordx4 v[144:145], off
	s_add_i32 m0, s46, 0x2000
	s_add_u32 s46, s20, 0x40000
	v_lshl_add_u64 v[214:215], s[20:21], 0, v[130:131]
	s_addc_u32 s47, s21, 0
	s_add_i32 s80, s67, s48
	global_load_lds_dwordx4 v[214:215], off
	v_lshl_add_u64 v[216:217], s[46:47], 0, v[128:129]
	s_mov_b32 m0, s80
	v_lshl_add_u64 v[218:219], s[22:23], 0, v[132:133]
	global_load_lds_dwordx4 v[216:217], off
	v_lshl_add_u64 v[216:217], s[46:47], 0, v[130:131]
	s_add_i32 m0, s80, 0x2000
	s_nop 0
	global_load_lds_dwordx4 v[216:217], off
	v_lshl_add_u64 v[216:217], s[22:23], 0, v[134:135]
	s_mov_b32 m0, s49
	s_nop 0
	global_load_lds_dwordx4 v[216:217], off
	s_mov_b32 m0, s50
	s_nop 0
	global_load_lds_dwordx4 v[218:219], off
	s_waitcnt vmcnt(8)
	s_waitcnt lgkmcnt(0)
	s_barrier
; #define PG8_STAGE_A(bufoff, gbase, h, nx) do { _Pragma("unroll") for (int _i = 0; _i < 2; ++_i) { \
;         const unsigned vo_ = GA ? ((nx) ? vgn[h][_i] : vgc[h][_i]) : voffA[_i]; \
;         __builtin_amdgcn_global_load_lds((const unsigned*)((const char*)(gbase) + vo_), (PG8_LAS unsigned*)(lds + (bufoff) + ldsw + _i * 8192), 16, 0, 0); } } while (0)
; #define PG8_LDA(dst, b, h) do { _Pragma("unroll") for (int m = 0; m < 4; ++m) _Pragma("unroll") for (int k = 0; k < 2; ++k) dst[m][k] = *(const PG8_LAS bf16x8*)(lds + PG8_SA(b, h) + aoff + m * 2048 + k * 1024); } while (0)
; #define PG8_LDB(dst, b, h) do { _Pragma("unroll") for (int n = 0; n < 2; ++n) _Pragma("unroll") for (int k = 0; k < 2; ++k) dst[n][k] = *(const PG8_LAS bf16x8*)(lds + PG8_SB(b, h) + boff + n * 2048 + k * 1024); } while (0)
; #define PG8_MMA(ai, bj, At, Bt) do { __builtin_amdgcn_s_setprio(1); _Pragma("unroll") for (int m = 0; m < 4; ++m) _Pragma("unroll") for (int n = 0; n < 2; ++n) _Pragma("unroll") for (int k = 0; k < 2; ++k) \
;         acc[ai][bj][m][n] = __builtin_amdgcn_mfma_f32_16x16x32_bf16(Bt[n][k], At[m][k], acc[ai][bj][m][n], 0, 0, 0); __builtin_amdgcn_s_setprio(0); } while (0)
; #define PG8_WAIT_V(n) asm volatile("s_waitcnt vmcnt(" #n ")" ::: "memory")
; #define PG8_WAIT_L(n) asm volatile("s_waitcnt lgkmcnt(" #n ")" ::: "memory")
; #define PG8_BAR __builtin_amdgcn_s_barrier()
; #define PG8_SCHED __builtin_amdgcn_sched_barrier(0)
; template <class Epi, class Sched>
; __device__ __forceinline__ void gemm_phase(const int WID_, PG8_LAS unsigned char* lds, const Sched& S, const Epi& E) {
;     ...
;             PG8_WAIT_V(8); PG8_WAIT_L(0); PG8_BAR; PG8_MMA(1, 0, At, B0); PG8_MMA(1, 1, At, B1); PG8_BAR; PG8_SCHED;
;             PG8_LDB(B0, 1, 0); PG8_LDB(B1, 1, 1); PG8_SCHED; PG8_LDA(At, 1, 0); PG8_STAGE_A(PG8_SA(0, 1), a2 + hstepA, 1, last);
;             PG8_WAIT_V(8); PG8_WAIT_L(0); PG8_BAR; PG8_MMA(0, 0, At, B0); PG8_MMA(0, 1, At, B1); PG8_BAR; PG8_SCHED;
	s_setprio 1
	s_waitcnt lgkmcnt(0)
	v_mfma_f32_16x16x32_bf16 v[60:63], v[140:143], v[178:181], v[60:63]
	v_mfma_f32_16x16x32_bf16 v[56:59], v[154:157], v[178:181], v[56:59]
	v_mfma_f32_16x16x32_bf16 v[44:47], v[140:143], v[186:189], v[44:47]
	v_mfma_f32_16x16x32_bf16 v[40:43], v[154:157], v[186:189], v[40:43]
	v_mfma_f32_16x16x32_bf16 v[28:31], v[140:143], v[198:201], v[28:31]
	v_mfma_f32_16x16x32_bf16 v[24:27], v[154:157], v[198:201], v[24:27]
	v_mfma_f32_16x16x32_bf16 v[12:15], v[140:143], v[206:209], v[12:15]
	v_mfma_f32_16x16x32_bf16 v[8:11], v[154:157], v[206:209], v[8:11]
	v_mfma_f32_16x16x32_bf16 v[60:63], v[150:153], v[182:185], v[60:63]
	v_mfma_f32_16x16x32_bf16 v[56:59], v[158:161], v[182:185], v[56:59]
	v_mfma_f32_16x16x32_bf16 v[44:47], v[150:153], v[190:193], v[44:47]
	v_mfma_f32_16x16x32_bf16 v[40:43], v[158:161], v[190:193], v[40:43]
	v_mfma_f32_16x16x32_bf16 v[28:31], v[150:153], v[202:205], v[28:31]
	v_mfma_f32_16x16x32_bf16 v[24:27], v[158:161], v[202:205], v[24:27]
	v_mfma_f32_16x16x32_bf16 v[12:15], v[150:153], v[210:213], v[12:15]
	v_mfma_f32_16x16x32_bf16 v[8:11], v[158:161], v[210:213], v[8:11]
	s_setprio 0
	s_setprio 1
	v_mfma_f32_16x16x32_bf16 v[52:55], v[162:165], v[178:181], v[52:55]
	v_mfma_f32_16x16x32_bf16 v[48:51], v[170:173], v[178:181], v[48:51]
	v_mfma_f32_16x16x32_bf16 v[36:39], v[162:165], v[186:189], v[36:39]
	v_mfma_f32_16x16x32_bf16 v[32:35], v[170:173], v[186:189], v[32:35]
	v_mfma_f32_16x16x32_bf16 v[20:23], v[162:165], v[198:201], v[20:23]
	v_mfma_f32_16x16x32_bf16 v[16:19], v[170:173], v[198:201], v[16:19]
	v_mfma_f32_16x16x32_bf16 v[4:7], v[162:165], v[206:209], v[4:7]
	v_mfma_f32_16x16x32_bf16 v[0:3], v[170:173], v[206:209], v[0:3]
	v_mfma_f32_16x16x32_bf16 v[52:55], v[166:169], v[182:185], v[52:55]
	v_mfma_f32_16x16x32_bf16 v[48:51], v[174:177], v[182:185], v[48:51]
	v_mfma_f32_16x16x32_bf16 v[36:39], v[166:169], v[190:193], v[36:39]
	v_mfma_f32_16x16x32_bf16 v[32:35], v[174:177], v[190:193], v[32:35]
	v_mfma_f32_16x16x32_bf16 v[20:23], v[166:169], v[202:205], v[20:23]
	v_mfma_f32_16x16x32_bf16 v[16:19], v[174:177], v[202:205], v[16:19]
	v_mfma_f32_16x16x32_bf16 v[4:7], v[166:169], v[210:213], v[4:7]
	v_mfma_f32_16x16x32_bf16 v[0:3], v[174:177], v[210:213], v[0:3]
	s_setprio 0
	s_barrier
	v_add_u32_e32 v158, s82, v147
	v_add_u32_e32 v174, s83, v147
	ds_read_b128 v[140:143], v158
	ds_read_b128 v[150:153], v158 offset:1024
	ds_read_b128 v[154:157], v158 offset:2048
	ds_read_b128 v[158:161], v158 offset:3072
	ds_read_b128 v[162:165], v174
	ds_read_b128 v[166:169], v174 offset:1024
	ds_read_b128 v[170:173], v174 offset:2048
	ds_read_b128 v[174:177], v174 offset:3072
	s_add_u32 s22, s22, 0x40000
	s_addc_u32 s23, s23, 0
	s_mov_b32 m0, s51
	v_lshl_add_u64 v[220:221], s[22:23], 0, v[134:135]
	ds_read_b128 v[178:181], v149 offset:32768
	ds_read_b128 v[182:185], v149 offset:33792
	ds_read_b128 v[186:189], v149 offset:34816
	ds_read_b128 v[190:193], v149 offset:35840
	ds_read_b128 v[198:201], v149 offset:36864
	ds_read_b128 v[202:205], v149 offset:37888
	ds_read_b128 v[206:209], v149 offset:38912
	ds_read_b128 v[210:213], v149 offset:39936
	global_load_lds_dwordx4 v[220:221], off
	v_lshl_add_u64 v[220:221], s[22:23], 0, v[132:133]
	s_mov_b32 m0, s60
	s_nop 0
	global_load_lds_dwordx4 v[220:221], off
	s_waitcnt vmcnt(8)
	s_waitcnt lgkmcnt(0)
	s_barrier
	s_setprio 1
	s_waitcnt lgkmcnt(0)
	v_mfma_f32_16x16x32_bf16 v[124:127], v[140:143], v[178:181], v[124:127]
	v_mfma_f32_16x16x32_bf16 v[120:123], v[154:157], v[178:181], v[120:123]
	v_mfma_f32_16x16x32_bf16 v[108:111], v[140:143], v[186:189], v[108:111]
	v_mfma_f32_16x16x32_bf16 v[104:107], v[154:157], v[186:189], v[104:107]
	v_mfma_f32_16x16x32_bf16 v[92:95], v[140:143], v[198:201], v[92:95]
	v_mfma_f32_16x16x32_bf16 v[88:91], v[154:157], v[198:201], v[88:91]
	v_mfma_f32_16x16x32_bf16 v[76:79], v[140:143], v[206:209], v[76:79]
	v_mfma_f32_16x16x32_bf16 v[72:75], v[154:157], v[206:209], v[72:75]
	v_mfma_f32_16x16x32_bf16 v[124:127], v[150:153], v[182:185], v[124:127]
	v_mfma_f32_16x16x32_bf16 v[120:123], v[158:161], v[182:185], v[120:123]
	v_mfma_f32_16x16x32_bf16 v[108:111], v[150:153], v[190:193], v[108:111]
	v_mfma_f32_16x16x32_bf16 v[104:107], v[158:161], v[190:193], v[104:107]
	v_mfma_f32_16x16x32_bf16 v[92:95], v[150:153], v[202:205], v[92:95]
	v_mfma_f32_16x16x32_bf16 v[88:91], v[158:161], v[202:205], v[88:91]
	v_mfma_f32_16x16x32_bf16 v[76:79], v[150:153], v[210:213], v[76:79]
	v_mfma_f32_16x16x32_bf16 v[72:75], v[158:161], v[210:213], v[72:75]
	s_setprio 0
	s_setprio 1
	v_mfma_f32_16x16x32_bf16 v[116:119], v[162:165], v[178:181], v[116:119]
	v_mfma_f32_16x16x32_bf16 v[112:115], v[170:173], v[178:181], v[112:115]
	v_mfma_f32_16x16x32_bf16 v[100:103], v[162:165], v[186:189], v[100:103]
	v_mfma_f32_16x16x32_bf16 v[96:99], v[170:173], v[186:189], v[96:99]
	v_mfma_f32_16x16x32_bf16 v[84:87], v[162:165], v[198:201], v[84:87]
	v_mfma_f32_16x16x32_bf16 v[80:83], v[170:173], v[198:201], v[80:83]
	v_mfma_f32_16x16x32_bf16 v[68:71], v[162:165], v[206:209], v[68:71]
	v_mfma_f32_16x16x32_bf16 v[64:67], v[170:173], v[206:209], v[64:67]
	v_mfma_f32_16x16x32_bf16 v[116:119], v[166:169], v[182:185], v[116:119]
	v_mfma_f32_16x16x32_bf16 v[112:115], v[174:177], v[182:185], v[112:115]
	v_mfma_f32_16x16x32_bf16 v[100:103], v[166:169], v[190:193], v[100:103]
	v_mfma_f32_16x16x32_bf16 v[96:99], v[174:177], v[190:193], v[96:99]
	v_mfma_f32_16x16x32_bf16 v[84:87], v[166:169], v[202:205], v[84:87]
	v_mfma_f32_16x16x32_bf16 v[80:83], v[174:177], v[202:205], v[80:83]
	v_mfma_f32_16x16x32_bf16 v[68:71], v[166:169], v[210:213], v[68:71]
	v_mfma_f32_16x16x32_bf16 v[64:67], v[174:177], v[210:213], v[64:67]
	s_setprio 0
	s_barrier
; #define PG8_STAGE(bufoff, gbase, voff) do { _Pragma("unroll") for (int _i = 0; _i < 2; ++_i) \
;         __builtin_amdgcn_global_load_lds((const unsigned*)((const char*)(gbase) + (voff)[_i]), (PG8_LAS unsigned*)(lds + (bufoff) + ldsw + _i * 8192), 16, 0, 0); } while (0)
; #define PG8_STAGE_A(bufoff, gbase, h, nx) do { _Pragma("unroll") for (int _i = 0; _i < 2; ++_i) { \
;         const unsigned vo_ = GA ? ((nx) ? vgn[h][_i] : vgc[h][_i]) : voffA[_i]; \
;         __builtin_amdgcn_global_load_lds((const unsigned*)((const char*)(gbase) + vo_), (PG8_LAS unsigned*)(lds + (bufoff) + ldsw + _i * 8192), 16, 0, 0); } } while (0)
; #define PG8_LDA(dst, b, h) do { _Pragma("unroll") for (int m = 0; m < 4; ++m) _Pragma("unroll") for (int k = 0; k < 2; ++k) dst[m][k] = *(const PG8_LAS bf16x8*)(lds + PG8_SA(b, h) + aoff + m * 2048 + k * 1024); } while (0)
; #define PG8_MMA(ai, bj, At, Bt) do { __builtin_amdgcn_s_setprio(1); _Pragma("unroll") for (int m = 0; m < 4; ++m) _Pragma("unroll") for (int n = 0; n < 2; ++n) _Pragma("unroll") for (int k = 0; k < 2; ++k) \
;         acc[ai][bj][m][n] = __builtin_amdgcn_mfma_f32_16x16x32_bf16(Bt[n][k], At[m][k], acc[ai][bj][m][n], 0, 0, 0); __builtin_amdgcn_s_setprio(0); } while (0)
; #define PG8_WAIT_V(n) asm volatile("s_waitcnt vmcnt(" #n ")" ::: "memory")
; #define PG8_WAIT_L(n) asm volatile("s_waitcnt lgkmcnt(" #n ")" ::: "memory")
; #define PG8_BAR __builtin_amdgcn_s_barrier()
; #define PG8_SCHED __builtin_amdgcn_sched_barrier(0)
; template <class Epi, class Sched>
; __device__ __forceinline__ void gemm_phase(const int WID_, PG8_LAS unsigned char* lds, const Sched& S, const Epi& E) {
;     ...
;             PG8_LDA(At, 1, 1); PG8_STAGE(PG8_SB(1, 0), b3, voffB); PG8_STAGE(PG8_SB(1, 1), b3 + hstepB, voffB); PG8_STAGE_A(PG8_SA(1, 0), a3, 0, last);
;             PG8_WAIT_V(8); PG8_WAIT_L(0); PG8_BAR; PG8_MMA(1, 0, At, B0); PG8_MMA(1, 1, At, B1); PG8_BAR; PG8_SCHED;
;         }
;         if (wr == 0) PG8_BAR;
	s_add_i32 s22, s82, s48
	v_lshl_add_u64 v[144:145], v[144:145], 0, s[68:69]
	s_mov_b32 m0, s22
	ds_read_b128 v[178:181], v149 offset:49152
	ds_read_b128 v[182:185], v149 offset:50176
	ds_read_b128 v[186:189], v149 offset:51200
	ds_read_b128 v[190:193], v149 offset:52224
	ds_read_b128 v[198:201], v149 offset:53248
	ds_read_b128 v[202:205], v149 offset:54272
	ds_read_b128 v[206:209], v149 offset:55296
	ds_read_b128 v[210:213], v149 offset:56320
	global_load_lds_dwordx4 v[144:145], off
	s_add_i32 m0, s22, 0x2000
	s_add_u32 s20, s20, 0x40080
	v_lshl_add_u64 v[144:145], v[214:215], 0, s[68:69]
	s_addc_u32 s21, s21, 0
	s_add_i32 s22, s83, s48
	global_load_lds_dwordx4 v[144:145], off
	v_lshl_add_u64 v[144:145], s[20:21], 0, v[128:129]
	s_mov_b32 m0, s22
	s_nop 0
	global_load_lds_dwordx4 v[144:145], off
	v_lshl_add_u64 v[144:145], s[20:21], 0, v[130:131]
	s_add_i32 m0, s22, 0x2000
	s_nop 0
	global_load_lds_dwordx4 v[144:145], off
	v_lshl_add_u64 v[144:145], v[216:217], 0, s[68:69]
	s_mov_b32 m0, s61
	s_nop 0
	global_load_lds_dwordx4 v[144:145], off
	v_lshl_add_u64 v[144:145], v[218:219], 0, s[68:69]
	s_mov_b32 m0, s62
	s_nop 0
	global_load_lds_dwordx4 v[144:145], off
	s_waitcnt vmcnt(8)
	s_waitcnt lgkmcnt(0)
	s_barrier
	s_setprio 1
	s_waitcnt lgkmcnt(0)
	v_mfma_f32_16x16x32_bf16 v[60:63], v[140:143], v[178:181], v[60:63]
	v_mfma_f32_16x16x32_bf16 v[56:59], v[154:157], v[178:181], v[56:59]
	v_mfma_f32_16x16x32_bf16 v[44:47], v[140:143], v[186:189], v[44:47]
	v_mfma_f32_16x16x32_bf16 v[40:43], v[154:157], v[186:189], v[40:43]
	v_mfma_f32_16x16x32_bf16 v[28:31], v[140:143], v[198:201], v[28:31]
	v_mfma_f32_16x16x32_bf16 v[24:27], v[154:157], v[198:201], v[24:27]
	v_mfma_f32_16x16x32_bf16 v[12:15], v[140:143], v[206:209], v[12:15]
	v_mfma_f32_16x16x32_bf16 v[8:11], v[154:157], v[206:209], v[8:11]
	v_mfma_f32_16x16x32_bf16 v[60:63], v[150:153], v[182:185], v[60:63]
	v_mfma_f32_16x16x32_bf16 v[56:59], v[158:161], v[182:185], v[56:59]
	v_mfma_f32_16x16x32_bf16 v[44:47], v[150:153], v[190:193], v[44:47]
	v_mfma_f32_16x16x32_bf16 v[40:43], v[158:161], v[190:193], v[40:43]
	v_mfma_f32_16x16x32_bf16 v[28:31], v[150:153], v[202:205], v[28:31]
	v_mfma_f32_16x16x32_bf16 v[24:27], v[158:161], v[202:205], v[24:27]
	v_mfma_f32_16x16x32_bf16 v[12:15], v[150:153], v[210:213], v[12:15]
	v_mfma_f32_16x16x32_bf16 v[8:11], v[158:161], v[210:213], v[8:11]
	s_setprio 0
	s_setprio 1
	v_mfma_f32_16x16x32_bf16 v[52:55], v[162:165], v[178:181], v[52:55]
	v_mfma_f32_16x16x32_bf16 v[48:51], v[170:173], v[178:181], v[48:51]
	v_mfma_f32_16x16x32_bf16 v[36:39], v[162:165], v[186:189], v[36:39]
	v_mfma_f32_16x16x32_bf16 v[32:35], v[170:173], v[186:189], v[32:35]
	v_mfma_f32_16x16x32_bf16 v[20:23], v[162:165], v[198:201], v[20:23]
	v_mfma_f32_16x16x32_bf16 v[16:19], v[170:173], v[198:201], v[16:19]
	v_mfma_f32_16x16x32_bf16 v[4:7], v[162:165], v[206:209], v[4:7]
	v_mfma_f32_16x16x32_bf16 v[0:3], v[170:173], v[206:209], v[0:3]
	v_mfma_f32_16x16x32_bf16 v[52:55], v[166:169], v[182:185], v[52:55]
	v_mfma_f32_16x16x32_bf16 v[48:51], v[174:177], v[182:185], v[48:51]
	v_mfma_f32_16x16x32_bf16 v[36:39], v[166:169], v[190:193], v[36:39]
	v_mfma_f32_16x16x32_bf16 v[32:35], v[174:177], v[190:193], v[32:35]
	v_mfma_f32_16x16x32_bf16 v[20:23], v[166:169], v[202:205], v[20:23]
	v_mfma_f32_16x16x32_bf16 v[16:19], v[174:177], v[202:205], v[16:19]
	v_mfma_f32_16x16x32_bf16 v[4:7], v[166:169], v[210:213], v[4:7]
	v_mfma_f32_16x16x32_bf16 v[0:3], v[174:177], v[210:213], v[0:3]
	s_setprio 0
	s_add_i32 s79, s79, 2
	s_add_u32 s18, s18, 0x100
	s_addc_u32 s19, s19, 0
	s_add_u32 s9, s9, 0x100
	s_addc_u32 s11, s11, 0
	s_cmp_gt_u32 s79, 13
	s_barrier
	s_cbranch_scc0 .LBB0_2120
	s_and_b64 vcc, exec, s[6:7]
	s_cbranch_vccz .LBB0_2123
	s_barrier

; #define PG8_STAGE(bufoff, gbase, voff) do { _Pragma("unroll") for (int _i = 0; _i < 2; ++_i) \
;         __builtin_amdgcn_global_load_lds((const unsigned*)((const char*)(gbase) + (voff)[_i]), (PG8_LAS unsigned*)(lds + (bufoff) + ldsw + _i * 8192), 16, 0, 0); } while (0)
; #define PG8_STAGE_A(bufoff, gbase, h, nx) do { _Pragma("unroll") for (int _i = 0; _i < 2; ++_i) { \
;         const unsigned vo_ = GA ? ((nx) ? vgn[h][_i] : vgc[h][_i]) : voffA[_i]; \
;         __builtin_amdgcn_global_load_lds((const unsigned*)((const char*)(gbase) + vo_), (PG8_LAS unsigned*)(lds + (bufoff) + ldsw + _i * 8192), 16, 0, 0); } } while (0)
; #define PG8_LDA(dst, b, h) do { _Pragma("unroll") for (int m = 0; m < 4; ++m) _Pragma("unroll") for (int k = 0; k < 2; ++k) dst[m][k] = *(const PG8_LAS bf16x8*)(lds + PG8_SA(b, h) + aoff + m * 2048 + k * 1024); } while (0)
; #define PG8_LDB(dst, b, h) do { _Pragma("unroll") for (int n = 0; n < 2; ++n) _Pragma("unroll") for (int k = 0; k < 2; ++k) dst[n][k] = *(const PG8_LAS bf16x8*)(lds + PG8_SB(b, h) + boff + n * 2048 + k * 1024); } while (0)
; #define PG8_WAIT_V(n) asm volatile("s_waitcnt vmcnt(" #n ")" ::: "memory")
; #define PG8_WAIT_L(n) asm volatile("s_waitcnt lgkmcnt(" #n ")" ::: "memory")
; #define PG8_BAR __builtin_amdgcn_s_barrier()
; #define PG8_SCHED __builtin_amdgcn_sched_barrier(0)
; template <class Epi, class Sched>
; __device__ __forceinline__ void gemm_phase(const int WID_, PG8_LAS unsigned char* lds, const Sched& S, const Epi& E) {
;     ...
;         for (int t = 0; t < nt; t += 2) {
;             const bool last = (t == nt - 2);
;             const char* a1 = cA + (size_t)(t + 1) * kstep;
;             const char* a2 = last ? nA : cA + (size_t)(t + 2) * kstep; const char* b2 = last ? nB : cB + (size_t)(t + 2) * kstep;
;             const char* a3 = a2 + kstep; const char* b3 = b2 + kstep;
;             PG8_LDB(B0, 0, 0); PG8_LDB(B1, 0, 1); PG8_SCHED; PG8_LDA(At, 0, 0); PG8_STAGE_A(PG8_SA(1, 1), a1 + hstepA, 1, false);
;             PG8_WAIT_V(8); PG8_WAIT_L(0); PG8_BAR; PG8_MMA(0, 0, At, B0); PG8_MMA(0, 1, At, B1); PG8_BAR; PG8_SCHED;
;             PG8_LDA(At, 0, 1); PG8_STAGE(PG8_SB(0, 0), b2, voffB); PG8_STAGE(PG8_SB(0, 1), b2 + hstepB, voffB); PG8_STAGE_A(PG8_SA(0, 0), a2, 0, last);
;             PG8_WAIT_V(8); PG8_WAIT_L(0); PG8_BAR; PG8_MMA(1, 0, At, B0); PG8_MMA(1, 1, At, B1); PG8_BAR; PG8_SCHED;
.Lg1_nofix:
	ds_read_b128 v[162:165], v151
	ds_read_b128 v[166:169], v151 offset:1024
	ds_read_b128 v[170:173], v151 offset:2048
	ds_read_b128 v[174:177], v151 offset:3072
	ds_read_b128 v[178:181], v152
	ds_read_b128 v[182:185], v152 offset:1024
	ds_read_b128 v[186:189], v152 offset:2048
	ds_read_b128 v[190:193], v152 offset:3072
	s_add_u32 s8, s2, s4
	s_addc_u32 s9, s3, s5
	s_cmpk_eq_i32 s4, 0x800
	s_cselect_b64 vcc, -1, 0
	s_and_b64 s[6:7], vcc, exec
	s_cselect_b32 s66, 0, s4
	s_cselect_b32 s45, 0, s5
	s_cselect_b32 s6, s42, s8
	s_cselect_b32 s7, s43, s9
	s_add_u32 s8, s92, s66
	s_addc_u32 s9, s93, s45
	v_lshl_add_u64 v[226:227], v[142:143], 0, s[4:5]
	s_mov_b32 m0, s51
	v_lshl_add_u64 v[226:227], v[226:227], 0, s[40:41]
	ds_read_b128 v[194:197], v153
	ds_read_b128 v[198:201], v153 offset:1024
	ds_read_b128 v[202:205], v153 offset:2048
	ds_read_b128 v[206:209], v153 offset:3072
	ds_read_b128 v[210:213], v153 offset:4096
	ds_read_b128 v[214:217], v153 offset:5120
	ds_read_b128 v[218:221], v153 offset:6144
	ds_read_b128 v[222:225], v153 offset:7168
	global_load_lds_dwordx4 v[226:227], off
	v_lshl_add_u64 v[226:227], v[144:145], 0, s[4:5]
	v_lshl_add_u64 v[226:227], v[226:227], 0, s[40:41]
	s_mov_b32 m0, s52
	s_nop 0
	global_load_lds_dwordx4 v[226:227], off
	s_waitcnt vmcnt(8)
	s_waitcnt lgkmcnt(0)
	s_barrier
	s_setprio 1
	s_waitcnt lgkmcnt(0)
	v_mfma_f32_16x16x32_bf16 v[124:127], v[162:165], v[194:197], v[124:127]
	v_mfma_f32_16x16x32_bf16 v[116:119], v[170:173], v[194:197], v[116:119]
	v_mfma_f32_16x16x32_bf16 v[108:111], v[162:165], v[202:205], v[108:111]
	v_mfma_f32_16x16x32_bf16 v[100:103], v[170:173], v[202:205], v[100:103]
	v_mfma_f32_16x16x32_bf16 v[92:95], v[162:165], v[210:213], v[92:95]
	v_mfma_f32_16x16x32_bf16 v[84:87], v[170:173], v[210:213], v[84:87]
	v_mfma_f32_16x16x32_bf16 v[76:79], v[162:165], v[218:221], v[76:79]
	v_mfma_f32_16x16x32_bf16 v[68:71], v[170:173], v[218:221], v[68:71]
	v_mfma_f32_16x16x32_bf16 v[124:127], v[166:169], v[198:201], v[124:127]
	v_mfma_f32_16x16x32_bf16 v[116:119], v[174:177], v[198:201], v[116:119]
	v_mfma_f32_16x16x32_bf16 v[108:111], v[166:169], v[206:209], v[108:111]
	v_mfma_f32_16x16x32_bf16 v[100:103], v[174:177], v[206:209], v[100:103]
	v_mfma_f32_16x16x32_bf16 v[92:95], v[166:169], v[214:217], v[92:95]
	v_mfma_f32_16x16x32_bf16 v[84:87], v[174:177], v[214:217], v[84:87]
	v_mfma_f32_16x16x32_bf16 v[76:79], v[166:169], v[222:225], v[76:79]
	v_mfma_f32_16x16x32_bf16 v[68:71], v[174:177], v[222:225], v[68:71]
	s_setprio 0
	s_setprio 1
	v_mfma_f32_16x16x32_bf16 v[120:123], v[178:181], v[194:197], v[120:123]
	v_mfma_f32_16x16x32_bf16 v[112:115], v[186:189], v[194:197], v[112:115]
	v_mfma_f32_16x16x32_bf16 v[104:107], v[178:181], v[202:205], v[104:107]
	v_mfma_f32_16x16x32_bf16 v[96:99], v[186:189], v[202:205], v[96:99]
	v_mfma_f32_16x16x32_bf16 v[88:91], v[178:181], v[210:213], v[88:91]
	v_mfma_f32_16x16x32_bf16 v[80:83], v[186:189], v[210:213], v[80:83]
	v_mfma_f32_16x16x32_bf16 v[72:75], v[178:181], v[218:221], v[72:75]
	v_mfma_f32_16x16x32_bf16 v[64:67], v[186:189], v[218:221], v[64:67]
	v_mfma_f32_16x16x32_bf16 v[120:123], v[182:185], v[198:201], v[120:123]
	v_mfma_f32_16x16x32_bf16 v[112:115], v[190:193], v[198:201], v[112:115]
	v_mfma_f32_16x16x32_bf16 v[104:107], v[182:185], v[206:209], v[104:107]
	v_mfma_f32_16x16x32_bf16 v[96:99], v[190:193], v[206:209], v[96:99]
	v_mfma_f32_16x16x32_bf16 v[88:91], v[182:185], v[214:217], v[88:91]
	v_mfma_f32_16x16x32_bf16 v[80:83], v[190:193], v[214:217], v[80:83]
	v_mfma_f32_16x16x32_bf16 v[72:75], v[182:185], v[222:225], v[72:75]
	v_mfma_f32_16x16x32_bf16 v[64:67], v[190:193], v[222:225], v[64:67]
	s_setprio 0
	s_barrier
	s_mov_b32 m0, s53
	v_lshl_add_u64 v[226:227], s[6:7], 0, v[128:129]
	s_add_u32 s66, s6, 0x40000
	ds_read_b128 v[194:197], v153 offset:16384
	ds_read_b128 v[198:201], v153 offset:17408
	ds_read_b128 v[202:205], v153 offset:18432
	ds_read_b128 v[206:209], v153 offset:19456
	ds_read_b128 v[210:213], v153 offset:20480
	ds_read_b128 v[214:217], v153 offset:21504
	ds_read_b128 v[218:221], v153 offset:22528
	ds_read_b128 v[222:225], v153 offset:23552
	global_load_lds_dwordx4 v[226:227], off
	v_lshl_add_u64 v[228:229], s[6:7], 0, v[130:131]
	s_mov_b32 m0, s54
	s_addc_u32 s67, s7, 0
	global_load_lds_dwordx4 v[228:229], off
	v_lshl_add_u64 v[230:231], s[66:67], 0, v[128:129]
	s_mov_b32 m0, s55
	v_cndmask_b32_e32 v132, v134, v157, vcc
	global_load_lds_dwordx4 v[230:231], off
	v_lshl_add_u64 v[230:231], s[66:67], 0, v[130:131]
	s_mov_b32 m0, s56
	s_nop 0
	global_load_lds_dwordx4 v[230:231], off
	s_mov_b32 m0, s21
	v_lshl_add_u64 v[230:231], s[8:9], 0, v[132:133]
	global_load_lds_dwordx4 v132, s[8:9]
	v_cndmask_b32_e32 v132, v136, v158, vcc
	s_mov_b32 m0, s33
	v_lshl_add_u64 v[232:233], s[8:9], 0, v[132:133]
	global_load_lds_dwordx4 v132, s[8:9]
	s_waitcnt vmcnt(8)
	s_waitcnt lgkmcnt(0)
	s_barrier
; #define PG8_STAGE_A(bufoff, gbase, h, nx) do { _Pragma("unroll") for (int _i = 0; _i < 2; ++_i) { \
;         const unsigned vo_ = GA ? ((nx) ? vgn[h][_i] : vgc[h][_i]) : voffA[_i]; \
;         __builtin_amdgcn_global_load_lds((const unsigned*)((const char*)(gbase) + vo_), (PG8_LAS unsigned*)(lds + (bufoff) + ldsw + _i * 8192), 16, 0, 0); } } while (0)
; #define PG8_LDA(dst, b, h) do { _Pragma("unroll") for (int m = 0; m < 4; ++m) _Pragma("unroll") for (int k = 0; k < 2; ++k) dst[m][k] = *(const PG8_LAS bf16x8*)(lds + PG8_SA(b, h) + aoff + m * 2048 + k * 1024); } while (0)
; #define PG8_LDB(dst, b, h) do { _Pragma("unroll") for (int n = 0; n < 2; ++n) _Pragma("unroll") for (int k = 0; k < 2; ++k) dst[n][k] = *(const PG8_LAS bf16x8*)(lds + PG8_SB(b, h) + boff + n * 2048 + k * 1024); } while (0)
; #define PG8_MMA(ai, bj, At, Bt) do { __builtin_amdgcn_s_setprio(1); _Pragma("unroll") for (int m = 0; m < 4; ++m) _Pragma("unroll") for (int n = 0; n < 2; ++n) _Pragma("unroll") for (int k = 0; k < 2; ++k) \
;         acc[ai][bj][m][n] = __builtin_amdgcn_mfma_f32_16x16x32_bf16(Bt[n][k], At[m][k], acc[ai][bj][m][n], 0, 0, 0); __builtin_amdgcn_s_setprio(0); } while (0)
; #define PG8_WAIT_V(n) asm volatile("s_waitcnt vmcnt(" #n ")" ::: "memory")
; #define PG8_WAIT_L(n) asm volatile("s_waitcnt lgkmcnt(" #n ")" ::: "memory")
; #define PG8_BAR __builtin_amdgcn_s_barrier()
; #define PG8_SCHED __builtin_amdgcn_sched_barrier(0)
; template <class Epi, class Sched>
; __device__ __forceinline__ void gemm_phase(const int WID_, PG8_LAS unsigned char* lds, const Sched& S, const Epi& E) {
;     ...
;             PG8_WAIT_V(8); PG8_WAIT_L(0); PG8_BAR; PG8_MMA(1, 0, At, B0); PG8_MMA(1, 1, At, B1); PG8_BAR; PG8_SCHED;
;             PG8_LDB(B0, 1, 0); PG8_LDB(B1, 1, 1); PG8_SCHED; PG8_LDA(At, 1, 0); PG8_STAGE_A(PG8_SA(0, 1), a2 + hstepA, 1, last);
;             PG8_WAIT_V(8); PG8_WAIT_L(0); PG8_BAR; PG8_MMA(0, 0, At, B0); PG8_MMA(0, 1, At, B1); PG8_BAR; PG8_SCHED;
	s_setprio 1
	s_waitcnt lgkmcnt(0)
	v_mfma_f32_16x16x32_bf16 v[60:63], v[162:165], v[194:197], v[60:63]
	v_mfma_f32_16x16x32_bf16 v[52:55], v[170:173], v[194:197], v[52:55]
	v_mfma_f32_16x16x32_bf16 v[44:47], v[162:165], v[202:205], v[44:47]
	v_mfma_f32_16x16x32_bf16 v[36:39], v[170:173], v[202:205], v[36:39]
	v_mfma_f32_16x16x32_bf16 v[28:31], v[162:165], v[210:213], v[28:31]
	v_mfma_f32_16x16x32_bf16 v[20:23], v[170:173], v[210:213], v[20:23]
	v_mfma_f32_16x16x32_bf16 v[12:15], v[162:165], v[218:221], v[12:15]
	v_mfma_f32_16x16x32_bf16 v[4:7], v[170:173], v[218:221], v[4:7]
	v_mfma_f32_16x16x32_bf16 v[60:63], v[166:169], v[198:201], v[60:63]
	v_mfma_f32_16x16x32_bf16 v[52:55], v[174:177], v[198:201], v[52:55]
	v_mfma_f32_16x16x32_bf16 v[44:47], v[166:169], v[206:209], v[44:47]
	v_mfma_f32_16x16x32_bf16 v[36:39], v[174:177], v[206:209], v[36:39]
	v_mfma_f32_16x16x32_bf16 v[28:31], v[166:169], v[214:217], v[28:31]
	v_mfma_f32_16x16x32_bf16 v[20:23], v[174:177], v[214:217], v[20:23]
	v_mfma_f32_16x16x32_bf16 v[12:15], v[166:169], v[222:225], v[12:15]
	v_mfma_f32_16x16x32_bf16 v[4:7], v[174:177], v[222:225], v[4:7]
	s_setprio 0
	s_setprio 1
	v_mfma_f32_16x16x32_bf16 v[56:59], v[178:181], v[194:197], v[56:59]
	v_mfma_f32_16x16x32_bf16 v[48:51], v[186:189], v[194:197], v[48:51]
	v_mfma_f32_16x16x32_bf16 v[40:43], v[178:181], v[202:205], v[40:43]
	v_mfma_f32_16x16x32_bf16 v[32:35], v[186:189], v[202:205], v[32:35]
	v_mfma_f32_16x16x32_bf16 v[24:27], v[178:181], v[210:213], v[24:27]
	v_mfma_f32_16x16x32_bf16 v[16:19], v[186:189], v[210:213], v[16:19]
	v_mfma_f32_16x16x32_bf16 v[8:11], v[178:181], v[218:221], v[8:11]
	v_mfma_f32_16x16x32_bf16 v[0:3], v[186:189], v[218:221], v[0:3]
	v_mfma_f32_16x16x32_bf16 v[56:59], v[182:185], v[198:201], v[56:59]
	v_mfma_f32_16x16x32_bf16 v[48:51], v[190:193], v[198:201], v[48:51]
	v_mfma_f32_16x16x32_bf16 v[40:43], v[182:185], v[206:209], v[40:43]
	v_mfma_f32_16x16x32_bf16 v[32:35], v[190:193], v[206:209], v[32:35]
	v_mfma_f32_16x16x32_bf16 v[24:27], v[182:185], v[214:217], v[24:27]
	v_mfma_f32_16x16x32_bf16 v[16:19], v[190:193], v[214:217], v[16:19]
	v_mfma_f32_16x16x32_bf16 v[8:11], v[182:185], v[222:225], v[8:11]
	v_mfma_f32_16x16x32_bf16 v[0:3], v[190:193], v[222:225], v[0:3]
	s_setprio 0
	s_barrier
	ds_read_b128 v[162:165], v154
	ds_read_b128 v[166:169], v154 offset:1024
	ds_read_b128 v[170:173], v154 offset:2048
	ds_read_b128 v[174:177], v154 offset:3072
	ds_read_b128 v[178:181], v155
	ds_read_b128 v[182:185], v155 offset:1024
	ds_read_b128 v[186:189], v155 offset:2048
	ds_read_b128 v[190:193], v155 offset:3072
	s_mov_b32 m0, s46
	v_cndmask_b32_e32 v132, v138, v159, vcc
	ds_read_b128 v[194:197], v153 offset:32768
	ds_read_b128 v[198:201], v153 offset:33792
	ds_read_b128 v[202:205], v153 offset:34816
	ds_read_b128 v[206:209], v153 offset:35840
	ds_read_b128 v[210:213], v153 offset:36864
	ds_read_b128 v[214:217], v153 offset:37888
	ds_read_b128 v[218:221], v153 offset:38912
	ds_read_b128 v[222:225], v153 offset:39936
	global_load_lds_dwordx4 v132, s[8:9]
	v_cndmask_b32_e32 v132, v140, v160, vcc
	s_mov_b32 m0, s47
	s_nop 0
	global_load_lds_dwordx4 v132, s[8:9]
	s_waitcnt vmcnt(8)
	s_waitcnt lgkmcnt(0)
	s_barrier
	s_setprio 1
	s_waitcnt lgkmcnt(0)
	v_mfma_f32_16x16x32_bf16 v[124:127], v[162:165], v[194:197], v[124:127]
	v_mfma_f32_16x16x32_bf16 v[116:119], v[170:173], v[194:197], v[116:119]
	v_mfma_f32_16x16x32_bf16 v[108:111], v[162:165], v[202:205], v[108:111]
	v_mfma_f32_16x16x32_bf16 v[100:103], v[170:173], v[202:205], v[100:103]
	v_mfma_f32_16x16x32_bf16 v[92:95], v[162:165], v[210:213], v[92:95]
	v_mfma_f32_16x16x32_bf16 v[84:87], v[170:173], v[210:213], v[84:87]
	v_mfma_f32_16x16x32_bf16 v[76:79], v[162:165], v[218:221], v[76:79]
	v_mfma_f32_16x16x32_bf16 v[68:71], v[170:173], v[218:221], v[68:71]
	v_mfma_f32_16x16x32_bf16 v[124:127], v[166:169], v[198:201], v[124:127]
	v_mfma_f32_16x16x32_bf16 v[116:119], v[174:177], v[198:201], v[116:119]
	v_mfma_f32_16x16x32_bf16 v[108:111], v[166:169], v[206:209], v[108:111]
	v_mfma_f32_16x16x32_bf16 v[100:103], v[174:177], v[206:209], v[100:103]
	v_mfma_f32_16x16x32_bf16 v[92:95], v[166:169], v[214:217], v[92:95]
	v_mfma_f32_16x16x32_bf16 v[84:87], v[174:177], v[214:217], v[84:87]
	v_mfma_f32_16x16x32_bf16 v[76:79], v[166:169], v[222:225], v[76:79]
	v_mfma_f32_16x16x32_bf16 v[68:71], v[174:177], v[222:225], v[68:71]
	s_setprio 0
	s_setprio 1
	v_mfma_f32_16x16x32_bf16 v[120:123], v[178:181], v[194:197], v[120:123]
	v_mfma_f32_16x16x32_bf16 v[112:115], v[186:189], v[194:197], v[112:115]
	v_mfma_f32_16x16x32_bf16 v[104:107], v[178:181], v[202:205], v[104:107]
	v_mfma_f32_16x16x32_bf16 v[96:99], v[186:189], v[202:205], v[96:99]
	v_mfma_f32_16x16x32_bf16 v[88:91], v[178:181], v[210:213], v[88:91]
	v_mfma_f32_16x16x32_bf16 v[80:83], v[186:189], v[210:213], v[80:83]
	v_mfma_f32_16x16x32_bf16 v[72:75], v[178:181], v[218:221], v[72:75]
	v_mfma_f32_16x16x32_bf16 v[64:67], v[186:189], v[218:221], v[64:67]
	v_mfma_f32_16x16x32_bf16 v[120:123], v[182:185], v[198:201], v[120:123]
	v_mfma_f32_16x16x32_bf16 v[112:115], v[190:193], v[198:201], v[112:115]
	v_mfma_f32_16x16x32_bf16 v[104:107], v[182:185], v[206:209], v[104:107]
	v_mfma_f32_16x16x32_bf16 v[96:99], v[190:193], v[206:209], v[96:99]
	v_mfma_f32_16x16x32_bf16 v[88:91], v[182:185], v[214:217], v[88:91]
	v_mfma_f32_16x16x32_bf16 v[80:83], v[190:193], v[214:217], v[80:83]
	v_mfma_f32_16x16x32_bf16 v[72:75], v[182:185], v[222:225], v[72:75]
	v_mfma_f32_16x16x32_bf16 v[64:67], v[190:193], v[222:225], v[64:67]
	s_setprio 0
	s_barrier
; #define PG8_STAGE(bufoff, gbase, voff) do { _Pragma("unroll") for (int _i = 0; _i < 2; ++_i) \
;         __builtin_amdgcn_global_load_lds((const unsigned*)((const char*)(gbase) + (voff)[_i]), (PG8_LAS unsigned*)(lds + (bufoff) + ldsw + _i * 8192), 16, 0, 0); } while (0)
; #define PG8_STAGE_A(bufoff, gbase, h, nx) do { _Pragma("unroll") for (int _i = 0; _i < 2; ++_i) { \
;         const unsigned vo_ = GA ? ((nx) ? vgn[h][_i] : vgc[h][_i]) : voffA[_i]; \
;         __builtin_amdgcn_global_load_lds((const unsigned*)((const char*)(gbase) + vo_), (PG8_LAS unsigned*)(lds + (bufoff) + ldsw + _i * 8192), 16, 0, 0); } } while (0)
; #define PG8_LDA(dst, b, h) do { _Pragma("unroll") for (int m = 0; m < 4; ++m) _Pragma("unroll") for (int k = 0; k < 2; ++k) dst[m][k] = *(const PG8_LAS bf16x8*)(lds + PG8_SA(b, h) + aoff + m * 2048 + k * 1024); } while (0)
; #define PG8_MMA(ai, bj, At, Bt) do { __builtin_amdgcn_s_setprio(1); _Pragma("unroll") for (int m = 0; m < 4; ++m) _Pragma("unroll") for (int n = 0; n < 2; ++n) _Pragma("unroll") for (int k = 0; k < 2; ++k) \
;         acc[ai][bj][m][n] = __builtin_amdgcn_mfma_f32_16x16x32_bf16(Bt[n][k], At[m][k], acc[ai][bj][m][n], 0, 0, 0); __builtin_amdgcn_s_setprio(0); } while (0)
; #define PG8_WAIT_V(n) asm volatile("s_waitcnt vmcnt(" #n ")" ::: "memory")
; #define PG8_WAIT_L(n) asm volatile("s_waitcnt lgkmcnt(" #n ")" ::: "memory")
; #define PG8_BAR __builtin_amdgcn_s_barrier()
; #define PG8_SCHED __builtin_amdgcn_sched_barrier(0)
; template <class Epi, class Sched>
; __device__ __forceinline__ void gemm_phase(const int WID_, PG8_LAS unsigned char* lds, const Sched& S, const Epi& E) {
;     ...
;             PG8_LDA(At, 1, 1); PG8_STAGE(PG8_SB(1, 0), b3, voffB); PG8_STAGE(PG8_SB(1, 1), b3 + hstepB, voffB); PG8_STAGE_A(PG8_SA(1, 0), a3, 0, last);
;             PG8_WAIT_V(8); PG8_WAIT_L(0); PG8_BAR; PG8_MMA(1, 0, At, B0); PG8_MMA(1, 1, At, B1); PG8_BAR; PG8_SCHED;
;         }
;         if (wr == 0) PG8_BAR;
	s_mov_b32 m0, s60
	v_lshl_add_u64 v[226:227], v[226:227], 0, s[36:37]
	s_add_u32 s6, s6, 0x40080
	ds_read_b128 v[194:197], v153 offset:49152
	ds_read_b128 v[198:201], v153 offset:50176
	ds_read_b128 v[202:205], v153 offset:51200
	ds_read_b128 v[206:209], v153 offset:52224
	ds_read_b128 v[210:213], v153 offset:53248
	ds_read_b128 v[214:217], v153 offset:54272
	ds_read_b128 v[218:221], v153 offset:55296
	ds_read_b128 v[222:225], v153 offset:56320
	global_load_lds_dwordx4 v[226:227], off
	v_lshl_add_u64 v[226:227], v[228:229], 0, s[36:37]
	s_mov_b32 m0, s61
	s_addc_u32 s7, s7, 0
	global_load_lds_dwordx4 v[226:227], off
	v_lshl_add_u64 v[226:227], s[6:7], 0, v[128:129]
	s_mov_b32 m0, s62
	s_nop 0
	global_load_lds_dwordx4 v[226:227], off
	v_lshl_add_u64 v[226:227], s[6:7], 0, v[130:131]
	s_mov_b32 m0, s63
	s_nop 0
	global_load_lds_dwordx4 v[226:227], off
	v_lshl_add_u64 v[226:227], v[230:231], 0, s[36:37]
	s_mov_b32 m0, s49
	s_nop 0
	global_load_lds_dwordx4 v[226:227], off
	v_lshl_add_u64 v[226:227], v[232:233], 0, s[36:37]
	s_mov_b32 m0, s50
	s_nop 0
	global_load_lds_dwordx4 v[226:227], off
	s_waitcnt vmcnt(8)
	s_waitcnt lgkmcnt(0)
	s_barrier
	s_setprio 1
	s_waitcnt lgkmcnt(0)
	v_mfma_f32_16x16x32_bf16 v[60:63], v[162:165], v[194:197], v[60:63]
	v_mfma_f32_16x16x32_bf16 v[52:55], v[170:173], v[194:197], v[52:55]
	v_mfma_f32_16x16x32_bf16 v[44:47], v[162:165], v[202:205], v[44:47]
	v_mfma_f32_16x16x32_bf16 v[36:39], v[170:173], v[202:205], v[36:39]
	v_mfma_f32_16x16x32_bf16 v[28:31], v[162:165], v[210:213], v[28:31]
	v_mfma_f32_16x16x32_bf16 v[20:23], v[170:173], v[210:213], v[20:23]
	v_mfma_f32_16x16x32_bf16 v[12:15], v[162:165], v[218:221], v[12:15]
	v_mfma_f32_16x16x32_bf16 v[4:7], v[170:173], v[218:221], v[4:7]
	v_mfma_f32_16x16x32_bf16 v[60:63], v[166:169], v[198:201], v[60:63]
	v_mfma_f32_16x16x32_bf16 v[52:55], v[174:177], v[198:201], v[52:55]
	v_mfma_f32_16x16x32_bf16 v[44:47], v[166:169], v[206:209], v[44:47]
	v_mfma_f32_16x16x32_bf16 v[36:39], v[174:177], v[206:209], v[36:39]
	v_mfma_f32_16x16x32_bf16 v[28:31], v[166:169], v[214:217], v[28:31]
	v_mfma_f32_16x16x32_bf16 v[20:23], v[174:177], v[214:217], v[20:23]
	v_mfma_f32_16x16x32_bf16 v[12:15], v[166:169], v[222:225], v[12:15]
	v_mfma_f32_16x16x32_bf16 v[4:7], v[174:177], v[222:225], v[4:7]
	s_setprio 0
	s_setprio 1
	v_mfma_f32_16x16x32_bf16 v[56:59], v[178:181], v[194:197], v[56:59]
	v_mfma_f32_16x16x32_bf16 v[48:51], v[186:189], v[194:197], v[48:51]
	v_mfma_f32_16x16x32_bf16 v[40:43], v[178:181], v[202:205], v[40:43]
	v_mfma_f32_16x16x32_bf16 v[32:35], v[186:189], v[202:205], v[32:35]
	v_mfma_f32_16x16x32_bf16 v[24:27], v[178:181], v[210:213], v[24:27]
	v_mfma_f32_16x16x32_bf16 v[16:19], v[186:189], v[210:213], v[16:19]
	v_mfma_f32_16x16x32_bf16 v[8:11], v[178:181], v[218:221], v[8:11]
	v_mfma_f32_16x16x32_bf16 v[0:3], v[186:189], v[218:221], v[0:3]
	v_mfma_f32_16x16x32_bf16 v[56:59], v[182:185], v[198:201], v[56:59]
	v_mfma_f32_16x16x32_bf16 v[48:51], v[190:193], v[198:201], v[48:51]
	v_mfma_f32_16x16x32_bf16 v[40:43], v[182:185], v[206:209], v[40:43]
	v_mfma_f32_16x16x32_bf16 v[32:35], v[190:193], v[206:209], v[32:35]
	v_mfma_f32_16x16x32_bf16 v[24:27], v[182:185], v[214:217], v[24:27]
	v_mfma_f32_16x16x32_bf16 v[16:19], v[190:193], v[214:217], v[16:19]
	v_mfma_f32_16x16x32_bf16 v[8:11], v[182:185], v[222:225], v[8:11]
	v_mfma_f32_16x16x32_bf16 v[0:3], v[190:193], v[222:225], v[0:3]
	s_setprio 0
	s_add_i32 s11, s11, 2
	s_add_u32 s4, s4, 0x100
	s_addc_u32 s5, s5, 0
	s_cmp_gt_u32 s11, 13
	s_barrier
	s_cbranch_scc0 .LBB0_2294
	s_and_b64 vcc, exec, s[38:39]
	s_cbranch_vccz .LBB0_2297
	s_barrier

; #define PG8_STAGE(bufoff, gbase, voff) do { _Pragma("unroll") for (int _i = 0; _i < 2; ++_i) \
;         __builtin_amdgcn_global_load_lds((const unsigned*)((const char*)(gbase) + (voff)[_i]), (PG8_LAS unsigned*)(lds + (bufoff) + ldsw + _i * 8192), 16, 0, 0); } while (0)
; #define PG8_STAGE_A(bufoff, gbase, h, nx) do { _Pragma("unroll") for (int _i = 0; _i < 2; ++_i) { \
;         const unsigned vo_ = GA ? ((nx) ? vgn[h][_i] : vgc[h][_i]) : voffA[_i]; \
;         __builtin_amdgcn_global_load_lds((const unsigned*)((const char*)(gbase) + vo_), (PG8_LAS unsigned*)(lds + (bufoff) + ldsw + _i * 8192), 16, 0, 0); } } while (0)
; #define PG8_LDA(dst, b, h) do { _Pragma("unroll") for (int m = 0; m < 4; ++m) _Pragma("unroll") for (int k = 0; k < 2; ++k) dst[m][k] = *(const PG8_LAS bf16x8*)(lds + PG8_SA(b, h) + aoff + m * 2048 + k * 1024); } while (0)
; #define PG8_LDB(dst, b, h) do { _Pragma("unroll") for (int n = 0; n < 2; ++n) _Pragma("unroll") for (int k = 0; k < 2; ++k) dst[n][k] = *(const PG8_LAS bf16x8*)(lds + PG8_SB(b, h) + boff + n * 2048 + k * 1024); } while (0)
; #define PG8_WAIT_V(n) asm volatile("s_waitcnt vmcnt(" #n ")" ::: "memory")
; #define PG8_WAIT_L(n) asm volatile("s_waitcnt lgkmcnt(" #n ")" ::: "memory")
; #define PG8_BAR __builtin_amdgcn_s_barrier()
; #define PG8_SCHED __builtin_amdgcn_sched_barrier(0)
; template <class Epi, class Sched>
; __device__ __forceinline__ void gemm_phase(const int WID_, PG8_LAS unsigned char* lds, const Sched& S, const Epi& E) {
;     ...
;         for (int t = 0; t < nt; t += 2) {
;             const bool last = (t == nt - 2);
;             const char* a1 = cA + (size_t)(t + 1) * kstep;
;             const char* a2 = last ? nA : cA + (size_t)(t + 2) * kstep; const char* b2 = last ? nB : cB + (size_t)(t + 2) * kstep;
;             const char* a3 = a2 + kstep; const char* b3 = b2 + kstep;
;             PG8_LDB(B0, 0, 0); PG8_LDB(B1, 0, 1); PG8_SCHED; PG8_LDA(At, 0, 0); PG8_STAGE_A(PG8_SA(1, 1), a1 + hstepA, 1, false);
;             PG8_WAIT_V(8); PG8_WAIT_L(0); PG8_BAR; PG8_MMA(0, 0, At, B0); PG8_MMA(0, 1, At, B1); PG8_BAR; PG8_SCHED;
;             PG8_LDA(At, 0, 1); PG8_STAGE(PG8_SB(0, 0), b2, voffB); PG8_STAGE(PG8_SB(0, 1), b2 + hstepB, voffB); PG8_STAGE_A(PG8_SA(0, 0), a2, 0, last);
;             PG8_WAIT_V(8); PG8_WAIT_L(0); PG8_BAR; PG8_MMA(1, 0, At, B0); PG8_MMA(1, 1, At, B1); PG8_BAR; PG8_SCHED;
.Lg2_nofix:
	ds_read_b128 v[142:145], v148
	ds_read_b128 v[152:155], v148 offset:1024
	ds_read_b128 v[156:159], v148 offset:2048
	ds_read_b128 v[160:163], v148 offset:3072
	ds_read_b128 v[164:167], v149
	ds_read_b128 v[168:171], v149 offset:1024
	ds_read_b128 v[172:175], v149 offset:2048
	ds_read_b128 v[176:179], v149 offset:3072
	s_add_u32 s40, s38, 0xfffe0080
	s_addc_u32 s41, s39, -1
	s_cmp_eq_u32 s62, 4
	s_cselect_b32 s43, s31, s41
	s_cselect_b32 s42, s59, s40
	s_cselect_b32 s41, s29, s61
	s_cselect_b32 s40, s28, s60
	s_mov_b32 m0, s55
	v_lshl_add_u64 v[212:213], s[38:39], 0, v[138:139]
	ds_read_b128 v[180:183], v150
	ds_read_b128 v[184:187], v150 offset:1024
	ds_read_b128 v[188:191], v150 offset:2048
	ds_read_b128 v[192:195], v150 offset:3072
	ds_read_b128 v[196:199], v150 offset:4096
	ds_read_b128 v[200:203], v150 offset:5120
	ds_read_b128 v[204:207], v150 offset:6144
	ds_read_b128 v[208:211], v150 offset:7168
	global_load_lds_dwordx4 v[212:213], off
	v_lshl_add_u64 v[212:213], s[38:39], 0, v[140:141]
	s_mov_b32 m0, s56
	s_nop 0
	global_load_lds_dwordx4 v[212:213], off
	s_waitcnt vmcnt(8)
	s_waitcnt lgkmcnt(0)
	s_barrier
	s_setprio 1
	s_waitcnt lgkmcnt(0)
	v_mfma_f32_16x16x32_bf16 v[124:127], v[142:145], v[180:183], v[124:127]
	v_mfma_f32_16x16x32_bf16 v[120:123], v[156:159], v[180:183], v[120:123]
	v_mfma_f32_16x16x32_bf16 v[108:111], v[142:145], v[188:191], v[108:111]
	v_mfma_f32_16x16x32_bf16 v[104:107], v[156:159], v[188:191], v[104:107]
	v_mfma_f32_16x16x32_bf16 v[92:95], v[142:145], v[196:199], v[92:95]
	v_mfma_f32_16x16x32_bf16 v[88:91], v[156:159], v[196:199], v[88:91]
	v_mfma_f32_16x16x32_bf16 v[76:79], v[142:145], v[204:207], v[76:79]
	v_mfma_f32_16x16x32_bf16 v[72:75], v[156:159], v[204:207], v[72:75]
	v_mfma_f32_16x16x32_bf16 v[124:127], v[152:155], v[184:187], v[124:127]
	v_mfma_f32_16x16x32_bf16 v[120:123], v[160:163], v[184:187], v[120:123]
	v_mfma_f32_16x16x32_bf16 v[108:111], v[152:155], v[192:195], v[108:111]
	v_mfma_f32_16x16x32_bf16 v[104:107], v[160:163], v[192:195], v[104:107]
	v_mfma_f32_16x16x32_bf16 v[92:95], v[152:155], v[200:203], v[92:95]
	v_mfma_f32_16x16x32_bf16 v[88:91], v[160:163], v[200:203], v[88:91]
	v_mfma_f32_16x16x32_bf16 v[76:79], v[152:155], v[208:211], v[76:79]
	v_mfma_f32_16x16x32_bf16 v[72:75], v[160:163], v[208:211], v[72:75]
	s_setprio 0
	s_setprio 1
	v_mfma_f32_16x16x32_bf16 v[116:119], v[164:167], v[180:183], v[116:119]
	v_mfma_f32_16x16x32_bf16 v[112:115], v[172:175], v[180:183], v[112:115]
	v_mfma_f32_16x16x32_bf16 v[100:103], v[164:167], v[188:191], v[100:103]
	v_mfma_f32_16x16x32_bf16 v[96:99], v[172:175], v[188:191], v[96:99]
	v_mfma_f32_16x16x32_bf16 v[84:87], v[164:167], v[196:199], v[84:87]
	v_mfma_f32_16x16x32_bf16 v[80:83], v[172:175], v[196:199], v[80:83]
	v_mfma_f32_16x16x32_bf16 v[68:71], v[164:167], v[204:207], v[68:71]
	v_mfma_f32_16x16x32_bf16 v[64:67], v[172:175], v[204:207], v[64:67]
	v_mfma_f32_16x16x32_bf16 v[116:119], v[168:171], v[184:187], v[116:119]
	v_mfma_f32_16x16x32_bf16 v[112:115], v[176:179], v[184:187], v[112:115]
	v_mfma_f32_16x16x32_bf16 v[100:103], v[168:171], v[192:195], v[100:103]
	v_mfma_f32_16x16x32_bf16 v[96:99], v[176:179], v[192:195], v[96:99]
	v_mfma_f32_16x16x32_bf16 v[84:87], v[168:171], v[200:203], v[84:87]
	v_mfma_f32_16x16x32_bf16 v[80:83], v[176:179], v[200:203], v[80:83]
	v_mfma_f32_16x16x32_bf16 v[68:71], v[168:171], v[208:211], v[68:71]
	v_mfma_f32_16x16x32_bf16 v[64:67], v[176:179], v[208:211], v[64:67]
	s_setprio 0
	s_barrier
	s_mov_b32 m0, s57
	v_lshl_add_u64 v[212:213], s[40:41], 0, v[130:131]
	ds_read_b128 v[180:183], v150 offset:16384
	ds_read_b128 v[184:187], v150 offset:17408
	ds_read_b128 v[188:191], v150 offset:18432
	ds_read_b128 v[192:195], v150 offset:19456
	ds_read_b128 v[196:199], v150 offset:20480
	ds_read_b128 v[200:203], v150 offset:21504
	ds_read_b128 v[204:207], v150 offset:22528
	ds_read_b128 v[208:211], v150 offset:23552
	global_load_lds_dwordx4 v[212:213], off
	s_add_i32 m0, s57, 0x2000
	s_add_u32 s64, s40, 0x20000
	v_lshl_add_u64 v[214:215], s[40:41], 0, v[134:135]
	s_addc_u32 s65, s41, 0
	s_add_i32 s63, s50, s33
	global_load_lds_dwordx4 v[214:215], off
	v_lshl_add_u64 v[216:217], s[64:65], 0, v[130:131]
	s_mov_b32 m0, s63
	v_lshl_add_u64 v[218:219], s[42:43], 0, v[136:137]
	global_load_lds_dwordx4 v[216:217], off
	v_lshl_add_u64 v[216:217], s[64:65], 0, v[134:135]
	s_add_i32 m0, s63, 0x2000
	s_nop 0
	global_load_lds_dwordx4 v[216:217], off
	v_lshl_add_u64 v[216:217], s[42:43], 0, v[132:133]
	s_mov_b32 m0, s44
	s_nop 0
	global_load_lds_dwordx4 v[216:217], off
	s_mov_b32 m0, s21
	s_nop 0
	global_load_lds_dwordx4 v[218:219], off
	s_waitcnt vmcnt(8)
	s_waitcnt lgkmcnt(0)
	s_barrier
; #define PG8_STAGE_A(bufoff, gbase, h, nx) do { _Pragma("unroll") for (int _i = 0; _i < 2; ++_i) { \
;         const unsigned vo_ = GA ? ((nx) ? vgn[h][_i] : vgc[h][_i]) : voffA[_i]; \
;         __builtin_amdgcn_global_load_lds((const unsigned*)((const char*)(gbase) + vo_), (PG8_LAS unsigned*)(lds + (bufoff) + ldsw + _i * 8192), 16, 0, 0); } } while (0)
; #define PG8_LDA(dst, b, h) do { _Pragma("unroll") for (int m = 0; m < 4; ++m) _Pragma("unroll") for (int k = 0; k < 2; ++k) dst[m][k] = *(const PG8_LAS bf16x8*)(lds + PG8_SA(b, h) + aoff + m * 2048 + k * 1024); } while (0)
; #define PG8_LDB(dst, b, h) do { _Pragma("unroll") for (int n = 0; n < 2; ++n) _Pragma("unroll") for (int k = 0; k < 2; ++k) dst[n][k] = *(const PG8_LAS bf16x8*)(lds + PG8_SB(b, h) + boff + n * 2048 + k * 1024); } while (0)
; #define PG8_MMA(ai, bj, At, Bt) do { __builtin_amdgcn_s_setprio(1); _Pragma("unroll") for (int m = 0; m < 4; ++m) _Pragma("unroll") for (int n = 0; n < 2; ++n) _Pragma("unroll") for (int k = 0; k < 2; ++k) \
;         acc[ai][bj][m][n] = __builtin_amdgcn_mfma_f32_16x16x32_bf16(Bt[n][k], At[m][k], acc[ai][bj][m][n], 0, 0, 0); __builtin_amdgcn_s_setprio(0); } while (0)
; #define PG8_WAIT_V(n) asm volatile("s_waitcnt vmcnt(" #n ")" ::: "memory")
; #define PG8_WAIT_L(n) asm volatile("s_waitcnt lgkmcnt(" #n ")" ::: "memory")
; #define PG8_BAR __builtin_amdgcn_s_barrier()
; #define PG8_SCHED __builtin_amdgcn_sched_barrier(0)
; template <class Epi, class Sched>
; __device__ __forceinline__ void gemm_phase(const int WID_, PG8_LAS unsigned char* lds, const Sched& S, const Epi& E) {
;     ...
;             PG8_WAIT_V(8); PG8_WAIT_L(0); PG8_BAR; PG8_MMA(1, 0, At, B0); PG8_MMA(1, 1, At, B1); PG8_BAR; PG8_SCHED;
;             PG8_LDB(B0, 1, 0); PG8_LDB(B1, 1, 1); PG8_SCHED; PG8_LDA(At, 1, 0); PG8_STAGE_A(PG8_SA(0, 1), a2 + hstepA, 1, last);
;             PG8_WAIT_V(8); PG8_WAIT_L(0); PG8_BAR; PG8_MMA(0, 0, At, B0); PG8_MMA(0, 1, At, B1); PG8_BAR; PG8_SCHED;
	s_setprio 1
	s_waitcnt lgkmcnt(0)
	v_mfma_f32_16x16x32_bf16 v[60:63], v[142:145], v[180:183], v[60:63]
	v_mfma_f32_16x16x32_bf16 v[56:59], v[156:159], v[180:183], v[56:59]
	v_mfma_f32_16x16x32_bf16 v[44:47], v[142:145], v[188:191], v[44:47]
	v_mfma_f32_16x16x32_bf16 v[40:43], v[156:159], v[188:191], v[40:43]
	v_mfma_f32_16x16x32_bf16 v[28:31], v[142:145], v[196:199], v[28:31]
	v_mfma_f32_16x16x32_bf16 v[24:27], v[156:159], v[196:199], v[24:27]
	v_mfma_f32_16x16x32_bf16 v[12:15], v[142:145], v[204:207], v[12:15]
	v_mfma_f32_16x16x32_bf16 v[8:11], v[156:159], v[204:207], v[8:11]
	v_mfma_f32_16x16x32_bf16 v[60:63], v[152:155], v[184:187], v[60:63]
	v_mfma_f32_16x16x32_bf16 v[56:59], v[160:163], v[184:187], v[56:59]
	v_mfma_f32_16x16x32_bf16 v[44:47], v[152:155], v[192:195], v[44:47]
	v_mfma_f32_16x16x32_bf16 v[40:43], v[160:163], v[192:195], v[40:43]
	v_mfma_f32_16x16x32_bf16 v[28:31], v[152:155], v[200:203], v[28:31]
	v_mfma_f32_16x16x32_bf16 v[24:27], v[160:163], v[200:203], v[24:27]
	v_mfma_f32_16x16x32_bf16 v[12:15], v[152:155], v[208:211], v[12:15]
	v_mfma_f32_16x16x32_bf16 v[8:11], v[160:163], v[208:211], v[8:11]
	s_setprio 0
	s_setprio 1
	v_mfma_f32_16x16x32_bf16 v[52:55], v[164:167], v[180:183], v[52:55]
	v_mfma_f32_16x16x32_bf16 v[48:51], v[172:175], v[180:183], v[48:51]
	v_mfma_f32_16x16x32_bf16 v[36:39], v[164:167], v[188:191], v[36:39]
	v_mfma_f32_16x16x32_bf16 v[32:35], v[172:175], v[188:191], v[32:35]
	v_mfma_f32_16x16x32_bf16 v[20:23], v[164:167], v[196:199], v[20:23]
	v_mfma_f32_16x16x32_bf16 v[16:19], v[172:175], v[196:199], v[16:19]
	v_mfma_f32_16x16x32_bf16 v[4:7], v[164:167], v[204:207], v[4:7]
	v_mfma_f32_16x16x32_bf16 v[0:3], v[172:175], v[204:207], v[0:3]
	v_mfma_f32_16x16x32_bf16 v[52:55], v[168:171], v[184:187], v[52:55]
	v_mfma_f32_16x16x32_bf16 v[48:51], v[176:179], v[184:187], v[48:51]
	v_mfma_f32_16x16x32_bf16 v[36:39], v[168:171], v[192:195], v[36:39]
	v_mfma_f32_16x16x32_bf16 v[32:35], v[176:179], v[192:195], v[32:35]
	v_mfma_f32_16x16x32_bf16 v[20:23], v[168:171], v[200:203], v[20:23]
	v_mfma_f32_16x16x32_bf16 v[16:19], v[176:179], v[200:203], v[16:19]
	v_mfma_f32_16x16x32_bf16 v[4:7], v[168:171], v[208:211], v[4:7]
	v_mfma_f32_16x16x32_bf16 v[0:3], v[176:179], v[208:211], v[0:3]
	s_setprio 0
	s_barrier
	s_add_i32 s63, 0, 0x18000
	v_add_u32_e32 v128, s63, v147
	s_add_i32 s64, 0, 0x1c000
	ds_read_b128 v[142:145], v128
	ds_read_b128 v[152:155], v128 offset:1024
	ds_read_b128 v[156:159], v128 offset:2048
	ds_read_b128 v[160:163], v128 offset:3072
	v_add_u32_e32 v128, s64, v147
	ds_read_b128 v[164:167], v128
	ds_read_b128 v[168:171], v128 offset:1024
	ds_read_b128 v[172:175], v128 offset:2048
	ds_read_b128 v[176:179], v128 offset:3072
	s_add_u32 s42, s42, 0x20000
	s_addc_u32 s43, s43, 0
	s_mov_b32 m0, s45
	v_lshl_add_u64 v[220:221], s[42:43], 0, v[132:133]
	ds_read_b128 v[180:183], v150 offset:32768
	ds_read_b128 v[184:187], v150 offset:33792
	ds_read_b128 v[188:191], v150 offset:34816
	ds_read_b128 v[192:195], v150 offset:35840
	ds_read_b128 v[196:199], v150 offset:36864
	ds_read_b128 v[200:203], v150 offset:37888
	ds_read_b128 v[204:207], v150 offset:38912
	ds_read_b128 v[208:211], v150 offset:39936
	global_load_lds_dwordx4 v[220:221], off
	v_lshl_add_u64 v[220:221], s[42:43], 0, v[136:137]
	s_mov_b32 m0, s46
	s_nop 0
	global_load_lds_dwordx4 v[220:221], off
	s_waitcnt vmcnt(8)
	s_waitcnt lgkmcnt(0)
	s_barrier
	s_setprio 1
	s_waitcnt lgkmcnt(0)
	v_mfma_f32_16x16x32_bf16 v[124:127], v[142:145], v[180:183], v[124:127]
	v_mfma_f32_16x16x32_bf16 v[120:123], v[156:159], v[180:183], v[120:123]
	v_mfma_f32_16x16x32_bf16 v[108:111], v[142:145], v[188:191], v[108:111]
	v_mfma_f32_16x16x32_bf16 v[104:107], v[156:159], v[188:191], v[104:107]
	v_mfma_f32_16x16x32_bf16 v[92:95], v[142:145], v[196:199], v[92:95]
	v_mfma_f32_16x16x32_bf16 v[88:91], v[156:159], v[196:199], v[88:91]
	v_mfma_f32_16x16x32_bf16 v[76:79], v[142:145], v[204:207], v[76:79]
	v_mfma_f32_16x16x32_bf16 v[72:75], v[156:159], v[204:207], v[72:75]
	v_mfma_f32_16x16x32_bf16 v[124:127], v[152:155], v[184:187], v[124:127]
	v_mfma_f32_16x16x32_bf16 v[120:123], v[160:163], v[184:187], v[120:123]
	v_mfma_f32_16x16x32_bf16 v[108:111], v[152:155], v[192:195], v[108:111]
	v_mfma_f32_16x16x32_bf16 v[104:107], v[160:163], v[192:195], v[104:107]
	v_mfma_f32_16x16x32_bf16 v[92:95], v[152:155], v[200:203], v[92:95]
	v_mfma_f32_16x16x32_bf16 v[88:91], v[160:163], v[200:203], v[88:91]
	v_mfma_f32_16x16x32_bf16 v[76:79], v[152:155], v[208:211], v[76:79]
	v_mfma_f32_16x16x32_bf16 v[72:75], v[160:163], v[208:211], v[72:75]
	s_setprio 0
	s_setprio 1
	v_mfma_f32_16x16x32_bf16 v[116:119], v[164:167], v[180:183], v[116:119]
	v_mfma_f32_16x16x32_bf16 v[112:115], v[172:175], v[180:183], v[112:115]
	v_mfma_f32_16x16x32_bf16 v[100:103], v[164:167], v[188:191], v[100:103]
	v_mfma_f32_16x16x32_bf16 v[96:99], v[172:175], v[188:191], v[96:99]
	v_mfma_f32_16x16x32_bf16 v[84:87], v[164:167], v[196:199], v[84:87]
	v_mfma_f32_16x16x32_bf16 v[80:83], v[172:175], v[196:199], v[80:83]
	v_mfma_f32_16x16x32_bf16 v[68:71], v[164:167], v[204:207], v[68:71]
	v_mfma_f32_16x16x32_bf16 v[64:67], v[172:175], v[204:207], v[64:67]
	v_mfma_f32_16x16x32_bf16 v[116:119], v[168:171], v[184:187], v[116:119]
	v_mfma_f32_16x16x32_bf16 v[112:115], v[176:179], v[184:187], v[112:115]
	v_mfma_f32_16x16x32_bf16 v[100:103], v[168:171], v[192:195], v[100:103]
	v_mfma_f32_16x16x32_bf16 v[96:99], v[176:179], v[192:195], v[96:99]
	v_mfma_f32_16x16x32_bf16 v[84:87], v[168:171], v[200:203], v[84:87]
	v_mfma_f32_16x16x32_bf16 v[80:83], v[176:179], v[200:203], v[80:83]
	v_mfma_f32_16x16x32_bf16 v[68:71], v[168:171], v[208:211], v[68:71]
	v_mfma_f32_16x16x32_bf16 v[64:67], v[176:179], v[208:211], v[64:67]
	s_setprio 0
	s_barrier
; #define PG8_STAGE(bufoff, gbase, voff) do { _Pragma("unroll") for (int _i = 0; _i < 2; ++_i) \
;         __builtin_amdgcn_global_load_lds((const unsigned*)((const char*)(gbase) + (voff)[_i]), (PG8_LAS unsigned*)(lds + (bufoff) + ldsw + _i * 8192), 16, 0, 0); } while (0)
; #define PG8_STAGE_A(bufoff, gbase, h, nx) do { _Pragma("unroll") for (int _i = 0; _i < 2; ++_i) { \
;         const unsigned vo_ = GA ? ((nx) ? vgn[h][_i] : vgc[h][_i]) : voffA[_i]; \
;         __builtin_amdgcn_global_load_lds((const unsigned*)((const char*)(gbase) + vo_), (PG8_LAS unsigned*)(lds + (bufoff) + ldsw + _i * 8192), 16, 0, 0); } } while (0)
; #define PG8_LDA(dst, b, h) do { _Pragma("unroll") for (int m = 0; m < 4; ++m) _Pragma("unroll") for (int k = 0; k < 2; ++k) dst[m][k] = *(const PG8_LAS bf16x8*)(lds + PG8_SA(b, h) + aoff + m * 2048 + k * 1024); } while (0)
; #define PG8_MMA(ai, bj, At, Bt) do { __builtin_amdgcn_s_setprio(1); _Pragma("unroll") for (int m = 0; m < 4; ++m) _Pragma("unroll") for (int n = 0; n < 2; ++n) _Pragma("unroll") for (int k = 0; k < 2; ++k) \
;         acc[ai][bj][m][n] = __builtin_amdgcn_mfma_f32_16x16x32_bf16(Bt[n][k], At[m][k], acc[ai][bj][m][n], 0, 0, 0); __builtin_amdgcn_s_setprio(0); } while (0)
; #define PG8_WAIT_V(n) asm volatile("s_waitcnt vmcnt(" #n ")" ::: "memory")
; #define PG8_WAIT_L(n) asm volatile("s_waitcnt lgkmcnt(" #n ")" ::: "memory")
; #define PG8_BAR __builtin_amdgcn_s_barrier()
; #define PG8_SCHED __builtin_amdgcn_sched_barrier(0)
; template <class Epi, class Sched>
; __device__ __forceinline__ void gemm_phase(const int WID_, PG8_LAS unsigned char* lds, const Sched& S, const Epi& E) {
;     ...
;             PG8_LDA(At, 1, 1); PG8_STAGE(PG8_SB(1, 0), b3, voffB); PG8_STAGE(PG8_SB(1, 1), b3 + hstepB, voffB); PG8_STAGE_A(PG8_SA(1, 0), a3, 0, last);
;             PG8_WAIT_V(8); PG8_WAIT_L(0); PG8_BAR; PG8_MMA(1, 0, At, B0); PG8_MMA(1, 1, At, B1); PG8_BAR; PG8_SCHED;
;         }
;         if (wr == 0) PG8_BAR;
	s_add_i32 s42, s63, s33
	v_lshl_add_u64 v[212:213], v[212:213], 0, s[6:7]
	s_mov_b32 m0, s42
	ds_read_b128 v[180:183], v150 offset:49152
	ds_read_b128 v[184:187], v150 offset:50176
	ds_read_b128 v[188:191], v150 offset:51200
	ds_read_b128 v[192:195], v150 offset:52224
	ds_read_b128 v[196:199], v150 offset:53248
	ds_read_b128 v[200:203], v150 offset:54272
	ds_read_b128 v[204:207], v150 offset:55296
	ds_read_b128 v[208:211], v150 offset:56320
	global_load_lds_dwordx4 v[212:213], off
	s_add_i32 m0, s42, 0x2000
	s_add_u32 s40, s40, 0x20080
	v_lshl_add_u64 v[212:213], v[214:215], 0, s[6:7]
	s_addc_u32 s41, s41, 0
	s_add_i32 s42, s64, s33
	global_load_lds_dwordx4 v[212:213], off
	v_lshl_add_u64 v[212:213], s[40:41], 0, v[130:131]
	s_mov_b32 m0, s42
	s_nop 0
	global_load_lds_dwordx4 v[212:213], off
	v_lshl_add_u64 v[212:213], s[40:41], 0, v[134:135]
	s_add_i32 m0, s42, 0x2000
	s_nop 0
	global_load_lds_dwordx4 v[212:213], off
	v_lshl_add_u64 v[212:213], v[216:217], 0, s[6:7]
	s_mov_b32 m0, s48
	s_nop 0
	global_load_lds_dwordx4 v[212:213], off
	v_lshl_add_u64 v[212:213], v[218:219], 0, s[6:7]
	s_mov_b32 m0, s49
	s_nop 0
	global_load_lds_dwordx4 v[212:213], off
	s_waitcnt vmcnt(8)
	s_waitcnt lgkmcnt(0)
	s_barrier
	s_setprio 1
	s_waitcnt lgkmcnt(0)
	v_mfma_f32_16x16x32_bf16 v[60:63], v[142:145], v[180:183], v[60:63]
	v_mfma_f32_16x16x32_bf16 v[56:59], v[156:159], v[180:183], v[56:59]
	v_mfma_f32_16x16x32_bf16 v[44:47], v[142:145], v[188:191], v[44:47]
	v_mfma_f32_16x16x32_bf16 v[40:43], v[156:159], v[188:191], v[40:43]
	v_mfma_f32_16x16x32_bf16 v[28:31], v[142:145], v[196:199], v[28:31]
	v_mfma_f32_16x16x32_bf16 v[24:27], v[156:159], v[196:199], v[24:27]
	v_mfma_f32_16x16x32_bf16 v[12:15], v[142:145], v[204:207], v[12:15]
	v_mfma_f32_16x16x32_bf16 v[8:11], v[156:159], v[204:207], v[8:11]
	v_mfma_f32_16x16x32_bf16 v[60:63], v[152:155], v[184:187], v[60:63]
	v_mfma_f32_16x16x32_bf16 v[56:59], v[160:163], v[184:187], v[56:59]
	v_mfma_f32_16x16x32_bf16 v[44:47], v[152:155], v[192:195], v[44:47]
	v_mfma_f32_16x16x32_bf16 v[40:43], v[160:163], v[192:195], v[40:43]
	v_mfma_f32_16x16x32_bf16 v[28:31], v[152:155], v[200:203], v[28:31]
	v_mfma_f32_16x16x32_bf16 v[24:27], v[160:163], v[200:203], v[24:27]
	v_mfma_f32_16x16x32_bf16 v[12:15], v[152:155], v[208:211], v[12:15]
	v_mfma_f32_16x16x32_bf16 v[8:11], v[160:163], v[208:211], v[8:11]
	s_setprio 0
	s_setprio 1
	v_mfma_f32_16x16x32_bf16 v[52:55], v[164:167], v[180:183], v[52:55]
	v_mfma_f32_16x16x32_bf16 v[48:51], v[172:175], v[180:183], v[48:51]
	v_mfma_f32_16x16x32_bf16 v[36:39], v[164:167], v[188:191], v[36:39]
	v_mfma_f32_16x16x32_bf16 v[32:35], v[172:175], v[188:191], v[32:35]
	v_mfma_f32_16x16x32_bf16 v[20:23], v[164:167], v[196:199], v[20:23]
	v_mfma_f32_16x16x32_bf16 v[16:19], v[172:175], v[196:199], v[16:19]
	v_mfma_f32_16x16x32_bf16 v[4:7], v[164:167], v[204:207], v[4:7]
	v_mfma_f32_16x16x32_bf16 v[0:3], v[172:175], v[204:207], v[0:3]
	v_mfma_f32_16x16x32_bf16 v[52:55], v[168:171], v[184:187], v[52:55]
	v_mfma_f32_16x16x32_bf16 v[48:51], v[176:179], v[184:187], v[48:51]
	v_mfma_f32_16x16x32_bf16 v[36:39], v[168:171], v[192:195], v[36:39]
	v_mfma_f32_16x16x32_bf16 v[32:35], v[176:179], v[192:195], v[32:35]
	v_mfma_f32_16x16x32_bf16 v[20:23], v[168:171], v[200:203], v[20:23]
	v_mfma_f32_16x16x32_bf16 v[16:19], v[176:179], v[200:203], v[16:19]
	v_mfma_f32_16x16x32_bf16 v[4:7], v[168:171], v[208:211], v[4:7]
	v_mfma_f32_16x16x32_bf16 v[0:3], v[176:179], v[208:211], v[0:3]
	s_setprio 0
	s_add_i32 s62, s62, 2
	s_add_u32 s38, s38, 0x100
	s_addc_u32 s39, s39, 0
	s_add_u32 s60, s60, 0x100
	s_addc_u32 s61, s61, 0
	s_cmp_gt_u32 s62, 5
	s_barrier
	s_cbranch_scc0 .LBB0_2362
	s_and_b64 vcc, exec, s[8:9]
	s_cbranch_vccz .LBB0_2365
	s_barrier
